# v71 + fewer loop instructions: saddr-form LDS-DMA addressing and non-scaled fp8 MFMA form (unit scales; same e4m3 operands, f32 accumulate)
# speedup vs baseline: 1.0141x; 1.0141x over previous
; #define PG8_STAGE(bufoff, gbase, voff) do { _Pragma("unroll") for (int _i = 0; _i < 2; ++_i) \
;         __builtin_amdgcn_global_load_lds((const unsigned*)((const char*)(gbase) + (voff)[_i]), (PG8_LAS unsigned*)(lds + (bufoff) + ldsw + _i * 8192), 16, 0, 0); } while (0)
; #define PG8_WAIT_V(n) asm volatile("s_waitcnt vmcnt(" #n ")" ::: "memory")
; #define PG8_WAIT_L(n) asm volatile("s_waitcnt lgkmcnt(" #n ")" ::: "memory")
; #define PG8_BAR __builtin_amdgcn_s_barrier()
; #define PG8_SCHED __builtin_amdgcn_sched_barrier(0)
; template <class Epi, class Sched, bool ALIGN_EPI = true, bool F8 = false>
; __device__ __forceinline__ void gemm_phase(PG8_LAS unsigned char* lds, const Sched& S, const Epi& E) {
;     ...
;             PG8_LDB(B0, 0, 0); PG8_LDB(B1, 0, 1); PG8_SCHED; PG8_LDA(At, 0, 0); PG8_STAGE(PG8_SA(1, 1), a1, voffA[1]);
;             PG8_WAIT_V(8); PG8_WAIT_L(0); PG8_BAR; PG8_MMA(0, 0, At, B0); PG8_MMA(0, 1, At, B1); PG8_BAR; PG8_SCHED;
;             PG8_LDA(At, 0, 1); PG8_STAGE(PG8_SB(0, 0), b2, voffB[0]); PG8_STAGE(PG8_SB(0, 1), b2, voffB[1]); PG8_STAGE(PG8_SA(0, 0), a2, vA2[0]);
;             PG8_WAIT_V(8); PG8_WAIT_L(0); PG8_BAR; PG8_MMA(1, 0, At, B0); PG8_MMA(1, 1, At, B1); PG8_BAR; PG8_SCHED;
;             PG8_LDB(B0, 1, 0); PG8_LDB(B1, 1, 1); PG8_SCHED; PG8_LDA(At, 1, 0); PG8_STAGE(PG8_SA(0, 1), a2, vA2[1]);
;             PG8_WAIT_V(8); PG8_WAIT_L(0); PG8_BAR; PG8_MMA(0, 0, At, B0); PG8_MMA(0, 1, At, B1); PG8_BAR; PG8_SCHED;
;             PG8_LDA(At, 1, 1); PG8_STAGE(PG8_SB(1, 0), b3, voffB[0]); PG8_STAGE(PG8_SB(1, 1), b3, voffB[1]); PG8_STAGE(PG8_SA(1, 0), a3, vA2[0]);
;             PG8_WAIT_V(8); PG8_WAIT_L(0); PG8_BAR; PG8_MMA(1, 0, At, B0); PG8_MMA(1, 1, At, B1); PG8_BAR; PG8_SCHED;
.Lpk0_372:
	ds_read_b128 v[18:21], v207
	ds_read_b128 v[22:25], v207 offset:1024
	ds_read_b128 v[26:29], v207 offset:2048
	ds_read_b128 v[30:33], v207 offset:3072
	ds_read_b128 v[2:5], v208
	ds_read_b128 v[6:9], v208 offset:1024
	ds_read_b128 v[10:13], v208 offset:2048
	ds_read_b128 v[14:17], v208 offset:3072
	s_add_u32 s28, s26, 0x8000
	s_addc_u32 s29, s27, 0
	s_cmp_eq_u32 s21, 12
	s_cselect_b32 s40, s22, s28
	s_cselect_b32 s41, s23, s29
	s_cselect_b32 s30, s24, s5
	s_cselect_b32 s31, s25, s19
	s_add_u32 s28, s40, 0x8000
	s_addc_u32 s29, s41, 0
	s_add_i32 m0, s46, 0xc000
	ds_read_b128 v[212:215], v209
	ds_read_b128 v[216:219], v209 offset:1024
	ds_read_b128 v[220:223], v209 offset:2048
	ds_read_b128 v[224:227], v209 offset:3072
	ds_read_b128 v[228:231], v209 offset:4096
	ds_read_b128 v[232:235], v209 offset:5120
	ds_read_b128 v[236:239], v209 offset:6144
	ds_read_b128 v[240:243], v209 offset:7168
	global_load_lds_dwordx4 v190, s[26:27]
	s_add_i32 m0, s46, 0xe000
	s_nop 0
	global_load_lds_dwordx4 v188, s[26:27]
	s_waitcnt vmcnt(8)
	s_waitcnt lgkmcnt(0)
	s_setprio 1
	v_mfma_f32_16x16x128_f8f6f4 v[158:161], v[18:25], v[212:219], 0
	v_mfma_f32_16x16x128_f8f6f4 v[154:157], v[26:33], v[212:219], 0
	v_mfma_f32_16x16x128_f8f6f4 v[142:145], v[18:25], v[220:227], 0
	v_mfma_f32_16x16x128_f8f6f4 v[138:141], v[26:33], v[220:227], 0
	v_mfma_f32_16x16x128_f8f6f4 v[126:129], v[18:25], v[228:235], 0
	v_mfma_f32_16x16x128_f8f6f4 v[122:125], v[26:33], v[228:235], 0
	v_mfma_f32_16x16x128_f8f6f4 v[110:113], v[18:25], v[236:243], 0
	v_mfma_f32_16x16x128_f8f6f4 v[106:109], v[26:33], v[236:243], 0
	s_nop 3
	s_setprio 0
	s_setprio 1
	v_mfma_f32_16x16x128_f8f6f4 v[150:153], v[2:9], v[212:219], 0
	v_mfma_f32_16x16x128_f8f6f4 v[146:149], v[10:17], v[212:219], 0
	v_mfma_f32_16x16x128_f8f6f4 v[134:137], v[2:9], v[220:227], 0
	v_mfma_f32_16x16x128_f8f6f4 v[130:133], v[10:17], v[220:227], 0
	v_mfma_f32_16x16x128_f8f6f4 v[118:121], v[2:9], v[228:235], 0
	v_mfma_f32_16x16x128_f8f6f4 v[114:117], v[10:17], v[228:235], 0
	v_mfma_f32_16x16x128_f8f6f4 v[102:105], v[2:9], v[236:243], 0
	v_mfma_f32_16x16x128_f8f6f4 v[98:101], v[10:17], v[236:243], 0
	s_setprio 0
	s_barrier
	s_add_i32 s67, s62, s45
	s_mov_b32 m0, s67
	ds_read_b128 v[212:215], v209 offset:16384
	ds_read_b128 v[216:219], v209 offset:17408
	ds_read_b128 v[220:223], v209 offset:18432
	ds_read_b128 v[224:227], v209 offset:19456
	ds_read_b128 v[228:231], v209 offset:20480
	ds_read_b128 v[232:235], v209 offset:21504
	ds_read_b128 v[236:239], v209 offset:22528
	ds_read_b128 v[240:243], v209 offset:23552
	global_load_lds_dwordx4 v164, s[30:31]
	s_add_i32 m0, s67, 0x2000
	s_add_i32 s67, s63, s45
	global_load_lds_dwordx4 v166, s[30:31]
	s_add_u32 s98, s30, s8
	s_addc_u32 s99, s31, s9
	s_mov_b32 m0, s67
	s_nop 0
	global_load_lds_dwordx4 v164, s[98:99]
	s_add_u32 s100, s30, s8
	s_addc_u32 s101, s31, s9
	s_add_i32 m0, s67, 0x2000
	s_nop 0
	global_load_lds_dwordx4 v166, s[100:101]
	s_mov_b32 m0, s46
	s_nop 0
	global_load_lds_dwordx4 v174, s[40:41]
	s_mov_b32 m0, s47
	s_nop 0
	global_load_lds_dwordx4 v176, s[40:41]
	s_waitcnt vmcnt(8)
	s_waitcnt lgkmcnt(0)
	s_setprio 1
	v_mfma_f32_16x16x128_f8f6f4 v[94:97], v[18:25], v[212:219], 0
	v_mfma_f32_16x16x128_f8f6f4 v[90:93], v[26:33], v[212:219], 0
	v_mfma_f32_16x16x128_f8f6f4 v[78:81], v[18:25], v[220:227], 0
	v_mfma_f32_16x16x128_f8f6f4 v[74:77], v[26:33], v[220:227], 0
	v_mfma_f32_16x16x128_f8f6f4 v[62:65], v[18:25], v[228:235], 0
	v_mfma_f32_16x16x128_f8f6f4 v[58:61], v[26:33], v[228:235], 0
	v_mfma_f32_16x16x128_f8f6f4 v[46:49], v[18:25], v[236:243], 0
	v_mfma_f32_16x16x128_f8f6f4 v[42:45], v[26:33], v[236:243], 0
	s_nop 3
	s_setprio 0
	s_setprio 1
	v_mfma_f32_16x16x128_f8f6f4 v[86:89], v[2:9], v[212:219], 0
	v_mfma_f32_16x16x128_f8f6f4 v[82:85], v[10:17], v[212:219], 0
	v_mfma_f32_16x16x128_f8f6f4 v[70:73], v[2:9], v[220:227], 0
	v_mfma_f32_16x16x128_f8f6f4 v[66:69], v[10:17], v[220:227], 0
	v_mfma_f32_16x16x128_f8f6f4 v[54:57], v[2:9], v[228:235], 0
	v_mfma_f32_16x16x128_f8f6f4 v[50:53], v[10:17], v[228:235], 0
	v_mfma_f32_16x16x128_f8f6f4 v[38:41], v[2:9], v[236:243], 0
	v_mfma_f32_16x16x128_f8f6f4 v[34:37], v[10:17], v[236:243], 0
	s_setprio 0
	s_barrier
	s_add_i32 s67, 0, 0x18000
	s_add_i32 s68, 0, 0x1c000
	v_add_u32_e32 v14, s67, v202
	v_add_u32_e32 v30, s68, v202
	ds_read_b128 v[2:5], v14
	ds_read_b128 v[6:9], v14 offset:1024
	ds_read_b128 v[10:13], v14 offset:2048
	ds_read_b128 v[14:17], v14 offset:3072
	ds_read_b128 v[18:21], v30
	ds_read_b128 v[22:25], v30 offset:1024
	ds_read_b128 v[26:29], v30 offset:2048
	ds_read_b128 v[30:33], v30 offset:3072
	s_mov_b32 m0, s48
	ds_read_b128 v[212:215], v209 offset:32768
	ds_read_b128 v[216:219], v209 offset:33792
	ds_read_b128 v[220:223], v209 offset:34816
	ds_read_b128 v[224:227], v209 offset:35840
	ds_read_b128 v[228:231], v209 offset:36864
	ds_read_b128 v[232:235], v209 offset:37888
	ds_read_b128 v[236:239], v209 offset:38912
	ds_read_b128 v[240:243], v209 offset:39936
	global_load_lds_dwordx4 v178, s[40:41]
	s_mov_b32 m0, s49
	s_nop 0
	global_load_lds_dwordx4 v180, s[40:41]
	s_waitcnt vmcnt(8)
	s_waitcnt lgkmcnt(0)
	s_setprio 1
	v_mfma_f32_16x16x128_f8f6f4 v[158:161], v[2:9], v[212:219], v[158:161]
	v_mfma_f32_16x16x128_f8f6f4 v[154:157], v[10:17], v[212:219], v[154:157]
	v_mfma_f32_16x16x128_f8f6f4 v[142:145], v[2:9], v[220:227], v[142:145]
	v_mfma_f32_16x16x128_f8f6f4 v[138:141], v[10:17], v[220:227], v[138:141]
	v_mfma_f32_16x16x128_f8f6f4 v[126:129], v[2:9], v[228:235], v[126:129]
	v_mfma_f32_16x16x128_f8f6f4 v[122:125], v[10:17], v[228:235], v[122:125]
	v_mfma_f32_16x16x128_f8f6f4 v[110:113], v[2:9], v[236:243], v[110:113]
	v_mfma_f32_16x16x128_f8f6f4 v[106:109], v[10:17], v[236:243], v[106:109]
	s_nop 3
	s_setprio 0
	s_setprio 1
	v_mfma_f32_16x16x128_f8f6f4 v[150:153], v[18:25], v[212:219], v[150:153]
	v_mfma_f32_16x16x128_f8f6f4 v[146:149], v[26:33], v[212:219], v[146:149]
	v_mfma_f32_16x16x128_f8f6f4 v[134:137], v[18:25], v[220:227], v[134:137]
	v_mfma_f32_16x16x128_f8f6f4 v[130:133], v[26:33], v[220:227], v[130:133]
	v_mfma_f32_16x16x128_f8f6f4 v[118:121], v[18:25], v[228:235], v[118:121]
	v_mfma_f32_16x16x128_f8f6f4 v[114:117], v[26:33], v[228:235], v[114:117]
	v_mfma_f32_16x16x128_f8f6f4 v[102:105], v[18:25], v[236:243], v[102:105]
	v_mfma_f32_16x16x128_f8f6f4 v[98:101], v[26:33], v[236:243], v[98:101]
	s_setprio 0
	s_barrier
; #define PG8_STAGE(bufoff, gbase, voff) do { _Pragma("unroll") for (int _i = 0; _i < 2; ++_i) \
;         __builtin_amdgcn_global_load_lds((const unsigned*)((const char*)(gbase) + (voff)[_i]), (PG8_LAS unsigned*)(lds + (bufoff) + ldsw + _i * 8192), 16, 0, 0); } while (0)
; #define PG8_WAIT_V(n) asm volatile("s_waitcnt vmcnt(" #n ")" ::: "memory")
; #define PG8_WAIT_L(n) asm volatile("s_waitcnt lgkmcnt(" #n ")" ::: "memory")
; #define PG8_BAR __builtin_amdgcn_s_barrier()
; #define PG8_SCHED __builtin_amdgcn_sched_barrier(0)
; template <class Epi, class Sched, bool ALIGN_EPI = true, bool F8 = false>
; __device__ __forceinline__ void gemm_phase(PG8_LAS unsigned char* lds, const Sched& S, const Epi& E) {
;     ...
;             PG8_LDB(B0, 0, 0); PG8_LDB(B1, 0, 1); PG8_SCHED; PG8_LDA(At, 0, 0); PG8_STAGE(PG8_SA(1, 1), a1, voffA[1]);
;             PG8_WAIT_V(8); PG8_WAIT_L(0); PG8_BAR; PG8_MMA(0, 0, At, B0); PG8_MMA(0, 1, At, B1); PG8_BAR; PG8_SCHED;
;     ...
;             PG8_LDA(At, 1, 1); PG8_STAGE(PG8_SB(1, 0), b3, voffB[0]); PG8_STAGE(PG8_SB(1, 1), b3, voffB[1]); PG8_STAGE(PG8_SA(1, 0), a3, vA2[0]);
;             PG8_WAIT_V(8); PG8_WAIT_L(0); PG8_BAR; PG8_MMA(1, 0, At, B0); PG8_MMA(1, 1, At, B1); PG8_BAR; PG8_SCHED;
;         }
	s_add_u32 s30, s30, 0x8000
	s_addc_u32 s31, s31, 0
	s_add_i32 s40, s67, s45
	s_mov_b32 m0, s40
	ds_read_b128 v[212:215], v209 offset:49152
	ds_read_b128 v[216:219], v209 offset:50176
	ds_read_b128 v[220:223], v209 offset:51200
	ds_read_b128 v[224:227], v209 offset:52224
	ds_read_b128 v[228:231], v209 offset:53248
	ds_read_b128 v[232:235], v209 offset:54272
	ds_read_b128 v[236:239], v209 offset:55296
	ds_read_b128 v[240:243], v209 offset:56320
	global_load_lds_dwordx4 v164, s[30:31]
	s_add_i32 m0, s40, 0x2000
	s_add_i32 s40, s68, s45
	global_load_lds_dwordx4 v166, s[30:31]
	s_mov_b32 m0, s40
	s_nop 0
	global_load_lds_dwordx4 v168, s[30:31]
	s_add_i32 m0, s40, 0x2000
	s_nop 0
	global_load_lds_dwordx4 v172, s[30:31]
	s_mov_b32 m0, s52
	s_nop 0
	global_load_lds_dwordx4 v174, s[28:29]
	s_mov_b32 m0, s53
	s_nop 0
	global_load_lds_dwordx4 v176, s[28:29]
	s_waitcnt vmcnt(8)
	s_waitcnt lgkmcnt(0)
	s_setprio 1
	v_mfma_f32_16x16x128_f8f6f4 v[94:97], v[2:9], v[212:219], v[94:97]
	v_mfma_f32_16x16x128_f8f6f4 v[90:93], v[10:17], v[212:219], v[90:93]
	v_mfma_f32_16x16x128_f8f6f4 v[78:81], v[2:9], v[220:227], v[78:81]
	v_mfma_f32_16x16x128_f8f6f4 v[74:77], v[10:17], v[220:227], v[74:77]
	v_mfma_f32_16x16x128_f8f6f4 v[62:65], v[2:9], v[228:235], v[62:65]
	v_mfma_f32_16x16x128_f8f6f4 v[58:61], v[10:17], v[228:235], v[58:61]
	v_mfma_f32_16x16x128_f8f6f4 v[46:49], v[2:9], v[236:243], v[46:49]
	v_mfma_f32_16x16x128_f8f6f4 v[42:45], v[10:17], v[236:243], v[42:45]
	s_nop 3
	s_setprio 0
	s_setprio 1
	v_mfma_f32_16x16x128_f8f6f4 v[86:89], v[18:25], v[212:219], v[86:89]
	v_mfma_f32_16x16x128_f8f6f4 v[82:85], v[26:33], v[212:219], v[82:85]
	v_mfma_f32_16x16x128_f8f6f4 v[70:73], v[18:25], v[220:227], v[70:73]
	v_mfma_f32_16x16x128_f8f6f4 v[66:69], v[26:33], v[220:227], v[66:69]
	v_mfma_f32_16x16x128_f8f6f4 v[54:57], v[18:25], v[228:235], v[54:57]
	v_mfma_f32_16x16x128_f8f6f4 v[50:53], v[26:33], v[228:235], v[50:53]
	v_mfma_f32_16x16x128_f8f6f4 v[38:41], v[18:25], v[236:243], v[38:41]
	v_mfma_f32_16x16x128_f8f6f4 v[34:37], v[26:33], v[236:243], v[34:37]
	s_setprio 0
	s_barrier
	s_add_i32 s21, s21, 2
	s_add_u32 s5, s5, 0x10000
	s_addc_u32 s19, s19, 0
	s_add_u32 s26, s26, 0x10000
	s_addc_u32 s27, s27, 0
	s_cmp_gt_u32 s21, 13
	s_cbranch_scc0 .LBB0_372
	s_branch .Lfx_9967
.LBB0_372:
	ds_read_b128 v[18:21], v207
	ds_read_b128 v[22:25], v207 offset:1024
	ds_read_b128 v[26:29], v207 offset:2048
	ds_read_b128 v[30:33], v207 offset:3072
	ds_read_b128 v[2:5], v208
	ds_read_b128 v[6:9], v208 offset:1024
	ds_read_b128 v[10:13], v208 offset:2048
	ds_read_b128 v[14:17], v208 offset:3072
	s_add_u32 s28, s26, 0x8000
	s_addc_u32 s29, s27, 0
	s_cmp_eq_u32 s21, 12
	s_cselect_b32 s40, s22, s28
	s_cselect_b32 s41, s23, s29
	s_cselect_b32 s30, s24, s5
	s_cselect_b32 s31, s25, s19
	s_add_u32 s28, s40, 0x8000
	s_addc_u32 s29, s41, 0
	s_add_i32 m0, s46, 0xc000
	ds_read_b128 v[212:215], v209
	ds_read_b128 v[216:219], v209 offset:1024
	ds_read_b128 v[220:223], v209 offset:2048
	ds_read_b128 v[224:227], v209 offset:3072
	ds_read_b128 v[228:231], v209 offset:4096
	ds_read_b128 v[232:235], v209 offset:5120
	ds_read_b128 v[236:239], v209 offset:6144
	ds_read_b128 v[240:243], v209 offset:7168
	global_load_lds_dwordx4 v190, s[26:27]
	s_add_i32 m0, s46, 0xe000
	s_nop 0
	global_load_lds_dwordx4 v188, s[26:27]
	s_waitcnt vmcnt(8)
	s_waitcnt lgkmcnt(0)
	s_setprio 1
	v_mfma_f32_16x16x128_f8f6f4 v[158:161], v[18:25], v[212:219], v[158:161]
	v_mfma_f32_16x16x128_f8f6f4 v[154:157], v[26:33], v[212:219], v[154:157]
	v_mfma_f32_16x16x128_f8f6f4 v[142:145], v[18:25], v[220:227], v[142:145]
	v_mfma_f32_16x16x128_f8f6f4 v[138:141], v[26:33], v[220:227], v[138:141]
	v_mfma_f32_16x16x128_f8f6f4 v[126:129], v[18:25], v[228:235], v[126:129]
	v_mfma_f32_16x16x128_f8f6f4 v[122:125], v[26:33], v[228:235], v[122:125]
	v_mfma_f32_16x16x128_f8f6f4 v[110:113], v[18:25], v[236:243], v[110:113]
	v_mfma_f32_16x16x128_f8f6f4 v[106:109], v[26:33], v[236:243], v[106:109]
	s_nop 3
	s_setprio 0
	s_setprio 1
	v_mfma_f32_16x16x128_f8f6f4 v[150:153], v[2:9], v[212:219], v[150:153]
	v_mfma_f32_16x16x128_f8f6f4 v[146:149], v[10:17], v[212:219], v[146:149]
	v_mfma_f32_16x16x128_f8f6f4 v[134:137], v[2:9], v[220:227], v[134:137]
	v_mfma_f32_16x16x128_f8f6f4 v[130:133], v[10:17], v[220:227], v[130:133]
	v_mfma_f32_16x16x128_f8f6f4 v[118:121], v[2:9], v[228:235], v[118:121]
	v_mfma_f32_16x16x128_f8f6f4 v[114:117], v[10:17], v[228:235], v[114:117]
	v_mfma_f32_16x16x128_f8f6f4 v[102:105], v[2:9], v[236:243], v[102:105]
	v_mfma_f32_16x16x128_f8f6f4 v[98:101], v[10:17], v[236:243], v[98:101]
	s_setprio 0
	s_barrier
; #define PG8_STAGE(bufoff, gbase, voff) do { _Pragma("unroll") for (int _i = 0; _i < 2; ++_i) \
;         __builtin_amdgcn_global_load_lds((const unsigned*)((const char*)(gbase) + (voff)[_i]), (PG8_LAS unsigned*)(lds + (bufoff) + ldsw + _i * 8192), 16, 0, 0); } while (0)
; #define PG8_WAIT_V(n) asm volatile("s_waitcnt vmcnt(" #n ")" ::: "memory")
; #define PG8_WAIT_L(n) asm volatile("s_waitcnt lgkmcnt(" #n ")" ::: "memory")
; #define PG8_BAR __builtin_amdgcn_s_barrier()
; #define PG8_SCHED __builtin_amdgcn_sched_barrier(0)
; template <class Epi, class Sched, bool ALIGN_EPI = true, bool F8 = false>
; __device__ __forceinline__ void gemm_phase(PG8_LAS unsigned char* lds, const Sched& S, const Epi& E) {
;     ...
;             PG8_LDA(At, 0, 1); PG8_STAGE(PG8_SB(0, 0), b2, voffB[0]); PG8_STAGE(PG8_SB(0, 1), b2, voffB[1]); PG8_STAGE(PG8_SA(0, 0), a2, vA2[0]);
;             PG8_WAIT_V(8); PG8_WAIT_L(0); PG8_BAR; PG8_MMA(1, 0, At, B0); PG8_MMA(1, 1, At, B1); PG8_BAR; PG8_SCHED;
;             PG8_LDB(B0, 1, 0); PG8_LDB(B1, 1, 1); PG8_SCHED; PG8_LDA(At, 1, 0); PG8_STAGE(PG8_SA(0, 1), a2, vA2[1]);
;             PG8_WAIT_V(8); PG8_WAIT_L(0); PG8_BAR; PG8_MMA(0, 0, At, B0); PG8_MMA(0, 1, At, B1); PG8_BAR; PG8_SCHED;
;             PG8_LDA(At, 1, 1); PG8_STAGE(PG8_SB(1, 0), b3, voffB[0]); PG8_STAGE(PG8_SB(1, 1), b3, voffB[1]); PG8_STAGE(PG8_SA(1, 0), a3, vA2[0]);
;             PG8_WAIT_V(8); PG8_WAIT_L(0); PG8_BAR; PG8_MMA(1, 0, At, B0); PG8_MMA(1, 1, At, B1); PG8_BAR; PG8_SCHED;
;         }
	s_add_i32 s67, s62, s45
	s_mov_b32 m0, s67
	ds_read_b128 v[212:215], v209 offset:16384
	ds_read_b128 v[216:219], v209 offset:17408
	ds_read_b128 v[220:223], v209 offset:18432
	ds_read_b128 v[224:227], v209 offset:19456
	ds_read_b128 v[228:231], v209 offset:20480
	ds_read_b128 v[232:235], v209 offset:21504
	ds_read_b128 v[236:239], v209 offset:22528
	ds_read_b128 v[240:243], v209 offset:23552
	global_load_lds_dwordx4 v164, s[30:31]
	s_add_i32 m0, s67, 0x2000
	s_add_i32 s67, s63, s45
	global_load_lds_dwordx4 v166, s[30:31]
	s_add_u32 s98, s30, s8
	s_addc_u32 s99, s31, s9
	s_mov_b32 m0, s67
	s_nop 0
	global_load_lds_dwordx4 v164, s[98:99]
	s_add_u32 s100, s30, s8
	s_addc_u32 s101, s31, s9
	s_add_i32 m0, s67, 0x2000
	s_nop 0
	global_load_lds_dwordx4 v166, s[100:101]
	s_mov_b32 m0, s46
	s_nop 0
	global_load_lds_dwordx4 v174, s[40:41]
	s_mov_b32 m0, s47
	s_nop 0
	global_load_lds_dwordx4 v176, s[40:41]
	s_waitcnt vmcnt(8)
	s_waitcnt lgkmcnt(0)
	s_setprio 1
	v_mfma_f32_16x16x128_f8f6f4 v[94:97], v[18:25], v[212:219], v[94:97]
	v_mfma_f32_16x16x128_f8f6f4 v[90:93], v[26:33], v[212:219], v[90:93]
	v_mfma_f32_16x16x128_f8f6f4 v[78:81], v[18:25], v[220:227], v[78:81]
	v_mfma_f32_16x16x128_f8f6f4 v[74:77], v[26:33], v[220:227], v[74:77]
	v_mfma_f32_16x16x128_f8f6f4 v[62:65], v[18:25], v[228:235], v[62:65]
	v_mfma_f32_16x16x128_f8f6f4 v[58:61], v[26:33], v[228:235], v[58:61]
	v_mfma_f32_16x16x128_f8f6f4 v[46:49], v[18:25], v[236:243], v[46:49]
	v_mfma_f32_16x16x128_f8f6f4 v[42:45], v[26:33], v[236:243], v[42:45]
	s_nop 3
	s_setprio 0
	s_setprio 1
	v_mfma_f32_16x16x128_f8f6f4 v[86:89], v[2:9], v[212:219], v[86:89]
	v_mfma_f32_16x16x128_f8f6f4 v[82:85], v[10:17], v[212:219], v[82:85]
	v_mfma_f32_16x16x128_f8f6f4 v[70:73], v[2:9], v[220:227], v[70:73]
	v_mfma_f32_16x16x128_f8f6f4 v[66:69], v[10:17], v[220:227], v[66:69]
	v_mfma_f32_16x16x128_f8f6f4 v[54:57], v[2:9], v[228:235], v[54:57]
	v_mfma_f32_16x16x128_f8f6f4 v[50:53], v[10:17], v[228:235], v[50:53]
	v_mfma_f32_16x16x128_f8f6f4 v[38:41], v[2:9], v[236:243], v[38:41]
	v_mfma_f32_16x16x128_f8f6f4 v[34:37], v[10:17], v[236:243], v[34:37]
	s_setprio 0
	s_barrier
	s_add_i32 s67, 0, 0x18000
	s_add_i32 s68, 0, 0x1c000
	v_add_u32_e32 v14, s67, v202
	v_add_u32_e32 v30, s68, v202
	ds_read_b128 v[2:5], v14
	ds_read_b128 v[6:9], v14 offset:1024
	ds_read_b128 v[10:13], v14 offset:2048
	ds_read_b128 v[14:17], v14 offset:3072
	ds_read_b128 v[18:21], v30
	ds_read_b128 v[22:25], v30 offset:1024
	ds_read_b128 v[26:29], v30 offset:2048
	ds_read_b128 v[30:33], v30 offset:3072
	s_mov_b32 m0, s48
	ds_read_b128 v[212:215], v209 offset:32768
	ds_read_b128 v[216:219], v209 offset:33792
	ds_read_b128 v[220:223], v209 offset:34816
	ds_read_b128 v[224:227], v209 offset:35840
	ds_read_b128 v[228:231], v209 offset:36864
	ds_read_b128 v[232:235], v209 offset:37888
	ds_read_b128 v[236:239], v209 offset:38912
	ds_read_b128 v[240:243], v209 offset:39936
	global_load_lds_dwordx4 v178, s[40:41]
	s_mov_b32 m0, s49
	s_nop 0
	global_load_lds_dwordx4 v180, s[40:41]
	s_waitcnt vmcnt(8)
	s_waitcnt lgkmcnt(0)
	s_setprio 1
	v_mfma_f32_16x16x128_f8f6f4 v[158:161], v[2:9], v[212:219], v[158:161]
	v_mfma_f32_16x16x128_f8f6f4 v[154:157], v[10:17], v[212:219], v[154:157]
	v_mfma_f32_16x16x128_f8f6f4 v[142:145], v[2:9], v[220:227], v[142:145]
	v_mfma_f32_16x16x128_f8f6f4 v[138:141], v[10:17], v[220:227], v[138:141]
	v_mfma_f32_16x16x128_f8f6f4 v[126:129], v[2:9], v[228:235], v[126:129]
	v_mfma_f32_16x16x128_f8f6f4 v[122:125], v[10:17], v[228:235], v[122:125]
	v_mfma_f32_16x16x128_f8f6f4 v[110:113], v[2:9], v[236:243], v[110:113]
	v_mfma_f32_16x16x128_f8f6f4 v[106:109], v[10:17], v[236:243], v[106:109]
	s_nop 3
	s_setprio 0
	s_setprio 1
	v_mfma_f32_16x16x128_f8f6f4 v[150:153], v[18:25], v[212:219], v[150:153]
	v_mfma_f32_16x16x128_f8f6f4 v[146:149], v[26:33], v[212:219], v[146:149]
	v_mfma_f32_16x16x128_f8f6f4 v[134:137], v[18:25], v[220:227], v[134:137]
	v_mfma_f32_16x16x128_f8f6f4 v[130:133], v[26:33], v[220:227], v[130:133]
	v_mfma_f32_16x16x128_f8f6f4 v[118:121], v[18:25], v[228:235], v[118:121]
	v_mfma_f32_16x16x128_f8f6f4 v[114:117], v[26:33], v[228:235], v[114:117]
	v_mfma_f32_16x16x128_f8f6f4 v[102:105], v[18:25], v[236:243], v[102:105]
	v_mfma_f32_16x16x128_f8f6f4 v[98:101], v[26:33], v[236:243], v[98:101]
	s_setprio 0
	s_barrier
	s_add_u32 s30, s30, 0x8000
	s_addc_u32 s31, s31, 0
	s_add_i32 s40, s67, s45
	s_mov_b32 m0, s40
	ds_read_b128 v[212:215], v209 offset:49152
	ds_read_b128 v[216:219], v209 offset:50176
	ds_read_b128 v[220:223], v209 offset:51200
	ds_read_b128 v[224:227], v209 offset:52224
	ds_read_b128 v[228:231], v209 offset:53248
	ds_read_b128 v[232:235], v209 offset:54272
	ds_read_b128 v[236:239], v209 offset:55296
	ds_read_b128 v[240:243], v209 offset:56320
	global_load_lds_dwordx4 v164, s[30:31]
	s_add_i32 m0, s40, 0x2000
	s_add_i32 s40, s68, s45
	global_load_lds_dwordx4 v166, s[30:31]
	s_mov_b32 m0, s40
	s_nop 0
	global_load_lds_dwordx4 v168, s[30:31]
	s_add_i32 m0, s40, 0x2000
	s_nop 0
	global_load_lds_dwordx4 v172, s[30:31]
	s_mov_b32 m0, s52
	s_nop 0
	global_load_lds_dwordx4 v174, s[28:29]
	s_mov_b32 m0, s53
	s_nop 0
	global_load_lds_dwordx4 v176, s[28:29]
	s_waitcnt vmcnt(8)
	s_waitcnt lgkmcnt(0)
	s_setprio 1
	v_mfma_f32_16x16x128_f8f6f4 v[94:97], v[2:9], v[212:219], v[94:97]
	v_mfma_f32_16x16x128_f8f6f4 v[90:93], v[10:17], v[212:219], v[90:93]
	v_mfma_f32_16x16x128_f8f6f4 v[78:81], v[2:9], v[220:227], v[78:81]
	v_mfma_f32_16x16x128_f8f6f4 v[74:77], v[10:17], v[220:227], v[74:77]
	v_mfma_f32_16x16x128_f8f6f4 v[62:65], v[2:9], v[228:235], v[62:65]
	v_mfma_f32_16x16x128_f8f6f4 v[58:61], v[10:17], v[228:235], v[58:61]
	v_mfma_f32_16x16x128_f8f6f4 v[46:49], v[2:9], v[236:243], v[46:49]
	v_mfma_f32_16x16x128_f8f6f4 v[42:45], v[10:17], v[236:243], v[42:45]
	s_nop 3
	s_setprio 0
	s_setprio 1
	v_mfma_f32_16x16x128_f8f6f4 v[86:89], v[18:25], v[212:219], v[86:89]
	v_mfma_f32_16x16x128_f8f6f4 v[82:85], v[26:33], v[212:219], v[82:85]
	v_mfma_f32_16x16x128_f8f6f4 v[70:73], v[18:25], v[220:227], v[70:73]
	v_mfma_f32_16x16x128_f8f6f4 v[66:69], v[26:33], v[220:227], v[66:69]
	v_mfma_f32_16x16x128_f8f6f4 v[54:57], v[18:25], v[228:235], v[54:57]
	v_mfma_f32_16x16x128_f8f6f4 v[50:53], v[26:33], v[228:235], v[50:53]
	v_mfma_f32_16x16x128_f8f6f4 v[38:41], v[18:25], v[236:243], v[38:41]
	v_mfma_f32_16x16x128_f8f6f4 v[34:37], v[26:33], v[236:243], v[34:37]
	s_setprio 0
	s_barrier
	s_add_i32 s21, s21, 2
	s_add_u32 s5, s5, 0x10000
	s_addc_u32 s19, s19, 0
	s_add_u32 s26, s26, 0x10000
	s_addc_u32 s27, s27, 0
	s_cmp_gt_u32 s21, 13
	s_cbranch_scc0 .LBB0_372
	s_branch .Lfx_9967
; #define PG8_STAGE(bufoff, gbase, voff) do { _Pragma("unroll") for (int _i = 0; _i < 2; ++_i) \
;         __builtin_amdgcn_global_load_lds((const unsigned*)((const char*)(gbase) + (voff)[_i]), (PG8_LAS unsigned*)(lds + (bufoff) + ldsw + _i * 8192), 16, 0, 0); } while (0)
; #define PG8_WAIT_V(n) asm volatile("s_waitcnt vmcnt(" #n ")" ::: "memory")
; #define PG8_WAIT_L(n) asm volatile("s_waitcnt lgkmcnt(" #n ")" ::: "memory")
; #define PG8_BAR __builtin_amdgcn_s_barrier()
; #define PG8_SCHED __builtin_amdgcn_sched_barrier(0)
; template <class Epi, class Sched, bool ALIGN_EPI = true, bool F8 = false>
; __device__ __forceinline__ void gemm_phase(PG8_LAS unsigned char* lds, const Sched& S, const Epi& E) {
;     ...
;             PG8_LDB(B0, 0, 0); PG8_LDB(B1, 0, 1); PG8_SCHED; PG8_LDA(At, 0, 0); PG8_STAGE(PG8_SA(1, 1), a1, voffA[1]);
;             PG8_WAIT_V(8); PG8_WAIT_L(0); PG8_BAR; PG8_MMA(0, 0, At, B0); PG8_MMA(0, 1, At, B1); PG8_BAR; PG8_SCHED;
;             PG8_LDA(At, 0, 1); PG8_STAGE(PG8_SB(0, 0), b2, voffB[0]); PG8_STAGE(PG8_SB(0, 1), b2, voffB[1]); PG8_STAGE(PG8_SA(0, 0), a2, vA2[0]);
;             PG8_WAIT_V(8); PG8_WAIT_L(0); PG8_BAR; PG8_MMA(1, 0, At, B0); PG8_MMA(1, 1, At, B1); PG8_BAR; PG8_SCHED;
;             PG8_LDB(B0, 1, 0); PG8_LDB(B1, 1, 1); PG8_SCHED; PG8_LDA(At, 1, 0); PG8_STAGE(PG8_SA(0, 1), a2, vA2[1]);
;             PG8_WAIT_V(8); PG8_WAIT_L(0); PG8_BAR; PG8_MMA(0, 0, At, B0); PG8_MMA(0, 1, At, B1); PG8_BAR; PG8_SCHED;
;             PG8_LDA(At, 1, 1); PG8_STAGE(PG8_SB(1, 0), b3, voffB[0]); PG8_STAGE(PG8_SB(1, 1), b3, voffB[1]); PG8_STAGE(PG8_SA(1, 0), a3, vA2[0]);
;             PG8_WAIT_V(8); PG8_WAIT_L(0); PG8_BAR; PG8_MMA(1, 0, At, B0); PG8_MMA(1, 1, At, B1); PG8_BAR; PG8_SCHED;
.Lh1e_9967:
.Lpk1_372:
	ds_read_b128 v[18:21], v207
	ds_read_b128 v[22:25], v207 offset:1024
	ds_read_b128 v[26:29], v207 offset:2048
	ds_read_b128 v[30:33], v207 offset:3072
	ds_read_b128 v[2:5], v208
	ds_read_b128 v[6:9], v208 offset:1024
	ds_read_b128 v[10:13], v208 offset:2048
	ds_read_b128 v[14:17], v208 offset:3072
	s_add_u32 s28, s26, 0x8000
	s_addc_u32 s29, s27, 0
	s_cmp_eq_u32 s21, 12
	s_cselect_b32 s40, s22, s28
	s_cselect_b32 s41, s23, s29
	s_cselect_b32 s30, s24, s5
	s_cselect_b32 s31, s25, s19
	s_add_u32 s28, s40, 0x8000
	s_addc_u32 s29, s41, 0
	s_add_i32 m0, s46, 0xc000
	ds_read_b128 v[212:215], v209
	ds_read_b128 v[216:219], v209 offset:1024
	ds_read_b128 v[220:223], v209 offset:2048
	ds_read_b128 v[224:227], v209 offset:3072
	ds_read_b128 v[228:231], v209 offset:4096
	ds_read_b128 v[232:235], v209 offset:5120
	ds_read_b128 v[236:239], v209 offset:6144
	ds_read_b128 v[240:243], v209 offset:7168
	global_load_lds_dwordx4 v190, s[26:27]
	s_add_i32 m0, s46, 0xe000
	s_nop 0
	global_load_lds_dwordx4 v188, s[26:27]
	s_waitcnt vmcnt(8)
	s_waitcnt lgkmcnt(0)
	s_barrier
	s_setprio 2
	v_mfma_f32_16x16x128_f8f6f4 v[158:161], v[18:25], v[212:219], 0
	v_mfma_f32_16x16x128_f8f6f4 v[154:157], v[26:33], v[212:219], 0
	v_mfma_f32_16x16x128_f8f6f4 v[142:145], v[18:25], v[220:227], 0
	v_mfma_f32_16x16x128_f8f6f4 v[138:141], v[26:33], v[220:227], 0
	v_mfma_f32_16x16x128_f8f6f4 v[126:129], v[18:25], v[228:235], 0
	v_mfma_f32_16x16x128_f8f6f4 v[122:125], v[26:33], v[228:235], 0
	v_mfma_f32_16x16x128_f8f6f4 v[110:113], v[18:25], v[236:243], 0
	v_mfma_f32_16x16x128_f8f6f4 v[106:109], v[26:33], v[236:243], 0
	s_nop 3
	s_setprio 0
	s_setprio 2
	v_mfma_f32_16x16x128_f8f6f4 v[150:153], v[2:9], v[212:219], 0
	v_mfma_f32_16x16x128_f8f6f4 v[146:149], v[10:17], v[212:219], 0
	v_mfma_f32_16x16x128_f8f6f4 v[134:137], v[2:9], v[220:227], 0
	v_mfma_f32_16x16x128_f8f6f4 v[130:133], v[10:17], v[220:227], 0
	v_mfma_f32_16x16x128_f8f6f4 v[118:121], v[2:9], v[228:235], 0
	v_mfma_f32_16x16x128_f8f6f4 v[114:117], v[10:17], v[228:235], 0
	v_mfma_f32_16x16x128_f8f6f4 v[102:105], v[2:9], v[236:243], 0
	v_mfma_f32_16x16x128_f8f6f4 v[98:101], v[10:17], v[236:243], 0
	s_setprio 0
	s_add_i32 s67, s62, s45
	s_mov_b32 m0, s67
	ds_read_b128 v[212:215], v209 offset:16384
	ds_read_b128 v[216:219], v209 offset:17408
	ds_read_b128 v[220:223], v209 offset:18432
	ds_read_b128 v[224:227], v209 offset:19456
	ds_read_b128 v[228:231], v209 offset:20480
	ds_read_b128 v[232:235], v209 offset:21504
	ds_read_b128 v[236:239], v209 offset:22528
	ds_read_b128 v[240:243], v209 offset:23552
	global_load_lds_dwordx4 v164, s[30:31]
	s_add_i32 m0, s67, 0x2000
	s_add_i32 s67, s63, s45
	global_load_lds_dwordx4 v166, s[30:31]
	s_add_u32 s98, s30, s8
	s_addc_u32 s99, s31, s9
	s_mov_b32 m0, s67
	s_nop 0
	global_load_lds_dwordx4 v164, s[98:99]
	s_add_u32 s100, s30, s8
	s_addc_u32 s101, s31, s9
	s_add_i32 m0, s67, 0x2000
	s_nop 0
	global_load_lds_dwordx4 v166, s[100:101]
	s_mov_b32 m0, s46
	s_nop 0
	global_load_lds_dwordx4 v174, s[40:41]
	s_mov_b32 m0, s47
	s_nop 0
	global_load_lds_dwordx4 v176, s[40:41]
	s_waitcnt vmcnt(8)
	s_waitcnt lgkmcnt(0)
	s_barrier
	s_setprio 2
	v_mfma_f32_16x16x128_f8f6f4 v[94:97], v[18:25], v[212:219], 0
	v_mfma_f32_16x16x128_f8f6f4 v[90:93], v[26:33], v[212:219], 0
	v_mfma_f32_16x16x128_f8f6f4 v[78:81], v[18:25], v[220:227], 0
	v_mfma_f32_16x16x128_f8f6f4 v[74:77], v[26:33], v[220:227], 0
	v_mfma_f32_16x16x128_f8f6f4 v[62:65], v[18:25], v[228:235], 0
	v_mfma_f32_16x16x128_f8f6f4 v[58:61], v[26:33], v[228:235], 0
	v_mfma_f32_16x16x128_f8f6f4 v[46:49], v[18:25], v[236:243], 0
	v_mfma_f32_16x16x128_f8f6f4 v[42:45], v[26:33], v[236:243], 0
	s_nop 3
	s_setprio 0
	s_setprio 2
	v_mfma_f32_16x16x128_f8f6f4 v[86:89], v[2:9], v[212:219], 0
	v_mfma_f32_16x16x128_f8f6f4 v[82:85], v[10:17], v[212:219], 0
	v_mfma_f32_16x16x128_f8f6f4 v[70:73], v[2:9], v[220:227], 0
	v_mfma_f32_16x16x128_f8f6f4 v[66:69], v[10:17], v[220:227], 0
	v_mfma_f32_16x16x128_f8f6f4 v[54:57], v[2:9], v[228:235], 0
	v_mfma_f32_16x16x128_f8f6f4 v[50:53], v[10:17], v[228:235], 0
	v_mfma_f32_16x16x128_f8f6f4 v[38:41], v[2:9], v[236:243], 0
	v_mfma_f32_16x16x128_f8f6f4 v[34:37], v[10:17], v[236:243], 0
	s_setprio 0
	s_add_i32 s67, 0, 0x18000
	s_add_i32 s68, 0, 0x1c000
	v_add_u32_e32 v14, s67, v202
	v_add_u32_e32 v30, s68, v202
	ds_read_b128 v[2:5], v14
	ds_read_b128 v[6:9], v14 offset:1024
	ds_read_b128 v[10:13], v14 offset:2048
	ds_read_b128 v[14:17], v14 offset:3072
	ds_read_b128 v[18:21], v30
	ds_read_b128 v[22:25], v30 offset:1024
	ds_read_b128 v[26:29], v30 offset:2048
	ds_read_b128 v[30:33], v30 offset:3072
	s_mov_b32 m0, s48
	ds_read_b128 v[212:215], v209 offset:32768
	ds_read_b128 v[216:219], v209 offset:33792
	ds_read_b128 v[220:223], v209 offset:34816
	ds_read_b128 v[224:227], v209 offset:35840
	ds_read_b128 v[228:231], v209 offset:36864
	ds_read_b128 v[232:235], v209 offset:37888
	ds_read_b128 v[236:239], v209 offset:38912
	ds_read_b128 v[240:243], v209 offset:39936
	global_load_lds_dwordx4 v178, s[40:41]
	s_mov_b32 m0, s49
	s_nop 0
	global_load_lds_dwordx4 v180, s[40:41]
	s_waitcnt vmcnt(8)
	s_waitcnt lgkmcnt(0)
	s_barrier
; #define PG8_STAGE(bufoff, gbase, voff) do { _Pragma("unroll") for (int _i = 0; _i < 2; ++_i) \
;         __builtin_amdgcn_global_load_lds((const unsigned*)((const char*)(gbase) + (voff)[_i]), (PG8_LAS unsigned*)(lds + (bufoff) + ldsw + _i * 8192), 16, 0, 0); } while (0)
; #define PG8_WAIT_V(n) asm volatile("s_waitcnt vmcnt(" #n ")" ::: "memory")
; #define PG8_WAIT_L(n) asm volatile("s_waitcnt lgkmcnt(" #n ")" ::: "memory")
; #define PG8_BAR __builtin_amdgcn_s_barrier()
; #define PG8_SCHED __builtin_amdgcn_sched_barrier(0)
; template <class Epi, class Sched, bool ALIGN_EPI = true, bool F8 = false>
; __device__ __forceinline__ void gemm_phase(PG8_LAS unsigned char* lds, const Sched& S, const Epi& E) {
;     ...
;             PG8_LDB(B0, 0, 0); PG8_LDB(B1, 0, 1); PG8_SCHED; PG8_LDA(At, 0, 0); PG8_STAGE(PG8_SA(1, 1), a1, voffA[1]);
;             PG8_WAIT_V(8); PG8_WAIT_L(0); PG8_BAR; PG8_MMA(0, 0, At, B0); PG8_MMA(0, 1, At, B1); PG8_BAR; PG8_SCHED;
;     ...
;             PG8_LDA(At, 1, 1); PG8_STAGE(PG8_SB(1, 0), b3, voffB[0]); PG8_STAGE(PG8_SB(1, 1), b3, voffB[1]); PG8_STAGE(PG8_SA(1, 0), a3, vA2[0]);
;             PG8_WAIT_V(8); PG8_WAIT_L(0); PG8_BAR; PG8_MMA(1, 0, At, B0); PG8_MMA(1, 1, At, B1); PG8_BAR; PG8_SCHED;
;         }
	s_setprio 2
	v_mfma_f32_16x16x128_f8f6f4 v[158:161], v[2:9], v[212:219], v[158:161]
	v_mfma_f32_16x16x128_f8f6f4 v[154:157], v[10:17], v[212:219], v[154:157]
	v_mfma_f32_16x16x128_f8f6f4 v[142:145], v[2:9], v[220:227], v[142:145]
	v_mfma_f32_16x16x128_f8f6f4 v[138:141], v[10:17], v[220:227], v[138:141]
	v_mfma_f32_16x16x128_f8f6f4 v[126:129], v[2:9], v[228:235], v[126:129]
	v_mfma_f32_16x16x128_f8f6f4 v[122:125], v[10:17], v[228:235], v[122:125]
	v_mfma_f32_16x16x128_f8f6f4 v[110:113], v[2:9], v[236:243], v[110:113]
	v_mfma_f32_16x16x128_f8f6f4 v[106:109], v[10:17], v[236:243], v[106:109]
	s_nop 3
	s_setprio 0
	s_setprio 2
	v_mfma_f32_16x16x128_f8f6f4 v[150:153], v[18:25], v[212:219], v[150:153]
	v_mfma_f32_16x16x128_f8f6f4 v[146:149], v[26:33], v[212:219], v[146:149]
	v_mfma_f32_16x16x128_f8f6f4 v[134:137], v[18:25], v[220:227], v[134:137]
	v_mfma_f32_16x16x128_f8f6f4 v[130:133], v[26:33], v[220:227], v[130:133]
	v_mfma_f32_16x16x128_f8f6f4 v[118:121], v[18:25], v[228:235], v[118:121]
	v_mfma_f32_16x16x128_f8f6f4 v[114:117], v[26:33], v[228:235], v[114:117]
	v_mfma_f32_16x16x128_f8f6f4 v[102:105], v[18:25], v[236:243], v[102:105]
	v_mfma_f32_16x16x128_f8f6f4 v[98:101], v[26:33], v[236:243], v[98:101]
	s_setprio 0
	s_add_u32 s30, s30, 0x8000
	s_addc_u32 s31, s31, 0
	s_add_i32 s40, s67, s45
	s_mov_b32 m0, s40
	ds_read_b128 v[212:215], v209 offset:49152
	ds_read_b128 v[216:219], v209 offset:50176
	ds_read_b128 v[220:223], v209 offset:51200
	ds_read_b128 v[224:227], v209 offset:52224
	ds_read_b128 v[228:231], v209 offset:53248
	ds_read_b128 v[232:235], v209 offset:54272
	ds_read_b128 v[236:239], v209 offset:55296
	ds_read_b128 v[240:243], v209 offset:56320
	global_load_lds_dwordx4 v164, s[30:31]
	s_add_i32 m0, s40, 0x2000
	s_add_i32 s40, s68, s45
	global_load_lds_dwordx4 v166, s[30:31]
	s_mov_b32 m0, s40
	s_nop 0
	global_load_lds_dwordx4 v168, s[30:31]
	s_add_i32 m0, s40, 0x2000
	s_nop 0
	global_load_lds_dwordx4 v172, s[30:31]
	s_mov_b32 m0, s52
	s_nop 0
	global_load_lds_dwordx4 v174, s[28:29]
	s_mov_b32 m0, s53
	s_nop 0
	global_load_lds_dwordx4 v176, s[28:29]
	s_waitcnt vmcnt(8)
	s_waitcnt lgkmcnt(0)
	s_barrier
	s_setprio 2
	v_mfma_f32_16x16x128_f8f6f4 v[94:97], v[2:9], v[212:219], v[94:97]
	v_mfma_f32_16x16x128_f8f6f4 v[90:93], v[10:17], v[212:219], v[90:93]
	v_mfma_f32_16x16x128_f8f6f4 v[78:81], v[2:9], v[220:227], v[78:81]
	v_mfma_f32_16x16x128_f8f6f4 v[74:77], v[10:17], v[220:227], v[74:77]
	v_mfma_f32_16x16x128_f8f6f4 v[62:65], v[2:9], v[228:235], v[62:65]
	v_mfma_f32_16x16x128_f8f6f4 v[58:61], v[10:17], v[228:235], v[58:61]
	v_mfma_f32_16x16x128_f8f6f4 v[46:49], v[2:9], v[236:243], v[46:49]
	v_mfma_f32_16x16x128_f8f6f4 v[42:45], v[10:17], v[236:243], v[42:45]
	s_nop 3
	s_setprio 0
	s_setprio 2
	v_mfma_f32_16x16x128_f8f6f4 v[86:89], v[18:25], v[212:219], v[86:89]
	v_mfma_f32_16x16x128_f8f6f4 v[82:85], v[26:33], v[212:219], v[82:85]
	v_mfma_f32_16x16x128_f8f6f4 v[70:73], v[18:25], v[220:227], v[70:73]
	v_mfma_f32_16x16x128_f8f6f4 v[66:69], v[26:33], v[220:227], v[66:69]
	v_mfma_f32_16x16x128_f8f6f4 v[54:57], v[18:25], v[228:235], v[54:57]
	v_mfma_f32_16x16x128_f8f6f4 v[50:53], v[26:33], v[228:235], v[50:53]
	v_mfma_f32_16x16x128_f8f6f4 v[38:41], v[18:25], v[236:243], v[38:41]
	v_mfma_f32_16x16x128_f8f6f4 v[34:37], v[26:33], v[236:243], v[34:37]
	s_setprio 0
	s_add_i32 s21, s21, 2
	s_add_u32 s5, s5, 0x10000
	s_addc_u32 s19, s19, 0
	s_add_u32 s26, s26, 0x10000
	s_addc_u32 s27, s27, 0
	s_cmp_gt_u32 s21, 13
	s_cbranch_scc0 .Lh1_372
	s_branch .Lfx_9967
.Lh1_372:
	ds_read_b128 v[18:21], v207
	ds_read_b128 v[22:25], v207 offset:1024
	ds_read_b128 v[26:29], v207 offset:2048
	ds_read_b128 v[30:33], v207 offset:3072
	ds_read_b128 v[2:5], v208
	ds_read_b128 v[6:9], v208 offset:1024
	ds_read_b128 v[10:13], v208 offset:2048
	ds_read_b128 v[14:17], v208 offset:3072
	s_add_u32 s28, s26, 0x8000
	s_addc_u32 s29, s27, 0
	s_cmp_eq_u32 s21, 12
	s_cselect_b32 s40, s22, s28
	s_cselect_b32 s41, s23, s29
	s_cselect_b32 s30, s24, s5
	s_cselect_b32 s31, s25, s19
	s_add_u32 s28, s40, 0x8000
	s_addc_u32 s29, s41, 0
	s_add_i32 m0, s46, 0xc000
	ds_read_b128 v[212:215], v209
	ds_read_b128 v[216:219], v209 offset:1024
	ds_read_b128 v[220:223], v209 offset:2048
	ds_read_b128 v[224:227], v209 offset:3072
	ds_read_b128 v[228:231], v209 offset:4096
	ds_read_b128 v[232:235], v209 offset:5120
	ds_read_b128 v[236:239], v209 offset:6144
	ds_read_b128 v[240:243], v209 offset:7168
	global_load_lds_dwordx4 v190, s[26:27]
	s_add_i32 m0, s46, 0xe000
	s_nop 0
	global_load_lds_dwordx4 v188, s[26:27]
	s_waitcnt vmcnt(8)
	s_waitcnt lgkmcnt(0)
	s_barrier
; #define PG8_STAGE(bufoff, gbase, voff) do { _Pragma("unroll") for (int _i = 0; _i < 2; ++_i) \
;         __builtin_amdgcn_global_load_lds((const unsigned*)((const char*)(gbase) + (voff)[_i]), (PG8_LAS unsigned*)(lds + (bufoff) + ldsw + _i * 8192), 16, 0, 0); } while (0)
; #define PG8_WAIT_V(n) asm volatile("s_waitcnt vmcnt(" #n ")" ::: "memory")
; #define PG8_WAIT_L(n) asm volatile("s_waitcnt lgkmcnt(" #n ")" ::: "memory")
; #define PG8_BAR __builtin_amdgcn_s_barrier()
; #define PG8_SCHED __builtin_amdgcn_sched_barrier(0)
; template <class Epi, class Sched, bool ALIGN_EPI = true, bool F8 = false>
; __device__ __forceinline__ void gemm_phase(PG8_LAS unsigned char* lds, const Sched& S, const Epi& E) {
;     ...
;             PG8_LDB(B0, 0, 0); PG8_LDB(B1, 0, 1); PG8_SCHED; PG8_LDA(At, 0, 0); PG8_STAGE(PG8_SA(1, 1), a1, voffA[1]);
;             PG8_WAIT_V(8); PG8_WAIT_L(0); PG8_BAR; PG8_MMA(0, 0, At, B0); PG8_MMA(0, 1, At, B1); PG8_BAR; PG8_SCHED;
;             PG8_LDA(At, 0, 1); PG8_STAGE(PG8_SB(0, 0), b2, voffB[0]); PG8_STAGE(PG8_SB(0, 1), b2, voffB[1]); PG8_STAGE(PG8_SA(0, 0), a2, vA2[0]);
;             PG8_WAIT_V(8); PG8_WAIT_L(0); PG8_BAR; PG8_MMA(1, 0, At, B0); PG8_MMA(1, 1, At, B1); PG8_BAR; PG8_SCHED;
;             PG8_LDB(B0, 1, 0); PG8_LDB(B1, 1, 1); PG8_SCHED; PG8_LDA(At, 1, 0); PG8_STAGE(PG8_SA(0, 1), a2, vA2[1]);
;             PG8_WAIT_V(8); PG8_WAIT_L(0); PG8_BAR; PG8_MMA(0, 0, At, B0); PG8_MMA(0, 1, At, B1); PG8_BAR; PG8_SCHED;
	s_setprio 2
	v_mfma_f32_16x16x128_f8f6f4 v[158:161], v[18:25], v[212:219], v[158:161]
	v_mfma_f32_16x16x128_f8f6f4 v[154:157], v[26:33], v[212:219], v[154:157]
	v_mfma_f32_16x16x128_f8f6f4 v[142:145], v[18:25], v[220:227], v[142:145]
	v_mfma_f32_16x16x128_f8f6f4 v[138:141], v[26:33], v[220:227], v[138:141]
	v_mfma_f32_16x16x128_f8f6f4 v[126:129], v[18:25], v[228:235], v[126:129]
	v_mfma_f32_16x16x128_f8f6f4 v[122:125], v[26:33], v[228:235], v[122:125]
	v_mfma_f32_16x16x128_f8f6f4 v[110:113], v[18:25], v[236:243], v[110:113]
	v_mfma_f32_16x16x128_f8f6f4 v[106:109], v[26:33], v[236:243], v[106:109]
	s_nop 3
	s_setprio 0
	s_setprio 2
	v_mfma_f32_16x16x128_f8f6f4 v[150:153], v[2:9], v[212:219], v[150:153]
	v_mfma_f32_16x16x128_f8f6f4 v[146:149], v[10:17], v[212:219], v[146:149]
	v_mfma_f32_16x16x128_f8f6f4 v[134:137], v[2:9], v[220:227], v[134:137]
	v_mfma_f32_16x16x128_f8f6f4 v[130:133], v[10:17], v[220:227], v[130:133]
	v_mfma_f32_16x16x128_f8f6f4 v[118:121], v[2:9], v[228:235], v[118:121]
	v_mfma_f32_16x16x128_f8f6f4 v[114:117], v[10:17], v[228:235], v[114:117]
	v_mfma_f32_16x16x128_f8f6f4 v[102:105], v[2:9], v[236:243], v[102:105]
	v_mfma_f32_16x16x128_f8f6f4 v[98:101], v[10:17], v[236:243], v[98:101]
	s_setprio 0
	s_add_i32 s67, s62, s45
	s_mov_b32 m0, s67
	ds_read_b128 v[212:215], v209 offset:16384
	ds_read_b128 v[216:219], v209 offset:17408
	ds_read_b128 v[220:223], v209 offset:18432
	ds_read_b128 v[224:227], v209 offset:19456
	ds_read_b128 v[228:231], v209 offset:20480
	ds_read_b128 v[232:235], v209 offset:21504
	ds_read_b128 v[236:239], v209 offset:22528
	ds_read_b128 v[240:243], v209 offset:23552
	global_load_lds_dwordx4 v164, s[30:31]
	s_add_i32 m0, s67, 0x2000
	s_add_i32 s67, s63, s45
	global_load_lds_dwordx4 v166, s[30:31]
	s_add_u32 s98, s30, s8
	s_addc_u32 s99, s31, s9
	s_mov_b32 m0, s67
	s_nop 0
	global_load_lds_dwordx4 v164, s[98:99]
	s_add_u32 s100, s30, s8
	s_addc_u32 s101, s31, s9
	s_add_i32 m0, s67, 0x2000
	s_nop 0
	global_load_lds_dwordx4 v166, s[100:101]
	s_mov_b32 m0, s46
	s_nop 0
	global_load_lds_dwordx4 v174, s[40:41]
	s_mov_b32 m0, s47
	s_nop 0
	global_load_lds_dwordx4 v176, s[40:41]
	s_waitcnt vmcnt(8)
	s_waitcnt lgkmcnt(0)
	s_barrier
	s_setprio 2
	v_mfma_f32_16x16x128_f8f6f4 v[94:97], v[18:25], v[212:219], v[94:97]
	v_mfma_f32_16x16x128_f8f6f4 v[90:93], v[26:33], v[212:219], v[90:93]
	v_mfma_f32_16x16x128_f8f6f4 v[78:81], v[18:25], v[220:227], v[78:81]
	v_mfma_f32_16x16x128_f8f6f4 v[74:77], v[26:33], v[220:227], v[74:77]
	v_mfma_f32_16x16x128_f8f6f4 v[62:65], v[18:25], v[228:235], v[62:65]
	v_mfma_f32_16x16x128_f8f6f4 v[58:61], v[26:33], v[228:235], v[58:61]
	v_mfma_f32_16x16x128_f8f6f4 v[46:49], v[18:25], v[236:243], v[46:49]
	v_mfma_f32_16x16x128_f8f6f4 v[42:45], v[26:33], v[236:243], v[42:45]
	s_nop 3
	s_setprio 0
	s_setprio 2
	v_mfma_f32_16x16x128_f8f6f4 v[86:89], v[2:9], v[212:219], v[86:89]
	v_mfma_f32_16x16x128_f8f6f4 v[82:85], v[10:17], v[212:219], v[82:85]
	v_mfma_f32_16x16x128_f8f6f4 v[70:73], v[2:9], v[220:227], v[70:73]
	v_mfma_f32_16x16x128_f8f6f4 v[66:69], v[10:17], v[220:227], v[66:69]
	v_mfma_f32_16x16x128_f8f6f4 v[54:57], v[2:9], v[228:235], v[54:57]
	v_mfma_f32_16x16x128_f8f6f4 v[50:53], v[10:17], v[228:235], v[50:53]
	v_mfma_f32_16x16x128_f8f6f4 v[38:41], v[2:9], v[236:243], v[38:41]
	v_mfma_f32_16x16x128_f8f6f4 v[34:37], v[10:17], v[236:243], v[34:37]
	s_setprio 0
	s_add_i32 s67, 0, 0x18000
	s_add_i32 s68, 0, 0x1c000
	v_add_u32_e32 v14, s67, v202
	v_add_u32_e32 v30, s68, v202
	ds_read_b128 v[2:5], v14
	ds_read_b128 v[6:9], v14 offset:1024
	ds_read_b128 v[10:13], v14 offset:2048
	ds_read_b128 v[14:17], v14 offset:3072
	ds_read_b128 v[18:21], v30
	ds_read_b128 v[22:25], v30 offset:1024
	ds_read_b128 v[26:29], v30 offset:2048
	ds_read_b128 v[30:33], v30 offset:3072
	s_mov_b32 m0, s48
	ds_read_b128 v[212:215], v209 offset:32768
	ds_read_b128 v[216:219], v209 offset:33792
	ds_read_b128 v[220:223], v209 offset:34816
	ds_read_b128 v[224:227], v209 offset:35840
	ds_read_b128 v[228:231], v209 offset:36864
	ds_read_b128 v[232:235], v209 offset:37888
	ds_read_b128 v[236:239], v209 offset:38912
	ds_read_b128 v[240:243], v209 offset:39936
	global_load_lds_dwordx4 v178, s[40:41]
	s_mov_b32 m0, s49
	s_nop 0
	global_load_lds_dwordx4 v180, s[40:41]
	s_waitcnt vmcnt(8)
	s_waitcnt lgkmcnt(0)
	s_barrier
; #define PG8_STAGE(bufoff, gbase, voff) do { _Pragma("unroll") for (int _i = 0; _i < 2; ++_i) \
;         __builtin_amdgcn_global_load_lds((const unsigned*)((const char*)(gbase) + (voff)[_i]), (PG8_LAS unsigned*)(lds + (bufoff) + ldsw + _i * 8192), 16, 0, 0); } while (0)
; #define PG8_WAIT_V(n) asm volatile("s_waitcnt vmcnt(" #n ")" ::: "memory")
; #define PG8_WAIT_L(n) asm volatile("s_waitcnt lgkmcnt(" #n ")" ::: "memory")
; #define PG8_BAR __builtin_amdgcn_s_barrier()
; #define PG8_SCHED __builtin_amdgcn_sched_barrier(0)
; template <class Epi, class Sched, bool ALIGN_EPI = true, bool F8 = false>
; __device__ __forceinline__ void gemm_phase(PG8_LAS unsigned char* lds, const Sched& S, const Epi& E) {
;     ...
;         for (int t = 0; t < nt; t += 2) {
;     ...
;             PG8_LDA(At, 1, 1); PG8_STAGE(PG8_SB(1, 0), b3, voffB[0]); PG8_STAGE(PG8_SB(1, 1), b3, voffB[1]); PG8_STAGE(PG8_SA(1, 0), a3, vA2[0]);
;             PG8_WAIT_V(8); PG8_WAIT_L(0); PG8_BAR; PG8_MMA(1, 0, At, B0); PG8_MMA(1, 1, At, B1); PG8_BAR; PG8_SCHED;
	s_setprio 2
	v_mfma_f32_16x16x128_f8f6f4 v[158:161], v[2:9], v[212:219], v[158:161]
	v_mfma_f32_16x16x128_f8f6f4 v[154:157], v[10:17], v[212:219], v[154:157]
	v_mfma_f32_16x16x128_f8f6f4 v[142:145], v[2:9], v[220:227], v[142:145]
	v_mfma_f32_16x16x128_f8f6f4 v[138:141], v[10:17], v[220:227], v[138:141]
	v_mfma_f32_16x16x128_f8f6f4 v[126:129], v[2:9], v[228:235], v[126:129]
	v_mfma_f32_16x16x128_f8f6f4 v[122:125], v[10:17], v[228:235], v[122:125]
	v_mfma_f32_16x16x128_f8f6f4 v[110:113], v[2:9], v[236:243], v[110:113]
	v_mfma_f32_16x16x128_f8f6f4 v[106:109], v[10:17], v[236:243], v[106:109]
	s_nop 3
	s_setprio 0
	s_setprio 2
	v_mfma_f32_16x16x128_f8f6f4 v[150:153], v[18:25], v[212:219], v[150:153]
	v_mfma_f32_16x16x128_f8f6f4 v[146:149], v[26:33], v[212:219], v[146:149]
	v_mfma_f32_16x16x128_f8f6f4 v[134:137], v[18:25], v[220:227], v[134:137]
	v_mfma_f32_16x16x128_f8f6f4 v[130:133], v[26:33], v[220:227], v[130:133]
	v_mfma_f32_16x16x128_f8f6f4 v[118:121], v[18:25], v[228:235], v[118:121]
	v_mfma_f32_16x16x128_f8f6f4 v[114:117], v[26:33], v[228:235], v[114:117]
	v_mfma_f32_16x16x128_f8f6f4 v[102:105], v[18:25], v[236:243], v[102:105]
	v_mfma_f32_16x16x128_f8f6f4 v[98:101], v[26:33], v[236:243], v[98:101]
	s_setprio 0
	s_add_u32 s30, s30, 0x8000
	s_addc_u32 s31, s31, 0
	s_add_i32 s40, s67, s45
	s_mov_b32 m0, s40
	ds_read_b128 v[212:215], v209 offset:49152
	ds_read_b128 v[216:219], v209 offset:50176
	ds_read_b128 v[220:223], v209 offset:51200
	ds_read_b128 v[224:227], v209 offset:52224
	ds_read_b128 v[228:231], v209 offset:53248
	ds_read_b128 v[232:235], v209 offset:54272
	ds_read_b128 v[236:239], v209 offset:55296
	ds_read_b128 v[240:243], v209 offset:56320
	global_load_lds_dwordx4 v164, s[30:31]
	s_add_i32 m0, s40, 0x2000
	s_add_i32 s40, s68, s45
	global_load_lds_dwordx4 v166, s[30:31]
	s_mov_b32 m0, s40
	s_nop 0
	global_load_lds_dwordx4 v168, s[30:31]
	s_add_i32 m0, s40, 0x2000
	s_nop 0
	global_load_lds_dwordx4 v172, s[30:31]
	s_mov_b32 m0, s52
	s_nop 0
	global_load_lds_dwordx4 v174, s[28:29]
	s_mov_b32 m0, s53
	s_nop 0
	global_load_lds_dwordx4 v176, s[28:29]
	s_waitcnt vmcnt(8)
	s_waitcnt lgkmcnt(0)
	s_barrier
	s_setprio 2
	v_mfma_f32_16x16x128_f8f6f4 v[94:97], v[2:9], v[212:219], v[94:97]
	v_mfma_f32_16x16x128_f8f6f4 v[90:93], v[10:17], v[212:219], v[90:93]
	v_mfma_f32_16x16x128_f8f6f4 v[78:81], v[2:9], v[220:227], v[78:81]
	v_mfma_f32_16x16x128_f8f6f4 v[74:77], v[10:17], v[220:227], v[74:77]
	v_mfma_f32_16x16x128_f8f6f4 v[62:65], v[2:9], v[228:235], v[62:65]
	v_mfma_f32_16x16x128_f8f6f4 v[58:61], v[10:17], v[228:235], v[58:61]
	v_mfma_f32_16x16x128_f8f6f4 v[46:49], v[2:9], v[236:243], v[46:49]
	v_mfma_f32_16x16x128_f8f6f4 v[42:45], v[10:17], v[236:243], v[42:45]
	s_nop 3
	s_setprio 0
	s_setprio 2
	v_mfma_f32_16x16x128_f8f6f4 v[86:89], v[18:25], v[212:219], v[86:89]
	v_mfma_f32_16x16x128_f8f6f4 v[82:85], v[26:33], v[212:219], v[82:85]
	v_mfma_f32_16x16x128_f8f6f4 v[70:73], v[18:25], v[220:227], v[70:73]
	v_mfma_f32_16x16x128_f8f6f4 v[66:69], v[26:33], v[220:227], v[66:69]
	v_mfma_f32_16x16x128_f8f6f4 v[54:57], v[18:25], v[228:235], v[54:57]
	v_mfma_f32_16x16x128_f8f6f4 v[50:53], v[26:33], v[228:235], v[50:53]
	v_mfma_f32_16x16x128_f8f6f4 v[38:41], v[18:25], v[236:243], v[38:41]
	v_mfma_f32_16x16x128_f8f6f4 v[34:37], v[26:33], v[236:243], v[34:37]
	s_setprio 0
	s_add_i32 s21, s21, 2
	s_add_u32 s5, s5, 0x10000
	s_addc_u32 s19, s19, 0
	s_add_u32 s26, s26, 0x10000
	s_addc_u32 s27, s27, 0
	s_cmp_gt_u32 s21, 13
	s_cbranch_scc0 .Lh1_372

; #define PG8_STAGE(bufoff, gbase, voff) do { _Pragma("unroll") for (int _i = 0; _i < 2; ++_i) \
;         __builtin_amdgcn_global_load_lds((const unsigned*)((const char*)(gbase) + (voff)[_i]), (PG8_LAS unsigned*)(lds + (bufoff) + ldsw + _i * 8192), 16, 0, 0); } while (0)
; #define PG8_WAIT_V(n) asm volatile("s_waitcnt vmcnt(" #n ")" ::: "memory")
; #define PG8_WAIT_L(n) asm volatile("s_waitcnt lgkmcnt(" #n ")" ::: "memory")
; #define PG8_BAR __builtin_amdgcn_s_barrier()
; #define PG8_SCHED __builtin_amdgcn_sched_barrier(0)
; template <class Epi, class Sched, bool ALIGN_EPI = true, bool F8 = false>
; __device__ __forceinline__ void gemm_phase(PG8_LAS unsigned char* lds, const Sched& S, const Epi& E) {
;     ...
;     f32x4 acc[2][2][4][2];
; #pragma unroll
;     for (int a = 0; a < 2; ++a)
; #pragma unroll
;         for (int b = 0; b < 2; ++b)
; #pragma unroll
;             for (int m = 0; m < 4; ++m)
; #pragma unroll
;                 for (int n = 0; n < 2; ++n) acc[a][b][m][n] = (f32x4){0.f, 0.f, 0.f, 0.f};
;     ...
;             PG8_LDB(B0, 0, 0); PG8_LDB(B1, 0, 1); PG8_SCHED; PG8_LDA(At, 0, 0); PG8_STAGE(PG8_SA(1, 1), a1, voffA[1]);
;             PG8_WAIT_V(8); PG8_WAIT_L(0); PG8_BAR; PG8_MMA(0, 0, At, B0); PG8_MMA(0, 1, At, B1); PG8_BAR; PG8_SCHED;
;             PG8_LDA(At, 0, 1); PG8_STAGE(PG8_SB(0, 0), b2, voffB[0]); PG8_STAGE(PG8_SB(0, 1), b2, voffB[1]); PG8_STAGE(PG8_SA(0, 0), a2, vA2[0]);
;             PG8_WAIT_V(8); PG8_WAIT_L(0); PG8_BAR; PG8_MMA(1, 0, At, B0); PG8_MMA(1, 1, At, B1); PG8_BAR; PG8_SCHED;
;             PG8_LDB(B0, 1, 0); PG8_LDB(B1, 1, 1); PG8_SCHED; PG8_LDA(At, 1, 0); PG8_STAGE(PG8_SA(0, 1), a2, vA2[1]);
;             PG8_WAIT_V(8); PG8_WAIT_L(0); PG8_BAR; PG8_MMA(0, 0, At, B0); PG8_MMA(0, 1, At, B1); PG8_BAR; PG8_SCHED;
.Lpk0_428:
	ds_read_b128 v[18:21], v192
	ds_read_b128 v[22:25], v192 offset:1024
	ds_read_b128 v[26:29], v192 offset:2048
	ds_read_b128 v[30:33], v192 offset:3072
	ds_read_b128 v[2:5], v193
	ds_read_b128 v[6:9], v193 offset:1024
	ds_read_b128 v[10:13], v193 offset:2048
	ds_read_b128 v[14:17], v193 offset:3072
	s_add_u32 s26, s24, 0x8000
	s_addc_u32 s27, s25, 0
	s_cmp_eq_u32 s74, 12
	s_cselect_b32 s30, s20, s26
	s_cselect_b32 s31, s21, s27
	s_cselect_b32 s28, s22, s17
	s_cselect_b32 s29, s23, s19
	s_add_u32 s26, s30, 0x8000
	s_addc_u32 s27, s31, 0
	s_add_i32 m0, s48, 0xc000
	ds_read_b128 v[198:201], v194
	ds_read_b128 v[202:205], v194 offset:1024
	ds_read_b128 v[206:209], v194 offset:2048
	ds_read_b128 v[210:213], v194 offset:3072
	ds_read_b128 v[214:217], v194 offset:4096
	ds_read_b128 v[218:221], v194 offset:5120
	ds_read_b128 v[222:225], v194 offset:6144
	ds_read_b128 v[226:229], v194 offset:7168
	global_load_lds_dwordx4 v184, s[24:25]
	s_add_i32 m0, s48, 0xe000
	s_nop 0
	global_load_lds_dwordx4 v182, s[24:25]
	s_waitcnt vmcnt(8)
	s_waitcnt lgkmcnt(0)
	s_setprio 1
	v_mfma_f32_16x16x128_f8f6f4 v[158:161], v[18:25], v[198:205], 0
	v_mfma_f32_16x16x128_f8f6f4 v[154:157], v[26:33], v[198:205], 0
	v_mfma_f32_16x16x128_f8f6f4 v[142:145], v[18:25], v[206:213], 0
	v_mfma_f32_16x16x128_f8f6f4 v[138:141], v[26:33], v[206:213], 0
	v_mfma_f32_16x16x128_f8f6f4 v[126:129], v[18:25], v[214:221], 0
	v_mfma_f32_16x16x128_f8f6f4 v[122:125], v[26:33], v[214:221], 0
	v_mfma_f32_16x16x128_f8f6f4 v[110:113], v[18:25], v[222:229], 0
	v_mfma_f32_16x16x128_f8f6f4 v[106:109], v[26:33], v[222:229], 0
	s_nop 3
	s_setprio 0
	s_setprio 1
	v_mfma_f32_16x16x128_f8f6f4 v[150:153], v[2:9], v[198:205], 0
	v_mfma_f32_16x16x128_f8f6f4 v[146:149], v[10:17], v[198:205], 0
	v_mfma_f32_16x16x128_f8f6f4 v[134:137], v[2:9], v[206:213], 0
	v_mfma_f32_16x16x128_f8f6f4 v[130:133], v[10:17], v[206:213], 0
	v_mfma_f32_16x16x128_f8f6f4 v[118:121], v[2:9], v[214:221], 0
	v_mfma_f32_16x16x128_f8f6f4 v[114:117], v[10:17], v[214:221], 0
	v_mfma_f32_16x16x128_f8f6f4 v[102:105], v[2:9], v[222:229], 0
	v_mfma_f32_16x16x128_f8f6f4 v[98:101], v[10:17], v[222:229], 0
	s_setprio 0
	s_barrier
	s_add_i32 s75, s65, s47
	s_mov_b32 m0, s75
	ds_read_b128 v[198:201], v194 offset:16384
	ds_read_b128 v[202:205], v194 offset:17408
	ds_read_b128 v[206:209], v194 offset:18432
	ds_read_b128 v[210:213], v194 offset:19456
	ds_read_b128 v[214:217], v194 offset:20480
	ds_read_b128 v[218:221], v194 offset:21504
	ds_read_b128 v[222:225], v194 offset:22528
	ds_read_b128 v[226:229], v194 offset:23552
	global_load_lds_dwordx4 v164, s[28:29]
	s_add_i32 m0, s75, 0x2000
	s_add_i32 s75, s66, s47
	global_load_lds_dwordx4 v166, s[28:29]
	s_add_u32 s98, s28, s4
	s_addc_u32 s99, s29, s5
	s_mov_b32 m0, s75
	s_nop 0
	global_load_lds_dwordx4 v164, s[98:99]
	s_add_u32 s100, s28, s4
	s_addc_u32 s101, s29, s5
	s_add_i32 m0, s75, 0x2000
	s_nop 0
	global_load_lds_dwordx4 v166, s[100:101]
	s_mov_b32 m0, s48
	s_nop 0
	global_load_lds_dwordx4 v174, s[30:31]
	s_mov_b32 m0, s49
	s_nop 0
	global_load_lds_dwordx4 v176, s[30:31]
	s_waitcnt vmcnt(8)
	s_waitcnt lgkmcnt(0)
	s_setprio 1
	v_mfma_f32_16x16x128_f8f6f4 v[94:97], v[18:25], v[198:205], 0
	v_mfma_f32_16x16x128_f8f6f4 v[90:93], v[26:33], v[198:205], 0
	v_mfma_f32_16x16x128_f8f6f4 v[78:81], v[18:25], v[206:213], 0
	v_mfma_f32_16x16x128_f8f6f4 v[74:77], v[26:33], v[206:213], 0
	v_mfma_f32_16x16x128_f8f6f4 v[62:65], v[18:25], v[214:221], 0
	v_mfma_f32_16x16x128_f8f6f4 v[58:61], v[26:33], v[214:221], 0
	v_mfma_f32_16x16x128_f8f6f4 v[46:49], v[18:25], v[222:229], 0
	v_mfma_f32_16x16x128_f8f6f4 v[42:45], v[26:33], v[222:229], 0
	s_nop 3
	s_setprio 0
	s_setprio 1
	v_mfma_f32_16x16x128_f8f6f4 v[86:89], v[2:9], v[198:205], 0
	v_mfma_f32_16x16x128_f8f6f4 v[82:85], v[10:17], v[198:205], 0
	v_mfma_f32_16x16x128_f8f6f4 v[70:73], v[2:9], v[206:213], 0
	v_mfma_f32_16x16x128_f8f6f4 v[66:69], v[10:17], v[206:213], 0
	v_mfma_f32_16x16x128_f8f6f4 v[54:57], v[2:9], v[214:221], 0
	v_mfma_f32_16x16x128_f8f6f4 v[50:53], v[10:17], v[214:221], 0
	v_mfma_f32_16x16x128_f8f6f4 v[38:41], v[2:9], v[222:229], 0
	v_mfma_f32_16x16x128_f8f6f4 v[34:37], v[10:17], v[222:229], 0
	s_setprio 0
	s_barrier
	s_add_i32 s75, 0, 0x18000
	s_add_i32 s76, 0, 0x1c000
	v_add_u32_e32 v14, s75, v191
	v_add_u32_e32 v30, s76, v191
	ds_read_b128 v[2:5], v14
	ds_read_b128 v[6:9], v14 offset:1024
	ds_read_b128 v[10:13], v14 offset:2048
	ds_read_b128 v[14:17], v14 offset:3072
	ds_read_b128 v[18:21], v30
	ds_read_b128 v[22:25], v30 offset:1024
	ds_read_b128 v[26:29], v30 offset:2048
	ds_read_b128 v[30:33], v30 offset:3072
	s_mov_b32 m0, s50
	ds_read_b128 v[198:201], v194 offset:32768
	ds_read_b128 v[202:205], v194 offset:33792
	ds_read_b128 v[206:209], v194 offset:34816
	ds_read_b128 v[210:213], v194 offset:35840
	ds_read_b128 v[214:217], v194 offset:36864
	ds_read_b128 v[218:221], v194 offset:37888
	ds_read_b128 v[222:225], v194 offset:38912
	ds_read_b128 v[226:229], v194 offset:39936
	global_load_lds_dwordx4 v178, s[30:31]
	s_mov_b32 m0, s51
	s_nop 0
	global_load_lds_dwordx4 v180, s[30:31]
	s_waitcnt vmcnt(8)
	s_waitcnt lgkmcnt(0)
	s_setprio 1
	v_mfma_f32_16x16x128_f8f6f4 v[158:161], v[2:9], v[198:205], v[158:161]
	v_mfma_f32_16x16x128_f8f6f4 v[154:157], v[10:17], v[198:205], v[154:157]
	v_mfma_f32_16x16x128_f8f6f4 v[142:145], v[2:9], v[206:213], v[142:145]
	v_mfma_f32_16x16x128_f8f6f4 v[138:141], v[10:17], v[206:213], v[138:141]
	v_mfma_f32_16x16x128_f8f6f4 v[126:129], v[2:9], v[214:221], v[126:129]
	v_mfma_f32_16x16x128_f8f6f4 v[122:125], v[10:17], v[214:221], v[122:125]
	v_mfma_f32_16x16x128_f8f6f4 v[110:113], v[2:9], v[222:229], v[110:113]
	v_mfma_f32_16x16x128_f8f6f4 v[106:109], v[10:17], v[222:229], v[106:109]
	s_nop 3
	s_setprio 0
	s_setprio 1
	v_mfma_f32_16x16x128_f8f6f4 v[150:153], v[18:25], v[198:205], v[150:153]
	v_mfma_f32_16x16x128_f8f6f4 v[146:149], v[26:33], v[198:205], v[146:149]
	v_mfma_f32_16x16x128_f8f6f4 v[134:137], v[18:25], v[206:213], v[134:137]
	v_mfma_f32_16x16x128_f8f6f4 v[130:133], v[26:33], v[206:213], v[130:133]
	v_mfma_f32_16x16x128_f8f6f4 v[118:121], v[18:25], v[214:221], v[118:121]
	v_mfma_f32_16x16x128_f8f6f4 v[114:117], v[26:33], v[214:221], v[114:117]
	v_mfma_f32_16x16x128_f8f6f4 v[102:105], v[18:25], v[222:229], v[102:105]
	v_mfma_f32_16x16x128_f8f6f4 v[98:101], v[26:33], v[222:229], v[98:101]
	s_setprio 0
	s_barrier
; #define PG8_STAGE(bufoff, gbase, voff) do { _Pragma("unroll") for (int _i = 0; _i < 2; ++_i) \
;         __builtin_amdgcn_global_load_lds((const unsigned*)((const char*)(gbase) + (voff)[_i]), (PG8_LAS unsigned*)(lds + (bufoff) + ldsw + _i * 8192), 16, 0, 0); } while (0)
; #define PG8_WAIT_V(n) asm volatile("s_waitcnt vmcnt(" #n ")" ::: "memory")
; #define PG8_WAIT_L(n) asm volatile("s_waitcnt lgkmcnt(" #n ")" ::: "memory")
; template <class Epi, class Sched, bool ALIGN_EPI = true, bool F8 = false>
; __device__ __forceinline__ void gemm_phase(PG8_LAS unsigned char* lds, const Sched& S, const Epi& E) {
;     ...
;         for (int t = 0; t < nt; t += 2) {
;             const bool last = (t == nt - 2);
;             if constexpr (Sched::GATHER) { if (last && has_next) S.a_off(nxt, Rs, Cs, voffAn); }
;             const char* a1 = cA + (size_t)(t + 1) * kstep;
;             const char* a2 = last ? nA : cA + (size_t)(t + 2) * kstep; const char* b2 = last ? nB : cB + (size_t)(t + 2) * kstepB;
;             const char* a3 = a2 + kstep; const char* b3 = b2 + kstepB;
;             unsigned vA2[2][2];
; #pragma unroll
;             for (int h = 0; h < 2; ++h)
; #pragma unroll
;                 for (int i = 0; i < 2; ++i) { if constexpr (Sched::GATHER) vA2[h][i] = (last && has_next) ? voffAn[h][i] : voffA[h][i]; else vA2[h][i] = voffA[h][i]; }
;             PG8_LDB(B0, 0, 0); PG8_LDB(B1, 0, 1); PG8_SCHED; PG8_LDA(At, 0, 0); PG8_STAGE(PG8_SA(1, 1), a1, voffA[1]);
;             PG8_WAIT_V(8); PG8_WAIT_L(0); PG8_BAR; PG8_MMA(0, 0, At, B0); PG8_MMA(0, 1, At, B1); PG8_BAR; PG8_SCHED;
;             PG8_LDA(At, 0, 1); PG8_STAGE(PG8_SB(0, 0), b2, voffB[0]); PG8_STAGE(PG8_SB(0, 1), b2, voffB[1]); PG8_STAGE(PG8_SA(0, 0), a2, vA2[0]);
;             PG8_WAIT_V(8); PG8_WAIT_L(0); PG8_BAR; PG8_MMA(1, 0, At, B0); PG8_MMA(1, 1, At, B1); PG8_BAR; PG8_SCHED;
;             PG8_LDB(B0, 1, 0); PG8_LDB(B1, 1, 1); PG8_SCHED; PG8_LDA(At, 1, 0); PG8_STAGE(PG8_SA(0, 1), a2, vA2[1]);
;             PG8_WAIT_V(8); PG8_WAIT_L(0); PG8_BAR; PG8_MMA(0, 0, At, B0); PG8_MMA(0, 1, At, B1); PG8_BAR; PG8_SCHED;
;             PG8_LDA(At, 1, 1); PG8_STAGE(PG8_SB(1, 0), b3, voffB[0]); PG8_STAGE(PG8_SB(1, 1), b3, voffB[1]); PG8_STAGE(PG8_SA(1, 0), a3, vA2[0]);
;             PG8_WAIT_V(8); PG8_WAIT_L(0); PG8_BAR; PG8_MMA(1, 0, At, B0); PG8_MMA(1, 1, At, B1); PG8_BAR; PG8_SCHED;
	s_add_u32 s28, s28, 0x8000
	s_addc_u32 s29, s29, 0
	s_add_i32 s30, s75, s47
	s_mov_b32 m0, s30
	ds_read_b128 v[198:201], v194 offset:49152
	ds_read_b128 v[202:205], v194 offset:50176
	ds_read_b128 v[206:209], v194 offset:51200
	ds_read_b128 v[210:213], v194 offset:52224
	ds_read_b128 v[214:217], v194 offset:53248
	ds_read_b128 v[218:221], v194 offset:54272
	ds_read_b128 v[222:225], v194 offset:55296
	ds_read_b128 v[226:229], v194 offset:56320
	global_load_lds_dwordx4 v164, s[28:29]
	s_add_i32 m0, s30, 0x2000
	s_add_i32 s30, s76, s47
	global_load_lds_dwordx4 v166, s[28:29]
	s_mov_b32 m0, s30
	s_nop 0
	global_load_lds_dwordx4 v168, s[28:29]
	s_add_i32 m0, s30, 0x2000
	s_nop 0
	global_load_lds_dwordx4 v172, s[28:29]
	s_mov_b32 m0, s60
	s_nop 0
	global_load_lds_dwordx4 v174, s[26:27]
	s_mov_b32 m0, s61
	s_nop 0
	global_load_lds_dwordx4 v176, s[26:27]
	s_waitcnt vmcnt(8)
	s_waitcnt lgkmcnt(0)
	s_setprio 1
	v_mfma_f32_16x16x128_f8f6f4 v[94:97], v[2:9], v[198:205], v[94:97]
	v_mfma_f32_16x16x128_f8f6f4 v[90:93], v[10:17], v[198:205], v[90:93]
	v_mfma_f32_16x16x128_f8f6f4 v[78:81], v[2:9], v[206:213], v[78:81]
	v_mfma_f32_16x16x128_f8f6f4 v[74:77], v[10:17], v[206:213], v[74:77]
	v_mfma_f32_16x16x128_f8f6f4 v[62:65], v[2:9], v[214:221], v[62:65]
	v_mfma_f32_16x16x128_f8f6f4 v[58:61], v[10:17], v[214:221], v[58:61]
	v_mfma_f32_16x16x128_f8f6f4 v[46:49], v[2:9], v[222:229], v[46:49]
	v_mfma_f32_16x16x128_f8f6f4 v[42:45], v[10:17], v[222:229], v[42:45]
	s_nop 3
	s_setprio 0
	s_setprio 1
	v_mfma_f32_16x16x128_f8f6f4 v[86:89], v[18:25], v[198:205], v[86:89]
	v_mfma_f32_16x16x128_f8f6f4 v[82:85], v[26:33], v[198:205], v[82:85]
	v_mfma_f32_16x16x128_f8f6f4 v[70:73], v[18:25], v[206:213], v[70:73]
	v_mfma_f32_16x16x128_f8f6f4 v[66:69], v[26:33], v[206:213], v[66:69]
	v_mfma_f32_16x16x128_f8f6f4 v[54:57], v[18:25], v[214:221], v[54:57]
	v_mfma_f32_16x16x128_f8f6f4 v[50:53], v[26:33], v[214:221], v[50:53]
	v_mfma_f32_16x16x128_f8f6f4 v[38:41], v[18:25], v[222:229], v[38:41]
	v_mfma_f32_16x16x128_f8f6f4 v[34:37], v[26:33], v[222:229], v[34:37]
	s_setprio 0
	s_barrier
	s_add_i32 s74, s74, 2
	s_add_u32 s17, s17, 0x10000
	s_addc_u32 s19, s19, 0
	s_add_u32 s24, s24, 0x10000
	s_addc_u32 s25, s25, 0
	s_cmp_gt_u32 s74, 13
	s_cbranch_scc0 .LBB0_428
	s_branch .Lfx_11141
.LBB0_428:
	ds_read_b128 v[18:21], v192
	ds_read_b128 v[22:25], v192 offset:1024
	ds_read_b128 v[26:29], v192 offset:2048
	ds_read_b128 v[30:33], v192 offset:3072
	ds_read_b128 v[2:5], v193
	ds_read_b128 v[6:9], v193 offset:1024
	ds_read_b128 v[10:13], v193 offset:2048
	ds_read_b128 v[14:17], v193 offset:3072
	s_add_u32 s26, s24, 0x8000
	s_addc_u32 s27, s25, 0
	s_cmp_eq_u32 s74, 12
	s_cselect_b32 s30, s20, s26
	s_cselect_b32 s31, s21, s27
	s_cselect_b32 s28, s22, s17
	s_cselect_b32 s29, s23, s19
	s_add_u32 s26, s30, 0x8000
	s_addc_u32 s27, s31, 0
	s_add_i32 m0, s48, 0xc000
	ds_read_b128 v[198:201], v194
	ds_read_b128 v[202:205], v194 offset:1024
	ds_read_b128 v[206:209], v194 offset:2048
	ds_read_b128 v[210:213], v194 offset:3072
	ds_read_b128 v[214:217], v194 offset:4096
	ds_read_b128 v[218:221], v194 offset:5120
	ds_read_b128 v[222:225], v194 offset:6144
	ds_read_b128 v[226:229], v194 offset:7168
	global_load_lds_dwordx4 v184, s[24:25]
	s_add_i32 m0, s48, 0xe000
	s_nop 0
	global_load_lds_dwordx4 v182, s[24:25]
	s_waitcnt vmcnt(8)
	s_waitcnt lgkmcnt(0)
	s_setprio 1
	v_mfma_f32_16x16x128_f8f6f4 v[158:161], v[18:25], v[198:205], v[158:161]
	v_mfma_f32_16x16x128_f8f6f4 v[154:157], v[26:33], v[198:205], v[154:157]
	v_mfma_f32_16x16x128_f8f6f4 v[142:145], v[18:25], v[206:213], v[142:145]
	v_mfma_f32_16x16x128_f8f6f4 v[138:141], v[26:33], v[206:213], v[138:141]
	v_mfma_f32_16x16x128_f8f6f4 v[126:129], v[18:25], v[214:221], v[126:129]
	v_mfma_f32_16x16x128_f8f6f4 v[122:125], v[26:33], v[214:221], v[122:125]
	v_mfma_f32_16x16x128_f8f6f4 v[110:113], v[18:25], v[222:229], v[110:113]
	v_mfma_f32_16x16x128_f8f6f4 v[106:109], v[26:33], v[222:229], v[106:109]
	s_nop 3
	s_setprio 0
	s_setprio 1
	v_mfma_f32_16x16x128_f8f6f4 v[150:153], v[2:9], v[198:205], v[150:153]
	v_mfma_f32_16x16x128_f8f6f4 v[146:149], v[10:17], v[198:205], v[146:149]
	v_mfma_f32_16x16x128_f8f6f4 v[134:137], v[2:9], v[206:213], v[134:137]
	v_mfma_f32_16x16x128_f8f6f4 v[130:133], v[10:17], v[206:213], v[130:133]
	v_mfma_f32_16x16x128_f8f6f4 v[118:121], v[2:9], v[214:221], v[118:121]
	v_mfma_f32_16x16x128_f8f6f4 v[114:117], v[10:17], v[214:221], v[114:117]
	v_mfma_f32_16x16x128_f8f6f4 v[102:105], v[2:9], v[222:229], v[102:105]
	v_mfma_f32_16x16x128_f8f6f4 v[98:101], v[10:17], v[222:229], v[98:101]
	s_setprio 0
	s_barrier
; #define PG8_STAGE(bufoff, gbase, voff) do { _Pragma("unroll") for (int _i = 0; _i < 2; ++_i) \
;         __builtin_amdgcn_global_load_lds((const unsigned*)((const char*)(gbase) + (voff)[_i]), (PG8_LAS unsigned*)(lds + (bufoff) + ldsw + _i * 8192), 16, 0, 0); } while (0)
; #define PG8_WAIT_V(n) asm volatile("s_waitcnt vmcnt(" #n ")" ::: "memory")
; #define PG8_WAIT_L(n) asm volatile("s_waitcnt lgkmcnt(" #n ")" ::: "memory")
; #define PG8_BAR __builtin_amdgcn_s_barrier()
; #define PG8_SCHED __builtin_amdgcn_sched_barrier(0)
; template <class Epi, class Sched, bool ALIGN_EPI = true, bool F8 = false>
; __device__ __forceinline__ void gemm_phase(PG8_LAS unsigned char* lds, const Sched& S, const Epi& E) {
;     ...
;             PG8_LDA(At, 0, 1); PG8_STAGE(PG8_SB(0, 0), b2, voffB[0]); PG8_STAGE(PG8_SB(0, 1), b2, voffB[1]); PG8_STAGE(PG8_SA(0, 0), a2, vA2[0]);
;             PG8_WAIT_V(8); PG8_WAIT_L(0); PG8_BAR; PG8_MMA(1, 0, At, B0); PG8_MMA(1, 1, At, B1); PG8_BAR; PG8_SCHED;
;             PG8_LDB(B0, 1, 0); PG8_LDB(B1, 1, 1); PG8_SCHED; PG8_LDA(At, 1, 0); PG8_STAGE(PG8_SA(0, 1), a2, vA2[1]);
;             PG8_WAIT_V(8); PG8_WAIT_L(0); PG8_BAR; PG8_MMA(0, 0, At, B0); PG8_MMA(0, 1, At, B1); PG8_BAR; PG8_SCHED;
;             PG8_LDA(At, 1, 1); PG8_STAGE(PG8_SB(1, 0), b3, voffB[0]); PG8_STAGE(PG8_SB(1, 1), b3, voffB[1]); PG8_STAGE(PG8_SA(1, 0), a3, vA2[0]);
;             PG8_WAIT_V(8); PG8_WAIT_L(0); PG8_BAR; PG8_MMA(1, 0, At, B0); PG8_MMA(1, 1, At, B1); PG8_BAR; PG8_SCHED;
	s_add_i32 s75, s65, s47
	s_mov_b32 m0, s75
	ds_read_b128 v[198:201], v194 offset:16384
	ds_read_b128 v[202:205], v194 offset:17408
	ds_read_b128 v[206:209], v194 offset:18432
	ds_read_b128 v[210:213], v194 offset:19456
	ds_read_b128 v[214:217], v194 offset:20480
	ds_read_b128 v[218:221], v194 offset:21504
	ds_read_b128 v[222:225], v194 offset:22528
	ds_read_b128 v[226:229], v194 offset:23552
	global_load_lds_dwordx4 v164, s[28:29]
	s_add_i32 m0, s75, 0x2000
	s_add_i32 s75, s66, s47
	global_load_lds_dwordx4 v166, s[28:29]
	s_add_u32 s98, s28, s4
	s_addc_u32 s99, s29, s5
	s_mov_b32 m0, s75
	s_nop 0
	global_load_lds_dwordx4 v164, s[98:99]
	s_add_u32 s100, s28, s4
	s_addc_u32 s101, s29, s5
	s_add_i32 m0, s75, 0x2000
	s_nop 0
	global_load_lds_dwordx4 v166, s[100:101]
	s_mov_b32 m0, s48
	s_nop 0
	global_load_lds_dwordx4 v174, s[30:31]
	s_mov_b32 m0, s49
	s_nop 0
	global_load_lds_dwordx4 v176, s[30:31]
	s_waitcnt vmcnt(8)
	s_waitcnt lgkmcnt(0)
	s_setprio 1
	v_mfma_f32_16x16x128_f8f6f4 v[94:97], v[18:25], v[198:205], v[94:97]
	v_mfma_f32_16x16x128_f8f6f4 v[90:93], v[26:33], v[198:205], v[90:93]
	v_mfma_f32_16x16x128_f8f6f4 v[78:81], v[18:25], v[206:213], v[78:81]
	v_mfma_f32_16x16x128_f8f6f4 v[74:77], v[26:33], v[206:213], v[74:77]
	v_mfma_f32_16x16x128_f8f6f4 v[62:65], v[18:25], v[214:221], v[62:65]
	v_mfma_f32_16x16x128_f8f6f4 v[58:61], v[26:33], v[214:221], v[58:61]
	v_mfma_f32_16x16x128_f8f6f4 v[46:49], v[18:25], v[222:229], v[46:49]
	v_mfma_f32_16x16x128_f8f6f4 v[42:45], v[26:33], v[222:229], v[42:45]
	s_nop 3
	s_setprio 0
	s_setprio 1
	v_mfma_f32_16x16x128_f8f6f4 v[86:89], v[2:9], v[198:205], v[86:89]
	v_mfma_f32_16x16x128_f8f6f4 v[82:85], v[10:17], v[198:205], v[82:85]
	v_mfma_f32_16x16x128_f8f6f4 v[70:73], v[2:9], v[206:213], v[70:73]
	v_mfma_f32_16x16x128_f8f6f4 v[66:69], v[10:17], v[206:213], v[66:69]
	v_mfma_f32_16x16x128_f8f6f4 v[54:57], v[2:9], v[214:221], v[54:57]
	v_mfma_f32_16x16x128_f8f6f4 v[50:53], v[10:17], v[214:221], v[50:53]
	v_mfma_f32_16x16x128_f8f6f4 v[38:41], v[2:9], v[222:229], v[38:41]
	v_mfma_f32_16x16x128_f8f6f4 v[34:37], v[10:17], v[222:229], v[34:37]
	s_setprio 0
	s_barrier
	s_add_i32 s75, 0, 0x18000
	s_add_i32 s76, 0, 0x1c000
	v_add_u32_e32 v14, s75, v191
	v_add_u32_e32 v30, s76, v191
	ds_read_b128 v[2:5], v14
	ds_read_b128 v[6:9], v14 offset:1024
	ds_read_b128 v[10:13], v14 offset:2048
	ds_read_b128 v[14:17], v14 offset:3072
	ds_read_b128 v[18:21], v30
	ds_read_b128 v[22:25], v30 offset:1024
	ds_read_b128 v[26:29], v30 offset:2048
	ds_read_b128 v[30:33], v30 offset:3072
	s_mov_b32 m0, s50
	ds_read_b128 v[198:201], v194 offset:32768
	ds_read_b128 v[202:205], v194 offset:33792
	ds_read_b128 v[206:209], v194 offset:34816
	ds_read_b128 v[210:213], v194 offset:35840
	ds_read_b128 v[214:217], v194 offset:36864
	ds_read_b128 v[218:221], v194 offset:37888
	ds_read_b128 v[222:225], v194 offset:38912
	ds_read_b128 v[226:229], v194 offset:39936
	global_load_lds_dwordx4 v178, s[30:31]
	s_mov_b32 m0, s51
	s_nop 0
	global_load_lds_dwordx4 v180, s[30:31]
	s_waitcnt vmcnt(8)
	s_waitcnt lgkmcnt(0)
	s_setprio 1
	v_mfma_f32_16x16x128_f8f6f4 v[158:161], v[2:9], v[198:205], v[158:161]
	v_mfma_f32_16x16x128_f8f6f4 v[154:157], v[10:17], v[198:205], v[154:157]
	v_mfma_f32_16x16x128_f8f6f4 v[142:145], v[2:9], v[206:213], v[142:145]
	v_mfma_f32_16x16x128_f8f6f4 v[138:141], v[10:17], v[206:213], v[138:141]
	v_mfma_f32_16x16x128_f8f6f4 v[126:129], v[2:9], v[214:221], v[126:129]
	v_mfma_f32_16x16x128_f8f6f4 v[122:125], v[10:17], v[214:221], v[122:125]
	v_mfma_f32_16x16x128_f8f6f4 v[110:113], v[2:9], v[222:229], v[110:113]
	v_mfma_f32_16x16x128_f8f6f4 v[106:109], v[10:17], v[222:229], v[106:109]
	s_nop 3
	s_setprio 0
	s_setprio 1
	v_mfma_f32_16x16x128_f8f6f4 v[150:153], v[18:25], v[198:205], v[150:153]
	v_mfma_f32_16x16x128_f8f6f4 v[146:149], v[26:33], v[198:205], v[146:149]
	v_mfma_f32_16x16x128_f8f6f4 v[134:137], v[18:25], v[206:213], v[134:137]
	v_mfma_f32_16x16x128_f8f6f4 v[130:133], v[26:33], v[206:213], v[130:133]
	v_mfma_f32_16x16x128_f8f6f4 v[118:121], v[18:25], v[214:221], v[118:121]
	v_mfma_f32_16x16x128_f8f6f4 v[114:117], v[26:33], v[214:221], v[114:117]
	v_mfma_f32_16x16x128_f8f6f4 v[102:105], v[18:25], v[222:229], v[102:105]
	v_mfma_f32_16x16x128_f8f6f4 v[98:101], v[26:33], v[222:229], v[98:101]
	s_setprio 0
	s_barrier
	s_add_u32 s28, s28, 0x8000
	s_addc_u32 s29, s29, 0
	s_add_i32 s30, s75, s47
	s_mov_b32 m0, s30
	ds_read_b128 v[198:201], v194 offset:49152
	ds_read_b128 v[202:205], v194 offset:50176
	ds_read_b128 v[206:209], v194 offset:51200
	ds_read_b128 v[210:213], v194 offset:52224
	ds_read_b128 v[214:217], v194 offset:53248
	ds_read_b128 v[218:221], v194 offset:54272
	ds_read_b128 v[222:225], v194 offset:55296
	ds_read_b128 v[226:229], v194 offset:56320
	global_load_lds_dwordx4 v164, s[28:29]
	s_add_i32 m0, s30, 0x2000
	s_add_i32 s30, s76, s47
	global_load_lds_dwordx4 v166, s[28:29]
	s_mov_b32 m0, s30
	s_nop 0
	global_load_lds_dwordx4 v168, s[28:29]
	s_add_i32 m0, s30, 0x2000
	s_nop 0
	global_load_lds_dwordx4 v172, s[28:29]
	s_mov_b32 m0, s60
	s_nop 0
	global_load_lds_dwordx4 v174, s[26:27]
	s_mov_b32 m0, s61
	s_nop 0
	global_load_lds_dwordx4 v176, s[26:27]
	s_waitcnt vmcnt(8)
	s_waitcnt lgkmcnt(0)
	s_setprio 1
	v_mfma_f32_16x16x128_f8f6f4 v[94:97], v[2:9], v[198:205], v[94:97]
	v_mfma_f32_16x16x128_f8f6f4 v[90:93], v[10:17], v[198:205], v[90:93]
	v_mfma_f32_16x16x128_f8f6f4 v[78:81], v[2:9], v[206:213], v[78:81]
	v_mfma_f32_16x16x128_f8f6f4 v[74:77], v[10:17], v[206:213], v[74:77]
	v_mfma_f32_16x16x128_f8f6f4 v[62:65], v[2:9], v[214:221], v[62:65]
	v_mfma_f32_16x16x128_f8f6f4 v[58:61], v[10:17], v[214:221], v[58:61]
	v_mfma_f32_16x16x128_f8f6f4 v[46:49], v[2:9], v[222:229], v[46:49]
	v_mfma_f32_16x16x128_f8f6f4 v[42:45], v[10:17], v[222:229], v[42:45]
	s_nop 3
	s_setprio 0
	s_setprio 1
	v_mfma_f32_16x16x128_f8f6f4 v[86:89], v[18:25], v[198:205], v[86:89]
	v_mfma_f32_16x16x128_f8f6f4 v[82:85], v[26:33], v[198:205], v[82:85]
	v_mfma_f32_16x16x128_f8f6f4 v[70:73], v[18:25], v[206:213], v[70:73]
	v_mfma_f32_16x16x128_f8f6f4 v[66:69], v[26:33], v[206:213], v[66:69]
	v_mfma_f32_16x16x128_f8f6f4 v[54:57], v[18:25], v[214:221], v[54:57]
	v_mfma_f32_16x16x128_f8f6f4 v[50:53], v[26:33], v[214:221], v[50:53]
	v_mfma_f32_16x16x128_f8f6f4 v[38:41], v[18:25], v[222:229], v[38:41]
	v_mfma_f32_16x16x128_f8f6f4 v[34:37], v[26:33], v[222:229], v[34:37]
	s_setprio 0
	s_barrier
	s_add_i32 s74, s74, 2
	s_add_u32 s17, s17, 0x10000
	s_addc_u32 s19, s19, 0
	s_add_u32 s24, s24, 0x10000
	s_addc_u32 s25, s25, 0
	s_cmp_gt_u32 s74, 13
	s_cbranch_scc0 .LBB0_428
	s_branch .Lfx_11141
; #define PG8_STAGE(bufoff, gbase, voff) do { _Pragma("unroll") for (int _i = 0; _i < 2; ++_i) \
;         __builtin_amdgcn_global_load_lds((const unsigned*)((const char*)(gbase) + (voff)[_i]), (PG8_LAS unsigned*)(lds + (bufoff) + ldsw + _i * 8192), 16, 0, 0); } while (0)
; #define PG8_WAIT_V(n) asm volatile("s_waitcnt vmcnt(" #n ")" ::: "memory")
; #define PG8_WAIT_L(n) asm volatile("s_waitcnt lgkmcnt(" #n ")" ::: "memory")
; #define PG8_BAR __builtin_amdgcn_s_barrier()
; #define PG8_SCHED __builtin_amdgcn_sched_barrier(0)
; template <class Epi, class Sched, bool ALIGN_EPI = true, bool F8 = false>
; __device__ __forceinline__ void gemm_phase(PG8_LAS unsigned char* lds, const Sched& S, const Epi& E) {
;     ...
;     f32x4 acc[2][2][4][2];
; #pragma unroll
;     for (int a = 0; a < 2; ++a)
; #pragma unroll
;         for (int b = 0; b < 2; ++b)
; #pragma unroll
;             for (int m = 0; m < 4; ++m)
; #pragma unroll
;                 for (int n = 0; n < 2; ++n) acc[a][b][m][n] = (f32x4){0.f, 0.f, 0.f, 0.f};
;     ...
;             PG8_LDB(B0, 0, 0); PG8_LDB(B1, 0, 1); PG8_SCHED; PG8_LDA(At, 0, 0); PG8_STAGE(PG8_SA(1, 1), a1, voffA[1]);
;             PG8_WAIT_V(8); PG8_WAIT_L(0); PG8_BAR; PG8_MMA(0, 0, At, B0); PG8_MMA(0, 1, At, B1); PG8_BAR; PG8_SCHED;
;             PG8_LDA(At, 0, 1); PG8_STAGE(PG8_SB(0, 0), b2, voffB[0]); PG8_STAGE(PG8_SB(0, 1), b2, voffB[1]); PG8_STAGE(PG8_SA(0, 0), a2, vA2[0]);
;             PG8_WAIT_V(8); PG8_WAIT_L(0); PG8_BAR; PG8_MMA(1, 0, At, B0); PG8_MMA(1, 1, At, B1); PG8_BAR; PG8_SCHED;
;             PG8_LDB(B0, 1, 0); PG8_LDB(B1, 1, 1); PG8_SCHED; PG8_LDA(At, 1, 0); PG8_STAGE(PG8_SA(0, 1), a2, vA2[1]);
;             PG8_WAIT_V(8); PG8_WAIT_L(0); PG8_BAR; PG8_MMA(0, 0, At, B0); PG8_MMA(0, 1, At, B1); PG8_BAR; PG8_SCHED;
.Lh1e_11141:
.Lpk1_428:
	ds_read_b128 v[18:21], v192
	ds_read_b128 v[22:25], v192 offset:1024
	ds_read_b128 v[26:29], v192 offset:2048
	ds_read_b128 v[30:33], v192 offset:3072
	ds_read_b128 v[2:5], v193
	ds_read_b128 v[6:9], v193 offset:1024
	ds_read_b128 v[10:13], v193 offset:2048
	ds_read_b128 v[14:17], v193 offset:3072
	s_add_u32 s26, s24, 0x8000
	s_addc_u32 s27, s25, 0
	s_cmp_eq_u32 s74, 12
	s_cselect_b32 s30, s20, s26
	s_cselect_b32 s31, s21, s27
	s_cselect_b32 s28, s22, s17
	s_cselect_b32 s29, s23, s19
	s_add_u32 s26, s30, 0x8000
	s_addc_u32 s27, s31, 0
	s_add_i32 m0, s48, 0xc000
	ds_read_b128 v[198:201], v194
	ds_read_b128 v[202:205], v194 offset:1024
	ds_read_b128 v[206:209], v194 offset:2048
	ds_read_b128 v[210:213], v194 offset:3072
	ds_read_b128 v[214:217], v194 offset:4096
	ds_read_b128 v[218:221], v194 offset:5120
	ds_read_b128 v[222:225], v194 offset:6144
	ds_read_b128 v[226:229], v194 offset:7168
	global_load_lds_dwordx4 v184, s[24:25]
	s_add_i32 m0, s48, 0xe000
	s_nop 0
	global_load_lds_dwordx4 v182, s[24:25]
	s_waitcnt vmcnt(8)
	s_waitcnt lgkmcnt(0)
	s_barrier
	s_setprio 2
	v_mfma_f32_16x16x128_f8f6f4 v[158:161], v[18:25], v[198:205], 0
	v_mfma_f32_16x16x128_f8f6f4 v[154:157], v[26:33], v[198:205], 0
	v_mfma_f32_16x16x128_f8f6f4 v[142:145], v[18:25], v[206:213], 0
	v_mfma_f32_16x16x128_f8f6f4 v[138:141], v[26:33], v[206:213], 0
	v_mfma_f32_16x16x128_f8f6f4 v[126:129], v[18:25], v[214:221], 0
	v_mfma_f32_16x16x128_f8f6f4 v[122:125], v[26:33], v[214:221], 0
	v_mfma_f32_16x16x128_f8f6f4 v[110:113], v[18:25], v[222:229], 0
	v_mfma_f32_16x16x128_f8f6f4 v[106:109], v[26:33], v[222:229], 0
	s_nop 3
	s_setprio 0
	s_setprio 2
	v_mfma_f32_16x16x128_f8f6f4 v[150:153], v[2:9], v[198:205], 0
	v_mfma_f32_16x16x128_f8f6f4 v[146:149], v[10:17], v[198:205], 0
	v_mfma_f32_16x16x128_f8f6f4 v[134:137], v[2:9], v[206:213], 0
	v_mfma_f32_16x16x128_f8f6f4 v[130:133], v[10:17], v[206:213], 0
	v_mfma_f32_16x16x128_f8f6f4 v[118:121], v[2:9], v[214:221], 0
	v_mfma_f32_16x16x128_f8f6f4 v[114:117], v[10:17], v[214:221], 0
	v_mfma_f32_16x16x128_f8f6f4 v[102:105], v[2:9], v[222:229], 0
	v_mfma_f32_16x16x128_f8f6f4 v[98:101], v[10:17], v[222:229], 0
	s_setprio 0
	s_add_i32 s75, s65, s47
	s_mov_b32 m0, s75
	ds_read_b128 v[198:201], v194 offset:16384
	ds_read_b128 v[202:205], v194 offset:17408
	ds_read_b128 v[206:209], v194 offset:18432
	ds_read_b128 v[210:213], v194 offset:19456
	ds_read_b128 v[214:217], v194 offset:20480
	ds_read_b128 v[218:221], v194 offset:21504
	ds_read_b128 v[222:225], v194 offset:22528
	ds_read_b128 v[226:229], v194 offset:23552
	global_load_lds_dwordx4 v164, s[28:29]
	s_add_i32 m0, s75, 0x2000
	s_add_i32 s75, s66, s47
	global_load_lds_dwordx4 v166, s[28:29]
	s_add_u32 s98, s28, s4
	s_addc_u32 s99, s29, s5
	s_mov_b32 m0, s75
	s_nop 0
	global_load_lds_dwordx4 v164, s[98:99]
	s_add_u32 s100, s28, s4
	s_addc_u32 s101, s29, s5
	s_add_i32 m0, s75, 0x2000
	s_nop 0
	global_load_lds_dwordx4 v166, s[100:101]
	s_mov_b32 m0, s48
	s_nop 0
	global_load_lds_dwordx4 v174, s[30:31]
	s_mov_b32 m0, s49
	s_nop 0
	global_load_lds_dwordx4 v176, s[30:31]
	s_waitcnt vmcnt(8)
	s_waitcnt lgkmcnt(0)
	s_barrier
	s_setprio 2
	v_mfma_f32_16x16x128_f8f6f4 v[94:97], v[18:25], v[198:205], 0
	v_mfma_f32_16x16x128_f8f6f4 v[90:93], v[26:33], v[198:205], 0
	v_mfma_f32_16x16x128_f8f6f4 v[78:81], v[18:25], v[206:213], 0
	v_mfma_f32_16x16x128_f8f6f4 v[74:77], v[26:33], v[206:213], 0
	v_mfma_f32_16x16x128_f8f6f4 v[62:65], v[18:25], v[214:221], 0
	v_mfma_f32_16x16x128_f8f6f4 v[58:61], v[26:33], v[214:221], 0
	v_mfma_f32_16x16x128_f8f6f4 v[46:49], v[18:25], v[222:229], 0
	v_mfma_f32_16x16x128_f8f6f4 v[42:45], v[26:33], v[222:229], 0
	s_nop 3
	s_setprio 0
	s_setprio 2
	v_mfma_f32_16x16x128_f8f6f4 v[86:89], v[2:9], v[198:205], 0
	v_mfma_f32_16x16x128_f8f6f4 v[82:85], v[10:17], v[198:205], 0
	v_mfma_f32_16x16x128_f8f6f4 v[70:73], v[2:9], v[206:213], 0
	v_mfma_f32_16x16x128_f8f6f4 v[66:69], v[10:17], v[206:213], 0
	v_mfma_f32_16x16x128_f8f6f4 v[54:57], v[2:9], v[214:221], 0
	v_mfma_f32_16x16x128_f8f6f4 v[50:53], v[10:17], v[214:221], 0
	v_mfma_f32_16x16x128_f8f6f4 v[38:41], v[2:9], v[222:229], 0
	v_mfma_f32_16x16x128_f8f6f4 v[34:37], v[10:17], v[222:229], 0
	s_setprio 0
	s_add_i32 s75, 0, 0x18000
	s_add_i32 s76, 0, 0x1c000
	v_add_u32_e32 v14, s75, v191
	v_add_u32_e32 v30, s76, v191
	ds_read_b128 v[2:5], v14
	ds_read_b128 v[6:9], v14 offset:1024
	ds_read_b128 v[10:13], v14 offset:2048
	ds_read_b128 v[14:17], v14 offset:3072
	ds_read_b128 v[18:21], v30
	ds_read_b128 v[22:25], v30 offset:1024
	ds_read_b128 v[26:29], v30 offset:2048
	ds_read_b128 v[30:33], v30 offset:3072
	s_mov_b32 m0, s50
	ds_read_b128 v[198:201], v194 offset:32768
	ds_read_b128 v[202:205], v194 offset:33792
	ds_read_b128 v[206:209], v194 offset:34816
	ds_read_b128 v[210:213], v194 offset:35840
	ds_read_b128 v[214:217], v194 offset:36864
	ds_read_b128 v[218:221], v194 offset:37888
	ds_read_b128 v[222:225], v194 offset:38912
	ds_read_b128 v[226:229], v194 offset:39936
	global_load_lds_dwordx4 v178, s[30:31]
	s_mov_b32 m0, s51
	s_nop 0
	global_load_lds_dwordx4 v180, s[30:31]
	s_waitcnt vmcnt(8)
	s_waitcnt lgkmcnt(0)
	s_barrier
; #define PG8_STAGE(bufoff, gbase, voff) do { _Pragma("unroll") for (int _i = 0; _i < 2; ++_i) \
;         __builtin_amdgcn_global_load_lds((const unsigned*)((const char*)(gbase) + (voff)[_i]), (PG8_LAS unsigned*)(lds + (bufoff) + ldsw + _i * 8192), 16, 0, 0); } while (0)
; #define PG8_WAIT_V(n) asm volatile("s_waitcnt vmcnt(" #n ")" ::: "memory")
; #define PG8_WAIT_L(n) asm volatile("s_waitcnt lgkmcnt(" #n ")" ::: "memory")
; template <class Epi, class Sched, bool ALIGN_EPI = true, bool F8 = false>
; __device__ __forceinline__ void gemm_phase(PG8_LAS unsigned char* lds, const Sched& S, const Epi& E) {
;     ...
;         for (int t = 0; t < nt; t += 2) {
;             const bool last = (t == nt - 2);
;             if constexpr (Sched::GATHER) { if (last && has_next) S.a_off(nxt, Rs, Cs, voffAn); }
;             const char* a1 = cA + (size_t)(t + 1) * kstep;
;             const char* a2 = last ? nA : cA + (size_t)(t + 2) * kstep; const char* b2 = last ? nB : cB + (size_t)(t + 2) * kstepB;
;             const char* a3 = a2 + kstep; const char* b3 = b2 + kstepB;
;             unsigned vA2[2][2];
; #pragma unroll
;             for (int h = 0; h < 2; ++h)
; #pragma unroll
;                 for (int i = 0; i < 2; ++i) { if constexpr (Sched::GATHER) vA2[h][i] = (last && has_next) ? voffAn[h][i] : voffA[h][i]; else vA2[h][i] = voffA[h][i]; }
;             PG8_LDB(B0, 0, 0); PG8_LDB(B1, 0, 1); PG8_SCHED; PG8_LDA(At, 0, 0); PG8_STAGE(PG8_SA(1, 1), a1, voffA[1]);
;             PG8_WAIT_V(8); PG8_WAIT_L(0); PG8_BAR; PG8_MMA(0, 0, At, B0); PG8_MMA(0, 1, At, B1); PG8_BAR; PG8_SCHED;
;             PG8_LDA(At, 0, 1); PG8_STAGE(PG8_SB(0, 0), b2, voffB[0]); PG8_STAGE(PG8_SB(0, 1), b2, voffB[1]); PG8_STAGE(PG8_SA(0, 0), a2, vA2[0]);
;             PG8_WAIT_V(8); PG8_WAIT_L(0); PG8_BAR; PG8_MMA(1, 0, At, B0); PG8_MMA(1, 1, At, B1); PG8_BAR; PG8_SCHED;
;             PG8_LDB(B0, 1, 0); PG8_LDB(B1, 1, 1); PG8_SCHED; PG8_LDA(At, 1, 0); PG8_STAGE(PG8_SA(0, 1), a2, vA2[1]);
;             PG8_WAIT_V(8); PG8_WAIT_L(0); PG8_BAR; PG8_MMA(0, 0, At, B0); PG8_MMA(0, 1, At, B1); PG8_BAR; PG8_SCHED;
;             PG8_LDA(At, 1, 1); PG8_STAGE(PG8_SB(1, 0), b3, voffB[0]); PG8_STAGE(PG8_SB(1, 1), b3, voffB[1]); PG8_STAGE(PG8_SA(1, 0), a3, vA2[0]);
;             PG8_WAIT_V(8); PG8_WAIT_L(0); PG8_BAR; PG8_MMA(1, 0, At, B0); PG8_MMA(1, 1, At, B1); PG8_BAR; PG8_SCHED;
	s_setprio 2
	v_mfma_f32_16x16x128_f8f6f4 v[158:161], v[2:9], v[198:205], v[158:161]
	v_mfma_f32_16x16x128_f8f6f4 v[154:157], v[10:17], v[198:205], v[154:157]
	v_mfma_f32_16x16x128_f8f6f4 v[142:145], v[2:9], v[206:213], v[142:145]
	v_mfma_f32_16x16x128_f8f6f4 v[138:141], v[10:17], v[206:213], v[138:141]
	v_mfma_f32_16x16x128_f8f6f4 v[126:129], v[2:9], v[214:221], v[126:129]
	v_mfma_f32_16x16x128_f8f6f4 v[122:125], v[10:17], v[214:221], v[122:125]
	v_mfma_f32_16x16x128_f8f6f4 v[110:113], v[2:9], v[222:229], v[110:113]
	v_mfma_f32_16x16x128_f8f6f4 v[106:109], v[10:17], v[222:229], v[106:109]
	s_nop 3
	s_setprio 0
	s_setprio 2
	v_mfma_f32_16x16x128_f8f6f4 v[150:153], v[18:25], v[198:205], v[150:153]
	v_mfma_f32_16x16x128_f8f6f4 v[146:149], v[26:33], v[198:205], v[146:149]
	v_mfma_f32_16x16x128_f8f6f4 v[134:137], v[18:25], v[206:213], v[134:137]
	v_mfma_f32_16x16x128_f8f6f4 v[130:133], v[26:33], v[206:213], v[130:133]
	v_mfma_f32_16x16x128_f8f6f4 v[118:121], v[18:25], v[214:221], v[118:121]
	v_mfma_f32_16x16x128_f8f6f4 v[114:117], v[26:33], v[214:221], v[114:117]
	v_mfma_f32_16x16x128_f8f6f4 v[102:105], v[18:25], v[222:229], v[102:105]
	v_mfma_f32_16x16x128_f8f6f4 v[98:101], v[26:33], v[222:229], v[98:101]
	s_setprio 0
	s_add_u32 s28, s28, 0x8000
	s_addc_u32 s29, s29, 0
	s_add_i32 s30, s75, s47
	s_mov_b32 m0, s30
	ds_read_b128 v[198:201], v194 offset:49152
	ds_read_b128 v[202:205], v194 offset:50176
	ds_read_b128 v[206:209], v194 offset:51200
	ds_read_b128 v[210:213], v194 offset:52224
	ds_read_b128 v[214:217], v194 offset:53248
	ds_read_b128 v[218:221], v194 offset:54272
	ds_read_b128 v[222:225], v194 offset:55296
	ds_read_b128 v[226:229], v194 offset:56320
	global_load_lds_dwordx4 v164, s[28:29]
	s_add_i32 m0, s30, 0x2000
	s_add_i32 s30, s76, s47
	global_load_lds_dwordx4 v166, s[28:29]
	s_mov_b32 m0, s30
	s_nop 0
	global_load_lds_dwordx4 v168, s[28:29]
	s_add_i32 m0, s30, 0x2000
	s_nop 0
	global_load_lds_dwordx4 v172, s[28:29]
	s_mov_b32 m0, s60
	s_nop 0
	global_load_lds_dwordx4 v174, s[26:27]
	s_mov_b32 m0, s61
	s_nop 0
	global_load_lds_dwordx4 v176, s[26:27]
	s_waitcnt vmcnt(8)
	s_waitcnt lgkmcnt(0)
	s_barrier
	s_setprio 2
	v_mfma_f32_16x16x128_f8f6f4 v[94:97], v[2:9], v[198:205], v[94:97]
	v_mfma_f32_16x16x128_f8f6f4 v[90:93], v[10:17], v[198:205], v[90:93]
	v_mfma_f32_16x16x128_f8f6f4 v[78:81], v[2:9], v[206:213], v[78:81]
	v_mfma_f32_16x16x128_f8f6f4 v[74:77], v[10:17], v[206:213], v[74:77]
	v_mfma_f32_16x16x128_f8f6f4 v[62:65], v[2:9], v[214:221], v[62:65]
	v_mfma_f32_16x16x128_f8f6f4 v[58:61], v[10:17], v[214:221], v[58:61]
	v_mfma_f32_16x16x128_f8f6f4 v[46:49], v[2:9], v[222:229], v[46:49]
	v_mfma_f32_16x16x128_f8f6f4 v[42:45], v[10:17], v[222:229], v[42:45]
	s_nop 3
	s_setprio 0
	s_setprio 2
	v_mfma_f32_16x16x128_f8f6f4 v[86:89], v[18:25], v[198:205], v[86:89]
	v_mfma_f32_16x16x128_f8f6f4 v[82:85], v[26:33], v[198:205], v[82:85]
	v_mfma_f32_16x16x128_f8f6f4 v[70:73], v[18:25], v[206:213], v[70:73]
	v_mfma_f32_16x16x128_f8f6f4 v[66:69], v[26:33], v[206:213], v[66:69]
	v_mfma_f32_16x16x128_f8f6f4 v[54:57], v[18:25], v[214:221], v[54:57]
	v_mfma_f32_16x16x128_f8f6f4 v[50:53], v[26:33], v[214:221], v[50:53]
	v_mfma_f32_16x16x128_f8f6f4 v[38:41], v[18:25], v[222:229], v[38:41]
	v_mfma_f32_16x16x128_f8f6f4 v[34:37], v[26:33], v[222:229], v[34:37]
	s_setprio 0
	s_add_i32 s74, s74, 2
	s_add_u32 s17, s17, 0x10000
	s_addc_u32 s19, s19, 0
	s_add_u32 s24, s24, 0x10000
	s_addc_u32 s25, s25, 0
	s_cmp_gt_u32 s74, 13
	s_cbranch_scc0 .Lh1_428
	s_branch .Lfx_11141
.Lh1_428:
	ds_read_b128 v[18:21], v192
	ds_read_b128 v[22:25], v192 offset:1024
	ds_read_b128 v[26:29], v192 offset:2048
	ds_read_b128 v[30:33], v192 offset:3072
	ds_read_b128 v[2:5], v193
	ds_read_b128 v[6:9], v193 offset:1024
	ds_read_b128 v[10:13], v193 offset:2048
	ds_read_b128 v[14:17], v193 offset:3072
	s_add_u32 s26, s24, 0x8000
	s_addc_u32 s27, s25, 0
	s_cmp_eq_u32 s74, 12
	s_cselect_b32 s30, s20, s26
	s_cselect_b32 s31, s21, s27
	s_cselect_b32 s28, s22, s17
	s_cselect_b32 s29, s23, s19
	s_add_u32 s26, s30, 0x8000
	s_addc_u32 s27, s31, 0
	s_add_i32 m0, s48, 0xc000
	ds_read_b128 v[198:201], v194
	ds_read_b128 v[202:205], v194 offset:1024
	ds_read_b128 v[206:209], v194 offset:2048
	ds_read_b128 v[210:213], v194 offset:3072
	ds_read_b128 v[214:217], v194 offset:4096
	ds_read_b128 v[218:221], v194 offset:5120
	ds_read_b128 v[222:225], v194 offset:6144
	ds_read_b128 v[226:229], v194 offset:7168
	global_load_lds_dwordx4 v184, s[24:25]
	s_add_i32 m0, s48, 0xe000
	s_nop 0
	global_load_lds_dwordx4 v182, s[24:25]
	s_waitcnt vmcnt(8)
	s_waitcnt lgkmcnt(0)
	s_barrier
; #define PG8_STAGE(bufoff, gbase, voff) do { _Pragma("unroll") for (int _i = 0; _i < 2; ++_i) \
;         __builtin_amdgcn_global_load_lds((const unsigned*)((const char*)(gbase) + (voff)[_i]), (PG8_LAS unsigned*)(lds + (bufoff) + ldsw + _i * 8192), 16, 0, 0); } while (0)
; #define PG8_WAIT_V(n) asm volatile("s_waitcnt vmcnt(" #n ")" ::: "memory")
; #define PG8_WAIT_L(n) asm volatile("s_waitcnt lgkmcnt(" #n ")" ::: "memory")
; #define PG8_BAR __builtin_amdgcn_s_barrier()
; #define PG8_SCHED __builtin_amdgcn_sched_barrier(0)
; template <class Epi, class Sched, bool ALIGN_EPI = true, bool F8 = false>
; __device__ __forceinline__ void gemm_phase(PG8_LAS unsigned char* lds, const Sched& S, const Epi& E) {
;     ...
;             PG8_WAIT_V(8); PG8_WAIT_L(0); PG8_BAR; PG8_MMA(0, 0, At, B0); PG8_MMA(0, 1, At, B1); PG8_BAR; PG8_SCHED;
;             PG8_LDA(At, 0, 1); PG8_STAGE(PG8_SB(0, 0), b2, voffB[0]); PG8_STAGE(PG8_SB(0, 1), b2, voffB[1]); PG8_STAGE(PG8_SA(0, 0), a2, vA2[0]);
;             PG8_WAIT_V(8); PG8_WAIT_L(0); PG8_BAR; PG8_MMA(1, 0, At, B0); PG8_MMA(1, 1, At, B1); PG8_BAR; PG8_SCHED;
;             PG8_LDB(B0, 1, 0); PG8_LDB(B1, 1, 1); PG8_SCHED; PG8_LDA(At, 1, 0); PG8_STAGE(PG8_SA(0, 1), a2, vA2[1]);
;             PG8_WAIT_V(8); PG8_WAIT_L(0); PG8_BAR; PG8_MMA(0, 0, At, B0); PG8_MMA(0, 1, At, B1); PG8_BAR; PG8_SCHED;
	s_setprio 2
	v_mfma_f32_16x16x128_f8f6f4 v[158:161], v[18:25], v[198:205], v[158:161]
	v_mfma_f32_16x16x128_f8f6f4 v[154:157], v[26:33], v[198:205], v[154:157]
	v_mfma_f32_16x16x128_f8f6f4 v[142:145], v[18:25], v[206:213], v[142:145]
	v_mfma_f32_16x16x128_f8f6f4 v[138:141], v[26:33], v[206:213], v[138:141]
	v_mfma_f32_16x16x128_f8f6f4 v[126:129], v[18:25], v[214:221], v[126:129]
	v_mfma_f32_16x16x128_f8f6f4 v[122:125], v[26:33], v[214:221], v[122:125]
	v_mfma_f32_16x16x128_f8f6f4 v[110:113], v[18:25], v[222:229], v[110:113]
	v_mfma_f32_16x16x128_f8f6f4 v[106:109], v[26:33], v[222:229], v[106:109]
	s_nop 3
	s_setprio 0
	s_setprio 2
	v_mfma_f32_16x16x128_f8f6f4 v[150:153], v[2:9], v[198:205], v[150:153]
	v_mfma_f32_16x16x128_f8f6f4 v[146:149], v[10:17], v[198:205], v[146:149]
	v_mfma_f32_16x16x128_f8f6f4 v[134:137], v[2:9], v[206:213], v[134:137]
	v_mfma_f32_16x16x128_f8f6f4 v[130:133], v[10:17], v[206:213], v[130:133]
	v_mfma_f32_16x16x128_f8f6f4 v[118:121], v[2:9], v[214:221], v[118:121]
	v_mfma_f32_16x16x128_f8f6f4 v[114:117], v[10:17], v[214:221], v[114:117]
	v_mfma_f32_16x16x128_f8f6f4 v[102:105], v[2:9], v[222:229], v[102:105]
	v_mfma_f32_16x16x128_f8f6f4 v[98:101], v[10:17], v[222:229], v[98:101]
	s_setprio 0
	s_add_i32 s75, s65, s47
	s_mov_b32 m0, s75
	ds_read_b128 v[198:201], v194 offset:16384
	ds_read_b128 v[202:205], v194 offset:17408
	ds_read_b128 v[206:209], v194 offset:18432
	ds_read_b128 v[210:213], v194 offset:19456
	ds_read_b128 v[214:217], v194 offset:20480
	ds_read_b128 v[218:221], v194 offset:21504
	ds_read_b128 v[222:225], v194 offset:22528
	ds_read_b128 v[226:229], v194 offset:23552
	global_load_lds_dwordx4 v164, s[28:29]
	s_add_i32 m0, s75, 0x2000
	s_add_i32 s75, s66, s47
	global_load_lds_dwordx4 v166, s[28:29]
	s_add_u32 s98, s28, s4
	s_addc_u32 s99, s29, s5
	s_mov_b32 m0, s75
	s_nop 0
	global_load_lds_dwordx4 v164, s[98:99]
	s_add_u32 s100, s28, s4
	s_addc_u32 s101, s29, s5
	s_add_i32 m0, s75, 0x2000
	s_nop 0
	global_load_lds_dwordx4 v166, s[100:101]
	s_mov_b32 m0, s48
	s_nop 0
	global_load_lds_dwordx4 v174, s[30:31]
	s_mov_b32 m0, s49
	s_nop 0
	global_load_lds_dwordx4 v176, s[30:31]
	s_waitcnt vmcnt(8)
	s_waitcnt lgkmcnt(0)
	s_barrier
	s_setprio 2
	v_mfma_f32_16x16x128_f8f6f4 v[94:97], v[18:25], v[198:205], v[94:97]
	v_mfma_f32_16x16x128_f8f6f4 v[90:93], v[26:33], v[198:205], v[90:93]
	v_mfma_f32_16x16x128_f8f6f4 v[78:81], v[18:25], v[206:213], v[78:81]
	v_mfma_f32_16x16x128_f8f6f4 v[74:77], v[26:33], v[206:213], v[74:77]
	v_mfma_f32_16x16x128_f8f6f4 v[62:65], v[18:25], v[214:221], v[62:65]
	v_mfma_f32_16x16x128_f8f6f4 v[58:61], v[26:33], v[214:221], v[58:61]
	v_mfma_f32_16x16x128_f8f6f4 v[46:49], v[18:25], v[222:229], v[46:49]
	v_mfma_f32_16x16x128_f8f6f4 v[42:45], v[26:33], v[222:229], v[42:45]
	s_nop 3
	s_setprio 0
	s_setprio 2
	v_mfma_f32_16x16x128_f8f6f4 v[86:89], v[2:9], v[198:205], v[86:89]
	v_mfma_f32_16x16x128_f8f6f4 v[82:85], v[10:17], v[198:205], v[82:85]
	v_mfma_f32_16x16x128_f8f6f4 v[70:73], v[2:9], v[206:213], v[70:73]
	v_mfma_f32_16x16x128_f8f6f4 v[66:69], v[10:17], v[206:213], v[66:69]
	v_mfma_f32_16x16x128_f8f6f4 v[54:57], v[2:9], v[214:221], v[54:57]
	v_mfma_f32_16x16x128_f8f6f4 v[50:53], v[10:17], v[214:221], v[50:53]
	v_mfma_f32_16x16x128_f8f6f4 v[38:41], v[2:9], v[222:229], v[38:41]
	v_mfma_f32_16x16x128_f8f6f4 v[34:37], v[10:17], v[222:229], v[34:37]
	s_setprio 0
	s_add_i32 s75, 0, 0x18000
	s_add_i32 s76, 0, 0x1c000
	v_add_u32_e32 v14, s75, v191
	v_add_u32_e32 v30, s76, v191
	ds_read_b128 v[2:5], v14
	ds_read_b128 v[6:9], v14 offset:1024
	ds_read_b128 v[10:13], v14 offset:2048
	ds_read_b128 v[14:17], v14 offset:3072
	ds_read_b128 v[18:21], v30
	ds_read_b128 v[22:25], v30 offset:1024
	ds_read_b128 v[26:29], v30 offset:2048
	ds_read_b128 v[30:33], v30 offset:3072
	s_mov_b32 m0, s50
	ds_read_b128 v[198:201], v194 offset:32768
	ds_read_b128 v[202:205], v194 offset:33792
	ds_read_b128 v[206:209], v194 offset:34816
	ds_read_b128 v[210:213], v194 offset:35840
	ds_read_b128 v[214:217], v194 offset:36864
	ds_read_b128 v[218:221], v194 offset:37888
	ds_read_b128 v[222:225], v194 offset:38912
	ds_read_b128 v[226:229], v194 offset:39936
	global_load_lds_dwordx4 v178, s[30:31]
	s_mov_b32 m0, s51
	s_nop 0
	global_load_lds_dwordx4 v180, s[30:31]
	s_waitcnt vmcnt(8)
	s_waitcnt lgkmcnt(0)
	s_barrier
; #define PG8_STAGE(bufoff, gbase, voff) do { _Pragma("unroll") for (int _i = 0; _i < 2; ++_i) \
;         __builtin_amdgcn_global_load_lds((const unsigned*)((const char*)(gbase) + (voff)[_i]), (PG8_LAS unsigned*)(lds + (bufoff) + ldsw + _i * 8192), 16, 0, 0); } while (0)
; #define PG8_WAIT_V(n) asm volatile("s_waitcnt vmcnt(" #n ")" ::: "memory")
; #define PG8_WAIT_L(n) asm volatile("s_waitcnt lgkmcnt(" #n ")" ::: "memory")
; #define PG8_BAR __builtin_amdgcn_s_barrier()
; #define PG8_SCHED __builtin_amdgcn_sched_barrier(0)
; template <class Epi, class Sched, bool ALIGN_EPI = true, bool F8 = false>
; __device__ __forceinline__ void gemm_phase(PG8_LAS unsigned char* lds, const Sched& S, const Epi& E) {
;     ...
;             PG8_LDA(At, 1, 1); PG8_STAGE(PG8_SB(1, 0), b3, voffB[0]); PG8_STAGE(PG8_SB(1, 1), b3, voffB[1]); PG8_STAGE(PG8_SA(1, 0), a3, vA2[0]);
;             PG8_WAIT_V(8); PG8_WAIT_L(0); PG8_BAR; PG8_MMA(1, 0, At, B0); PG8_MMA(1, 1, At, B1); PG8_BAR; PG8_SCHED;
	s_setprio 2
	v_mfma_f32_16x16x128_f8f6f4 v[158:161], v[2:9], v[198:205], v[158:161]
	v_mfma_f32_16x16x128_f8f6f4 v[154:157], v[10:17], v[198:205], v[154:157]
	v_mfma_f32_16x16x128_f8f6f4 v[142:145], v[2:9], v[206:213], v[142:145]
	v_mfma_f32_16x16x128_f8f6f4 v[138:141], v[10:17], v[206:213], v[138:141]
	v_mfma_f32_16x16x128_f8f6f4 v[126:129], v[2:9], v[214:221], v[126:129]
	v_mfma_f32_16x16x128_f8f6f4 v[122:125], v[10:17], v[214:221], v[122:125]
	v_mfma_f32_16x16x128_f8f6f4 v[110:113], v[2:9], v[222:229], v[110:113]
	v_mfma_f32_16x16x128_f8f6f4 v[106:109], v[10:17], v[222:229], v[106:109]
	s_nop 3
	s_setprio 0
	s_setprio 2
	v_mfma_f32_16x16x128_f8f6f4 v[150:153], v[18:25], v[198:205], v[150:153]
	v_mfma_f32_16x16x128_f8f6f4 v[146:149], v[26:33], v[198:205], v[146:149]
	v_mfma_f32_16x16x128_f8f6f4 v[134:137], v[18:25], v[206:213], v[134:137]
	v_mfma_f32_16x16x128_f8f6f4 v[130:133], v[26:33], v[206:213], v[130:133]
	v_mfma_f32_16x16x128_f8f6f4 v[118:121], v[18:25], v[214:221], v[118:121]
	v_mfma_f32_16x16x128_f8f6f4 v[114:117], v[26:33], v[214:221], v[114:117]
	v_mfma_f32_16x16x128_f8f6f4 v[102:105], v[18:25], v[222:229], v[102:105]
	v_mfma_f32_16x16x128_f8f6f4 v[98:101], v[26:33], v[222:229], v[98:101]
	s_setprio 0
	s_add_u32 s28, s28, 0x8000
	s_addc_u32 s29, s29, 0
	s_add_i32 s30, s75, s47
	s_mov_b32 m0, s30
	ds_read_b128 v[198:201], v194 offset:49152
	ds_read_b128 v[202:205], v194 offset:50176
	ds_read_b128 v[206:209], v194 offset:51200
	ds_read_b128 v[210:213], v194 offset:52224
	ds_read_b128 v[214:217], v194 offset:53248
	ds_read_b128 v[218:221], v194 offset:54272
	ds_read_b128 v[222:225], v194 offset:55296
	ds_read_b128 v[226:229], v194 offset:56320
	global_load_lds_dwordx4 v164, s[28:29]
	s_add_i32 m0, s30, 0x2000
	s_add_i32 s30, s76, s47
	global_load_lds_dwordx4 v166, s[28:29]
	s_mov_b32 m0, s30
	s_nop 0
	global_load_lds_dwordx4 v168, s[28:29]
	s_add_i32 m0, s30, 0x2000
	s_nop 0
	global_load_lds_dwordx4 v172, s[28:29]
	s_mov_b32 m0, s60
	s_nop 0
	global_load_lds_dwordx4 v174, s[26:27]
	s_mov_b32 m0, s61
	s_nop 0
	global_load_lds_dwordx4 v176, s[26:27]
	s_waitcnt vmcnt(8)
	s_waitcnt lgkmcnt(0)
	s_barrier
	s_setprio 2
	v_mfma_f32_16x16x128_f8f6f4 v[94:97], v[2:9], v[198:205], v[94:97]
	v_mfma_f32_16x16x128_f8f6f4 v[90:93], v[10:17], v[198:205], v[90:93]
	v_mfma_f32_16x16x128_f8f6f4 v[78:81], v[2:9], v[206:213], v[78:81]
	v_mfma_f32_16x16x128_f8f6f4 v[74:77], v[10:17], v[206:213], v[74:77]
	v_mfma_f32_16x16x128_f8f6f4 v[62:65], v[2:9], v[214:221], v[62:65]
	v_mfma_f32_16x16x128_f8f6f4 v[58:61], v[10:17], v[214:221], v[58:61]
	v_mfma_f32_16x16x128_f8f6f4 v[46:49], v[2:9], v[222:229], v[46:49]
	v_mfma_f32_16x16x128_f8f6f4 v[42:45], v[10:17], v[222:229], v[42:45]
	s_nop 3
	s_setprio 0
	s_setprio 2
	v_mfma_f32_16x16x128_f8f6f4 v[86:89], v[18:25], v[198:205], v[86:89]
	v_mfma_f32_16x16x128_f8f6f4 v[82:85], v[26:33], v[198:205], v[82:85]
	v_mfma_f32_16x16x128_f8f6f4 v[70:73], v[18:25], v[206:213], v[70:73]
	v_mfma_f32_16x16x128_f8f6f4 v[66:69], v[26:33], v[206:213], v[66:69]
	v_mfma_f32_16x16x128_f8f6f4 v[54:57], v[18:25], v[214:221], v[54:57]
	v_mfma_f32_16x16x128_f8f6f4 v[50:53], v[26:33], v[214:221], v[50:53]
	v_mfma_f32_16x16x128_f8f6f4 v[38:41], v[18:25], v[222:229], v[38:41]
	v_mfma_f32_16x16x128_f8f6f4 v[34:37], v[26:33], v[222:229], v[34:37]
	s_setprio 0
	s_add_i32 s74, s74, 2
	s_add_u32 s17, s17, 0x10000
	s_addc_u32 s19, s19, 0
	s_add_u32 s24, s24, 0x10000
	s_addc_u32 s25, s25, 0
	s_cmp_gt_u32 s74, 13
	s_cbranch_scc0 .Lh1_428

; #define PG8_STAGE(bufoff, gbase, voff) do { _Pragma("unroll") for (int _i = 0; _i < 2; ++_i) \
;         __builtin_amdgcn_global_load_lds((const unsigned*)((const char*)(gbase) + (voff)[_i]), (PG8_LAS unsigned*)(lds + (bufoff) + ldsw + _i * 8192), 16, 0, 0); } while (0)
; #define PG8_WAIT_V(n) asm volatile("s_waitcnt vmcnt(" #n ")" ::: "memory")
; #define PG8_WAIT_L(n) asm volatile("s_waitcnt lgkmcnt(" #n ")" ::: "memory")
; #define PG8_BAR __builtin_amdgcn_s_barrier()
; #define PG8_SCHED __builtin_amdgcn_sched_barrier(0)
; template <class Epi, class Sched, bool ALIGN_EPI = true, bool F8 = false>
; __device__ __forceinline__ void gemm_phase(PG8_LAS unsigned char* lds, const Sched& S, const Epi& E) {
;     ...
;         for (int t = 0; t < nt; t += 2) {
;             const bool last = (t == nt - 2);
;             if constexpr (Sched::GATHER) { if (last && has_next) S.a_off(nxt, Rs, Cs, voffAn); }
;             const char* a1 = cA + (size_t)(t + 1) * kstep;
;             const char* a2 = last ? nA : cA + (size_t)(t + 2) * kstep; const char* b2 = last ? nB : cB + (size_t)(t + 2) * kstepB;
;             const char* a3 = a2 + kstep; const char* b3 = b2 + kstepB;
;             unsigned vA2[2][2];
; #pragma unroll
;             for (int h = 0; h < 2; ++h)
; #pragma unroll
;                 for (int i = 0; i < 2; ++i) { if constexpr (Sched::GATHER) vA2[h][i] = (last && has_next) ? voffAn[h][i] : voffA[h][i]; else vA2[h][i] = voffA[h][i]; }
;             PG8_LDB(B0, 0, 0); PG8_LDB(B1, 0, 1); PG8_SCHED; PG8_LDA(At, 0, 0); PG8_STAGE(PG8_SA(1, 1), a1, voffA[1]);
;             PG8_WAIT_V(8); PG8_WAIT_L(0); PG8_BAR; PG8_MMA(0, 0, At, B0); PG8_MMA(0, 1, At, B1); PG8_BAR; PG8_SCHED;
;             PG8_LDA(At, 0, 1); PG8_STAGE(PG8_SB(0, 0), b2, voffB[0]); PG8_STAGE(PG8_SB(0, 1), b2, voffB[1]); PG8_STAGE(PG8_SA(0, 0), a2, vA2[0]);
;             PG8_WAIT_V(8); PG8_WAIT_L(0); PG8_BAR; PG8_MMA(1, 0, At, B0); PG8_MMA(1, 1, At, B1); PG8_BAR; PG8_SCHED;
.LBB0_834:
	v_add_u32_e32 v10, s58, v190
	ds_read_b128 v[2:5], v10
	ds_read_b128 v[6:9], v10 offset:1024
	ds_read_b128 v[142:145], v10 offset:2048
	ds_read_b128 v[146:149], v10 offset:3072
	v_add_u32_e32 v10, s59, v190
	ds_read_b128 v[150:153], v10
	ds_read_b128 v[154:157], v10 offset:1024
	ds_read_b128 v[202:205], v10 offset:2048
	ds_read_b128 v[206:209], v10 offset:3072
	s_add_i32 s77, s26, 2
	s_add_u32 s27, s24, 0x8000
	s_addc_u32 s28, s25, 0
	s_cmp_eq_u32 s74, s26
	s_cselect_b32 s30, s20, s27
	s_cselect_b32 s31, s21, s28
	s_cselect_b32 s28, s22, s75
	s_cselect_b32 s29, s23, s76
	s_add_u32 s26, s30, 0x8000
	s_addc_u32 s27, s31, 0
	s_add_i32 m0, s45, 0xc000
	ds_read_b128 v[210:213], v198
	ds_read_b128 v[214:217], v198 offset:1024
	ds_read_b128 v[218:221], v198 offset:2048
	ds_read_b128 v[222:225], v198 offset:3072
	ds_read_b128 v[226:229], v198 offset:4096
	ds_read_b128 v[230:233], v198 offset:5120
	ds_read_b128 v[234:237], v198 offset:6144
	ds_read_b128 v[238:241], v198 offset:7168
	global_load_lds_dwordx4 v182, s[24:25]
	s_add_i32 m0, s45, 0xe000
	s_nop 0
	global_load_lds_dwordx4 v180, s[24:25]
	s_waitcnt vmcnt(8)
	s_waitcnt lgkmcnt(0)
	s_setprio 1
	v_mfma_f32_16x16x128_f8f6f4 v[138:141], v[2:9], v[210:217], v[138:141]
	v_mfma_f32_16x16x128_f8f6f4 v[134:137], v[142:149], v[210:217], v[134:137]
	v_mfma_f32_16x16x128_f8f6f4 v[130:133], v[2:9], v[218:225], v[130:133]
	v_mfma_f32_16x16x128_f8f6f4 v[126:129], v[142:149], v[218:225], v[126:129]
	v_mfma_f32_16x16x128_f8f6f4 v[122:125], v[2:9], v[226:233], v[122:125]
	v_mfma_f32_16x16x128_f8f6f4 v[118:121], v[142:149], v[226:233], v[118:121]
	v_mfma_f32_16x16x128_f8f6f4 v[114:117], v[2:9], v[234:241], v[114:117]
	v_mfma_f32_16x16x128_f8f6f4 v[110:113], v[142:149], v[234:241], v[110:113]
	s_nop 3
	s_setprio 0
	s_setprio 1
	v_mfma_f32_16x16x128_f8f6f4 v[106:109], v[150:157], v[210:217], v[106:109]
	v_mfma_f32_16x16x128_f8f6f4 v[102:105], v[202:209], v[210:217], v[102:105]
	v_mfma_f32_16x16x128_f8f6f4 v[98:101], v[150:157], v[218:225], v[98:101]
	v_mfma_f32_16x16x128_f8f6f4 v[94:97], v[202:209], v[218:225], v[94:97]
	v_mfma_f32_16x16x128_f8f6f4 v[90:93], v[150:157], v[226:233], v[90:93]
	v_mfma_f32_16x16x128_f8f6f4 v[86:89], v[202:209], v[226:233], v[86:89]
	v_mfma_f32_16x16x128_f8f6f4 v[82:85], v[150:157], v[234:241], v[82:85]
	v_mfma_f32_16x16x128_f8f6f4 v[78:81], v[202:209], v[234:241], v[78:81]
	s_setprio 0
	s_barrier
	s_add_i32 s78, s58, s44
	s_mov_b32 m0, s78
	ds_read_b128 v[210:213], v198 offset:16384
	ds_read_b128 v[214:217], v198 offset:17408
	ds_read_b128 v[218:221], v198 offset:18432
	ds_read_b128 v[222:225], v198 offset:19456
	ds_read_b128 v[226:229], v198 offset:20480
	ds_read_b128 v[230:233], v198 offset:21504
	ds_read_b128 v[234:237], v198 offset:22528
	ds_read_b128 v[238:241], v198 offset:23552
	global_load_lds_dwordx4 v158, s[28:29]
	s_add_i32 m0, s78, 0x2000
	s_add_i32 s78, s59, s44
	global_load_lds_dwordx4 v160, s[28:29]
	s_add_u32 s98, s28, s8
	s_addc_u32 s99, s29, s9
	s_mov_b32 m0, s78
	s_nop 0
	global_load_lds_dwordx4 v158, s[98:99]
	s_add_u32 s100, s28, s8
	s_addc_u32 s101, s29, s9
	s_add_i32 m0, s78, 0x2000
	s_nop 0
	global_load_lds_dwordx4 v160, s[100:101]
	s_mov_b32 m0, s45
	s_nop 0
	global_load_lds_dwordx4 v162, s[30:31]
	s_mov_b32 m0, s46
	s_nop 0
	global_load_lds_dwordx4 v164, s[30:31]
	s_waitcnt vmcnt(8)
	s_waitcnt lgkmcnt(0)
	s_setprio 1
	v_mfma_f32_16x16x128_f8f6f4 v[74:77], v[2:9], v[210:217], v[74:77]
	v_mfma_f32_16x16x128_f8f6f4 v[70:73], v[142:149], v[210:217], v[70:73]
	v_mfma_f32_16x16x128_f8f6f4 v[66:69], v[2:9], v[218:225], v[66:69]
	v_mfma_f32_16x16x128_f8f6f4 v[62:65], v[142:149], v[218:225], v[62:65]
	v_mfma_f32_16x16x128_f8f6f4 v[58:61], v[2:9], v[226:233], v[58:61]
	v_mfma_f32_16x16x128_f8f6f4 v[54:57], v[142:149], v[226:233], v[54:57]
	v_mfma_f32_16x16x128_f8f6f4 v[50:53], v[2:9], v[234:241], v[50:53]
	v_mfma_f32_16x16x128_f8f6f4 v[46:49], v[142:149], v[234:241], v[46:49]
	s_nop 3
	s_setprio 0
	s_setprio 1
	v_mfma_f32_16x16x128_f8f6f4 v[42:45], v[150:157], v[210:217], v[42:45]
	v_mfma_f32_16x16x128_f8f6f4 v[38:41], v[202:209], v[210:217], v[38:41]
	v_mfma_f32_16x16x128_f8f6f4 v[34:37], v[150:157], v[218:225], v[34:37]
	v_mfma_f32_16x16x128_f8f6f4 v[30:33], v[202:209], v[218:225], v[30:33]
	v_mfma_f32_16x16x128_f8f6f4 v[26:29], v[150:157], v[226:233], v[26:29]
	v_mfma_f32_16x16x128_f8f6f4 v[22:25], v[202:209], v[226:233], v[22:25]
	v_mfma_f32_16x16x128_f8f6f4 v[18:21], v[150:157], v[234:241], v[18:21]
	v_mfma_f32_16x16x128_f8f6f4 v[14:17], v[202:209], v[234:241], v[14:17]
	s_setprio 0
	s_barrier
; #define PG8_STAGE(bufoff, gbase, voff) do { _Pragma("unroll") for (int _i = 0; _i < 2; ++_i) \
;         __builtin_amdgcn_global_load_lds((const unsigned*)((const char*)(gbase) + (voff)[_i]), (PG8_LAS unsigned*)(lds + (bufoff) + ldsw + _i * 8192), 16, 0, 0); } while (0)
; #define PG8_WAIT_V(n) asm volatile("s_waitcnt vmcnt(" #n ")" ::: "memory")
; #define PG8_WAIT_L(n) asm volatile("s_waitcnt lgkmcnt(" #n ")" ::: "memory")
; #define PG8_BAR __builtin_amdgcn_s_barrier()
; #define PG8_SCHED __builtin_amdgcn_sched_barrier(0)
; template <class Epi, class Sched, bool ALIGN_EPI = true, bool F8 = false>
; __device__ __forceinline__ void gemm_phase(PG8_LAS unsigned char* lds, const Sched& S, const Epi& E) {
;     ...
;         for (int t = 0; t < nt; t += 2) {
;     ...
;             PG8_LDB(B0, 1, 0); PG8_LDB(B1, 1, 1); PG8_SCHED; PG8_LDA(At, 1, 0); PG8_STAGE(PG8_SA(0, 1), a2, vA2[1]);
;             PG8_WAIT_V(8); PG8_WAIT_L(0); PG8_BAR; PG8_MMA(0, 0, At, B0); PG8_MMA(0, 1, At, B1); PG8_BAR; PG8_SCHED;
;             PG8_LDA(At, 1, 1); PG8_STAGE(PG8_SB(1, 0), b3, voffB[0]); PG8_STAGE(PG8_SB(1, 1), b3, voffB[1]); PG8_STAGE(PG8_SA(1, 0), a3, vA2[0]);
;             PG8_WAIT_V(8); PG8_WAIT_L(0); PG8_BAR; PG8_MMA(1, 0, At, B0); PG8_MMA(1, 1, At, B1); PG8_BAR; PG8_SCHED;
	s_add_i32 s78, 0, 0x18000
	s_add_i32 s79, 0, 0x1c000
	v_add_u32_e32 v2, s78, v190
	v_add_u32_e32 v10, s79, v190
	ds_read_b128 v[142:145], v2
	ds_read_b128 v[146:149], v2 offset:1024
	ds_read_b128 v[150:153], v2 offset:2048
	ds_read_b128 v[154:157], v2 offset:3072
	ds_read_b128 v[2:5], v10
	ds_read_b128 v[6:9], v10 offset:1024
	ds_read_b128 v[202:205], v10 offset:2048
	ds_read_b128 v[206:209], v10 offset:3072
	s_mov_b32 m0, s47
	ds_read_b128 v[210:213], v198 offset:32768
	ds_read_b128 v[214:217], v198 offset:33792
	ds_read_b128 v[218:221], v198 offset:34816
	ds_read_b128 v[222:225], v198 offset:35840
	ds_read_b128 v[226:229], v198 offset:36864
	ds_read_b128 v[230:233], v198 offset:37888
	ds_read_b128 v[234:237], v198 offset:38912
	ds_read_b128 v[238:241], v198 offset:39936
	global_load_lds_dwordx4 v166, s[30:31]
	s_mov_b32 m0, s48
	s_nop 0
	global_load_lds_dwordx4 v168, s[30:31]
	s_waitcnt vmcnt(8)
	s_waitcnt lgkmcnt(0)
	s_setprio 1
	v_mfma_f32_16x16x128_f8f6f4 v[138:141], v[142:149], v[210:217], v[138:141]
	v_mfma_f32_16x16x128_f8f6f4 v[134:137], v[150:157], v[210:217], v[134:137]
	v_mfma_f32_16x16x128_f8f6f4 v[130:133], v[142:149], v[218:225], v[130:133]
	v_mfma_f32_16x16x128_f8f6f4 v[126:129], v[150:157], v[218:225], v[126:129]
	v_mfma_f32_16x16x128_f8f6f4 v[122:125], v[142:149], v[226:233], v[122:125]
	v_mfma_f32_16x16x128_f8f6f4 v[118:121], v[150:157], v[226:233], v[118:121]
	v_mfma_f32_16x16x128_f8f6f4 v[114:117], v[142:149], v[234:241], v[114:117]
	v_mfma_f32_16x16x128_f8f6f4 v[110:113], v[150:157], v[234:241], v[110:113]
	s_nop 3
	s_setprio 0
	s_setprio 1
	v_mfma_f32_16x16x128_f8f6f4 v[106:109], v[2:9], v[210:217], v[106:109]
	v_mfma_f32_16x16x128_f8f6f4 v[102:105], v[202:209], v[210:217], v[102:105]
	v_mfma_f32_16x16x128_f8f6f4 v[98:101], v[2:9], v[218:225], v[98:101]
	v_mfma_f32_16x16x128_f8f6f4 v[94:97], v[202:209], v[218:225], v[94:97]
	v_mfma_f32_16x16x128_f8f6f4 v[90:93], v[2:9], v[226:233], v[90:93]
	v_mfma_f32_16x16x128_f8f6f4 v[86:89], v[202:209], v[226:233], v[86:89]
	v_mfma_f32_16x16x128_f8f6f4 v[82:85], v[2:9], v[234:241], v[82:85]
	v_mfma_f32_16x16x128_f8f6f4 v[78:81], v[202:209], v[234:241], v[78:81]
	s_setprio 0
	s_barrier
	s_add_u32 s28, s28, 0x8000
	s_addc_u32 s29, s29, 0
	s_add_i32 s30, s78, s44
	s_mov_b32 m0, s30
	ds_read_b128 v[210:213], v198 offset:49152
	ds_read_b128 v[214:217], v198 offset:50176
	ds_read_b128 v[218:221], v198 offset:51200
	ds_read_b128 v[222:225], v198 offset:52224
	ds_read_b128 v[226:229], v198 offset:53248
	ds_read_b128 v[230:233], v198 offset:54272
	ds_read_b128 v[234:237], v198 offset:55296
	ds_read_b128 v[238:241], v198 offset:56320
	global_load_lds_dwordx4 v158, s[28:29]
	s_add_i32 m0, s30, 0x2000
	s_add_i32 s30, s79, s44
	global_load_lds_dwordx4 v160, s[28:29]
	s_mov_b32 m0, s30
	s_nop 0
	global_load_lds_dwordx4 v172, s[28:29]
	s_add_i32 m0, s30, 0x2000
	s_nop 0
	global_load_lds_dwordx4 v174, s[28:29]
	s_mov_b32 m0, s50
	s_nop 0
	global_load_lds_dwordx4 v162, s[26:27]
	s_mov_b32 m0, s51
	s_nop 0
	global_load_lds_dwordx4 v164, s[26:27]
	s_waitcnt vmcnt(8)
	s_waitcnt lgkmcnt(0)
	s_setprio 1
	v_mfma_f32_16x16x128_f8f6f4 v[74:77], v[142:149], v[210:217], v[74:77]
	v_mfma_f32_16x16x128_f8f6f4 v[70:73], v[150:157], v[210:217], v[70:73]
	v_mfma_f32_16x16x128_f8f6f4 v[66:69], v[142:149], v[218:225], v[66:69]
	v_mfma_f32_16x16x128_f8f6f4 v[62:65], v[150:157], v[218:225], v[62:65]
	v_mfma_f32_16x16x128_f8f6f4 v[58:61], v[142:149], v[226:233], v[58:61]
	v_mfma_f32_16x16x128_f8f6f4 v[54:57], v[150:157], v[226:233], v[54:57]
	v_mfma_f32_16x16x128_f8f6f4 v[50:53], v[142:149], v[234:241], v[50:53]
	v_mfma_f32_16x16x128_f8f6f4 v[46:49], v[150:157], v[234:241], v[46:49]
	s_nop 3
	s_setprio 0
	s_setprio 1
	v_mfma_f32_16x16x128_f8f6f4 v[42:45], v[2:9], v[210:217], v[42:45]
	v_mfma_f32_16x16x128_f8f6f4 v[38:41], v[202:209], v[210:217], v[38:41]
	v_mfma_f32_16x16x128_f8f6f4 v[34:37], v[2:9], v[218:225], v[34:37]
	v_mfma_f32_16x16x128_f8f6f4 v[30:33], v[202:209], v[218:225], v[30:33]
	v_mfma_f32_16x16x128_f8f6f4 v[26:29], v[2:9], v[226:233], v[26:29]
	v_mfma_f32_16x16x128_f8f6f4 v[22:25], v[202:209], v[226:233], v[22:25]
	v_mfma_f32_16x16x128_f8f6f4 v[18:21], v[2:9], v[234:241], v[18:21]
	v_mfma_f32_16x16x128_f8f6f4 v[14:17], v[202:209], v[234:241], v[14:17]
	s_setprio 0
	s_barrier
	s_add_u32 s75, s75, 0x10000
	s_addc_u32 s76, s76, 0
	s_add_u32 s24, s24, 0x10000
	s_addc_u32 s25, s25, 0
	s_cmp_ge_i32 s77, s72
	s_mov_b32 s26, s77
	s_cbranch_scc0 .LBB0_834
	s_branch .Lfx_23459
; #define PG8_STAGE(bufoff, gbase, voff) do { _Pragma("unroll") for (int _i = 0; _i < 2; ++_i) \
;         __builtin_amdgcn_global_load_lds((const unsigned*)((const char*)(gbase) + (voff)[_i]), (PG8_LAS unsigned*)(lds + (bufoff) + ldsw + _i * 8192), 16, 0, 0); } while (0)
; #define PG8_WAIT_V(n) asm volatile("s_waitcnt vmcnt(" #n ")" ::: "memory")
; #define PG8_WAIT_L(n) asm volatile("s_waitcnt lgkmcnt(" #n ")" ::: "memory")
; #define PG8_BAR __builtin_amdgcn_s_barrier()
; #define PG8_SCHED __builtin_amdgcn_sched_barrier(0)
; template <class Epi, class Sched, bool ALIGN_EPI = true, bool F8 = false>
; __device__ __forceinline__ void gemm_phase(PG8_LAS unsigned char* lds, const Sched& S, const Epi& E) {
;     ...
;             PG8_LDB(B0, 0, 0); PG8_LDB(B1, 0, 1); PG8_SCHED; PG8_LDA(At, 0, 0); PG8_STAGE(PG8_SA(1, 1), a1, voffA[1]);
;             PG8_WAIT_V(8); PG8_WAIT_L(0); PG8_BAR; PG8_MMA(0, 0, At, B0); PG8_MMA(0, 1, At, B1); PG8_BAR; PG8_SCHED;
;             PG8_LDA(At, 0, 1); PG8_STAGE(PG8_SB(0, 0), b2, voffB[0]); PG8_STAGE(PG8_SB(0, 1), b2, voffB[1]); PG8_STAGE(PG8_SA(0, 0), a2, vA2[0]);
;             PG8_WAIT_V(8); PG8_WAIT_L(0); PG8_BAR; PG8_MMA(1, 0, At, B0); PG8_MMA(1, 1, At, B1); PG8_BAR; PG8_SCHED;
;             PG8_LDB(B0, 1, 0); PG8_LDB(B1, 1, 1); PG8_SCHED; PG8_LDA(At, 1, 0); PG8_STAGE(PG8_SA(0, 1), a2, vA2[1]);
;             PG8_WAIT_V(8); PG8_WAIT_L(0); PG8_BAR; PG8_MMA(0, 0, At, B0); PG8_MMA(0, 1, At, B1); PG8_BAR; PG8_SCHED;
.Lh1e_23459:
.Lh1_834:
	v_add_u32_e32 v10, s58, v190
	ds_read_b128 v[2:5], v10
	ds_read_b128 v[6:9], v10 offset:1024
	ds_read_b128 v[142:145], v10 offset:2048
	ds_read_b128 v[146:149], v10 offset:3072
	v_add_u32_e32 v10, s59, v190
	ds_read_b128 v[150:153], v10
	ds_read_b128 v[154:157], v10 offset:1024
	ds_read_b128 v[202:205], v10 offset:2048
	ds_read_b128 v[206:209], v10 offset:3072
	s_add_i32 s77, s26, 2
	s_add_u32 s27, s24, 0x8000
	s_addc_u32 s28, s25, 0
	s_cmp_eq_u32 s74, s26
	s_cselect_b32 s30, s20, s27
	s_cselect_b32 s31, s21, s28
	s_cselect_b32 s28, s22, s75
	s_cselect_b32 s29, s23, s76
	s_add_u32 s26, s30, 0x8000
	s_addc_u32 s27, s31, 0
	s_add_i32 m0, s45, 0xc000
	ds_read_b128 v[210:213], v198
	ds_read_b128 v[214:217], v198 offset:1024
	ds_read_b128 v[218:221], v198 offset:2048
	ds_read_b128 v[222:225], v198 offset:3072
	ds_read_b128 v[226:229], v198 offset:4096
	ds_read_b128 v[230:233], v198 offset:5120
	ds_read_b128 v[234:237], v198 offset:6144
	ds_read_b128 v[238:241], v198 offset:7168
	global_load_lds_dwordx4 v182, s[24:25]
	s_add_i32 m0, s45, 0xe000
	s_nop 0
	global_load_lds_dwordx4 v180, s[24:25]
	s_waitcnt vmcnt(8)
	s_waitcnt lgkmcnt(0)
	s_barrier
	s_setprio 2
	v_mfma_f32_16x16x128_f8f6f4 v[138:141], v[2:9], v[210:217], v[138:141]
	v_mfma_f32_16x16x128_f8f6f4 v[134:137], v[142:149], v[210:217], v[134:137]
	v_mfma_f32_16x16x128_f8f6f4 v[130:133], v[2:9], v[218:225], v[130:133]
	v_mfma_f32_16x16x128_f8f6f4 v[126:129], v[142:149], v[218:225], v[126:129]
	v_mfma_f32_16x16x128_f8f6f4 v[122:125], v[2:9], v[226:233], v[122:125]
	v_mfma_f32_16x16x128_f8f6f4 v[118:121], v[142:149], v[226:233], v[118:121]
	v_mfma_f32_16x16x128_f8f6f4 v[114:117], v[2:9], v[234:241], v[114:117]
	v_mfma_f32_16x16x128_f8f6f4 v[110:113], v[142:149], v[234:241], v[110:113]
	s_nop 3
	s_setprio 0
	s_setprio 2
	v_mfma_f32_16x16x128_f8f6f4 v[106:109], v[150:157], v[210:217], v[106:109]
	v_mfma_f32_16x16x128_f8f6f4 v[102:105], v[202:209], v[210:217], v[102:105]
	v_mfma_f32_16x16x128_f8f6f4 v[98:101], v[150:157], v[218:225], v[98:101]
	v_mfma_f32_16x16x128_f8f6f4 v[94:97], v[202:209], v[218:225], v[94:97]
	v_mfma_f32_16x16x128_f8f6f4 v[90:93], v[150:157], v[226:233], v[90:93]
	v_mfma_f32_16x16x128_f8f6f4 v[86:89], v[202:209], v[226:233], v[86:89]
	v_mfma_f32_16x16x128_f8f6f4 v[82:85], v[150:157], v[234:241], v[82:85]
	v_mfma_f32_16x16x128_f8f6f4 v[78:81], v[202:209], v[234:241], v[78:81]
	s_setprio 0
	s_add_i32 s78, s58, s44
	s_mov_b32 m0, s78
	ds_read_b128 v[210:213], v198 offset:16384
	ds_read_b128 v[214:217], v198 offset:17408
	ds_read_b128 v[218:221], v198 offset:18432
	ds_read_b128 v[222:225], v198 offset:19456
	ds_read_b128 v[226:229], v198 offset:20480
	ds_read_b128 v[230:233], v198 offset:21504
	ds_read_b128 v[234:237], v198 offset:22528
	ds_read_b128 v[238:241], v198 offset:23552
	global_load_lds_dwordx4 v158, s[28:29]
	s_add_i32 m0, s78, 0x2000
	s_add_i32 s78, s59, s44
	global_load_lds_dwordx4 v160, s[28:29]
	s_add_u32 s98, s28, s8
	s_addc_u32 s99, s29, s9
	s_mov_b32 m0, s78
	s_nop 0
	global_load_lds_dwordx4 v158, s[98:99]
	s_add_u32 s100, s28, s8
	s_addc_u32 s101, s29, s9
	s_add_i32 m0, s78, 0x2000
	s_nop 0
	global_load_lds_dwordx4 v160, s[100:101]
	s_mov_b32 m0, s45
	s_nop 0
	global_load_lds_dwordx4 v162, s[30:31]
	s_mov_b32 m0, s46
	s_nop 0
	global_load_lds_dwordx4 v164, s[30:31]
	s_waitcnt vmcnt(8)
	s_waitcnt lgkmcnt(0)
	s_barrier
	s_setprio 2
	v_mfma_f32_16x16x128_f8f6f4 v[74:77], v[2:9], v[210:217], v[74:77]
	v_mfma_f32_16x16x128_f8f6f4 v[70:73], v[142:149], v[210:217], v[70:73]
	v_mfma_f32_16x16x128_f8f6f4 v[66:69], v[2:9], v[218:225], v[66:69]
	v_mfma_f32_16x16x128_f8f6f4 v[62:65], v[142:149], v[218:225], v[62:65]
	v_mfma_f32_16x16x128_f8f6f4 v[58:61], v[2:9], v[226:233], v[58:61]
	v_mfma_f32_16x16x128_f8f6f4 v[54:57], v[142:149], v[226:233], v[54:57]
	v_mfma_f32_16x16x128_f8f6f4 v[50:53], v[2:9], v[234:241], v[50:53]
	v_mfma_f32_16x16x128_f8f6f4 v[46:49], v[142:149], v[234:241], v[46:49]
	s_nop 3
	s_setprio 0
	s_setprio 2
	v_mfma_f32_16x16x128_f8f6f4 v[42:45], v[150:157], v[210:217], v[42:45]
	v_mfma_f32_16x16x128_f8f6f4 v[38:41], v[202:209], v[210:217], v[38:41]
	v_mfma_f32_16x16x128_f8f6f4 v[34:37], v[150:157], v[218:225], v[34:37]
	v_mfma_f32_16x16x128_f8f6f4 v[30:33], v[202:209], v[218:225], v[30:33]
	v_mfma_f32_16x16x128_f8f6f4 v[26:29], v[150:157], v[226:233], v[26:29]
	v_mfma_f32_16x16x128_f8f6f4 v[22:25], v[202:209], v[226:233], v[22:25]
	v_mfma_f32_16x16x128_f8f6f4 v[18:21], v[150:157], v[234:241], v[18:21]
	v_mfma_f32_16x16x128_f8f6f4 v[14:17], v[202:209], v[234:241], v[14:17]
	s_setprio 0
	s_add_i32 s78, 0, 0x18000
	s_add_i32 s79, 0, 0x1c000
	v_add_u32_e32 v2, s78, v190
	v_add_u32_e32 v10, s79, v190
	ds_read_b128 v[142:145], v2
	ds_read_b128 v[146:149], v2 offset:1024
	ds_read_b128 v[150:153], v2 offset:2048
	ds_read_b128 v[154:157], v2 offset:3072
	ds_read_b128 v[2:5], v10
	ds_read_b128 v[6:9], v10 offset:1024
	ds_read_b128 v[202:205], v10 offset:2048
	ds_read_b128 v[206:209], v10 offset:3072
	s_mov_b32 m0, s47
	ds_read_b128 v[210:213], v198 offset:32768
	ds_read_b128 v[214:217], v198 offset:33792
	ds_read_b128 v[218:221], v198 offset:34816
	ds_read_b128 v[222:225], v198 offset:35840
	ds_read_b128 v[226:229], v198 offset:36864
	ds_read_b128 v[230:233], v198 offset:37888
	ds_read_b128 v[234:237], v198 offset:38912
	ds_read_b128 v[238:241], v198 offset:39936
	global_load_lds_dwordx4 v166, s[30:31]
	s_mov_b32 m0, s48
	s_nop 0
	global_load_lds_dwordx4 v168, s[30:31]
	s_waitcnt vmcnt(8)
	s_waitcnt lgkmcnt(0)
	s_barrier
; #define PG8_STAGE(bufoff, gbase, voff) do { _Pragma("unroll") for (int _i = 0; _i < 2; ++_i) \
;         __builtin_amdgcn_global_load_lds((const unsigned*)((const char*)(gbase) + (voff)[_i]), (PG8_LAS unsigned*)(lds + (bufoff) + ldsw + _i * 8192), 16, 0, 0); } while (0)
; #define PG8_WAIT_V(n) asm volatile("s_waitcnt vmcnt(" #n ")" ::: "memory")
; #define PG8_WAIT_L(n) asm volatile("s_waitcnt lgkmcnt(" #n ")" ::: "memory")
; #define PG8_BAR __builtin_amdgcn_s_barrier()
; #define PG8_SCHED __builtin_amdgcn_sched_barrier(0)
; template <class Epi, class Sched, bool ALIGN_EPI = true, bool F8 = false>
; __device__ __forceinline__ void gemm_phase(PG8_LAS unsigned char* lds, const Sched& S, const Epi& E) {
;     ...
;         for (int t = 0; t < nt; t += 2) {
;     ...
;             PG8_LDA(At, 1, 1); PG8_STAGE(PG8_SB(1, 0), b3, voffB[0]); PG8_STAGE(PG8_SB(1, 1), b3, voffB[1]); PG8_STAGE(PG8_SA(1, 0), a3, vA2[0]);
;             PG8_WAIT_V(8); PG8_WAIT_L(0); PG8_BAR; PG8_MMA(1, 0, At, B0); PG8_MMA(1, 1, At, B1); PG8_BAR; PG8_SCHED;
	s_setprio 2
	v_mfma_f32_16x16x128_f8f6f4 v[138:141], v[142:149], v[210:217], v[138:141]
	v_mfma_f32_16x16x128_f8f6f4 v[134:137], v[150:157], v[210:217], v[134:137]
	v_mfma_f32_16x16x128_f8f6f4 v[130:133], v[142:149], v[218:225], v[130:133]
	v_mfma_f32_16x16x128_f8f6f4 v[126:129], v[150:157], v[218:225], v[126:129]
	v_mfma_f32_16x16x128_f8f6f4 v[122:125], v[142:149], v[226:233], v[122:125]
	v_mfma_f32_16x16x128_f8f6f4 v[118:121], v[150:157], v[226:233], v[118:121]
	v_mfma_f32_16x16x128_f8f6f4 v[114:117], v[142:149], v[234:241], v[114:117]
	v_mfma_f32_16x16x128_f8f6f4 v[110:113], v[150:157], v[234:241], v[110:113]
	s_nop 3
	s_setprio 0
	s_setprio 2
	v_mfma_f32_16x16x128_f8f6f4 v[106:109], v[2:9], v[210:217], v[106:109]
	v_mfma_f32_16x16x128_f8f6f4 v[102:105], v[202:209], v[210:217], v[102:105]
	v_mfma_f32_16x16x128_f8f6f4 v[98:101], v[2:9], v[218:225], v[98:101]
	v_mfma_f32_16x16x128_f8f6f4 v[94:97], v[202:209], v[218:225], v[94:97]
	v_mfma_f32_16x16x128_f8f6f4 v[90:93], v[2:9], v[226:233], v[90:93]
	v_mfma_f32_16x16x128_f8f6f4 v[86:89], v[202:209], v[226:233], v[86:89]
	v_mfma_f32_16x16x128_f8f6f4 v[82:85], v[2:9], v[234:241], v[82:85]
	v_mfma_f32_16x16x128_f8f6f4 v[78:81], v[202:209], v[234:241], v[78:81]
	s_setprio 0
	s_add_u32 s28, s28, 0x8000
	s_addc_u32 s29, s29, 0
	s_add_i32 s30, s78, s44
	s_mov_b32 m0, s30
	ds_read_b128 v[210:213], v198 offset:49152
	ds_read_b128 v[214:217], v198 offset:50176
	ds_read_b128 v[218:221], v198 offset:51200
	ds_read_b128 v[222:225], v198 offset:52224
	ds_read_b128 v[226:229], v198 offset:53248
	ds_read_b128 v[230:233], v198 offset:54272
	ds_read_b128 v[234:237], v198 offset:55296
	ds_read_b128 v[238:241], v198 offset:56320
	global_load_lds_dwordx4 v158, s[28:29]
	s_add_i32 m0, s30, 0x2000
	s_add_i32 s30, s79, s44
	global_load_lds_dwordx4 v160, s[28:29]
	s_mov_b32 m0, s30
	s_nop 0
	global_load_lds_dwordx4 v172, s[28:29]
	s_add_i32 m0, s30, 0x2000
	s_nop 0
	global_load_lds_dwordx4 v174, s[28:29]
	s_mov_b32 m0, s50
	s_nop 0
	global_load_lds_dwordx4 v162, s[26:27]
	s_mov_b32 m0, s51
	s_nop 0
	global_load_lds_dwordx4 v164, s[26:27]
	s_waitcnt vmcnt(8)
	s_waitcnt lgkmcnt(0)
	s_barrier
	s_setprio 2
	v_mfma_f32_16x16x128_f8f6f4 v[74:77], v[142:149], v[210:217], v[74:77]
	v_mfma_f32_16x16x128_f8f6f4 v[70:73], v[150:157], v[210:217], v[70:73]
	v_mfma_f32_16x16x128_f8f6f4 v[66:69], v[142:149], v[218:225], v[66:69]
	v_mfma_f32_16x16x128_f8f6f4 v[62:65], v[150:157], v[218:225], v[62:65]
	v_mfma_f32_16x16x128_f8f6f4 v[58:61], v[142:149], v[226:233], v[58:61]
	v_mfma_f32_16x16x128_f8f6f4 v[54:57], v[150:157], v[226:233], v[54:57]
	v_mfma_f32_16x16x128_f8f6f4 v[50:53], v[142:149], v[234:241], v[50:53]
	v_mfma_f32_16x16x128_f8f6f4 v[46:49], v[150:157], v[234:241], v[46:49]
	s_nop 3
	s_setprio 0
	s_setprio 2
	v_mfma_f32_16x16x128_f8f6f4 v[42:45], v[2:9], v[210:217], v[42:45]
	v_mfma_f32_16x16x128_f8f6f4 v[38:41], v[202:209], v[210:217], v[38:41]
	v_mfma_f32_16x16x128_f8f6f4 v[34:37], v[2:9], v[218:225], v[34:37]
	v_mfma_f32_16x16x128_f8f6f4 v[30:33], v[202:209], v[218:225], v[30:33]
	v_mfma_f32_16x16x128_f8f6f4 v[26:29], v[2:9], v[226:233], v[26:29]
	v_mfma_f32_16x16x128_f8f6f4 v[22:25], v[202:209], v[226:233], v[22:25]
	v_mfma_f32_16x16x128_f8f6f4 v[18:21], v[2:9], v[234:241], v[18:21]
	v_mfma_f32_16x16x128_f8f6f4 v[14:17], v[202:209], v[234:241], v[14:17]
	s_setprio 0
	s_add_u32 s75, s75, 0x10000
	s_addc_u32 s76, s76, 0
	s_add_u32 s24, s24, 0x10000
	s_addc_u32 s25, s25, 0
	s_cmp_ge_i32 s77, s72
	s_mov_b32 s26, s77
	s_cbranch_scc0 .Lh1_834

; #define PG8_STAGE(bufoff, gbase, voff) do { _Pragma("unroll") for (int _i = 0; _i < 2; ++_i) \
;         __builtin_amdgcn_global_load_lds((const unsigned*)((const char*)(gbase) + (voff)[_i]), (PG8_LAS unsigned*)(lds + (bufoff) + ldsw + _i * 8192), 16, 0, 0); } while (0)
; #define PG8_WAIT_V(n) asm volatile("s_waitcnt vmcnt(" #n ")" ::: "memory")
; #define PG8_WAIT_L(n) asm volatile("s_waitcnt lgkmcnt(" #n ")" ::: "memory")
; template <class Epi, class Sched, bool ALIGN_EPI = true, bool F8 = false>
; __device__ __forceinline__ void gemm_phase(PG8_LAS unsigned char* lds, const Sched& S, const Epi& E) {
;     ...
;         for (int t = 0; t < nt; t += 2) {
;             const bool last = (t == nt - 2);
;             if constexpr (Sched::GATHER) { if (last && has_next) S.a_off(nxt, Rs, Cs, voffAn); }
;             const char* a1 = cA + (size_t)(t + 1) * kstep;
;             const char* a2 = last ? nA : cA + (size_t)(t + 2) * kstep; const char* b2 = last ? nB : cB + (size_t)(t + 2) * kstepB;
;             const char* a3 = a2 + kstep; const char* b3 = b2 + kstepB;
;             unsigned vA2[2][2];
; #pragma unroll
;             for (int h = 0; h < 2; ++h)
; #pragma unroll
;                 for (int i = 0; i < 2; ++i) { if constexpr (Sched::GATHER) vA2[h][i] = (last && has_next) ? voffAn[h][i] : voffA[h][i]; else vA2[h][i] = voffA[h][i]; }
;             PG8_LDB(B0, 0, 0); PG8_LDB(B1, 0, 1); PG8_SCHED; PG8_LDA(At, 0, 0); PG8_STAGE(PG8_SA(1, 1), a1, voffA[1]);
;             PG8_WAIT_V(8); PG8_WAIT_L(0); PG8_BAR; PG8_MMA(0, 0, At, B0); PG8_MMA(0, 1, At, B1); PG8_BAR; PG8_SCHED;
;             PG8_LDA(At, 0, 1); PG8_STAGE(PG8_SB(0, 0), b2, voffB[0]); PG8_STAGE(PG8_SB(0, 1), b2, voffB[1]); PG8_STAGE(PG8_SA(0, 0), a2, vA2[0]);
;             PG8_WAIT_V(8); PG8_WAIT_L(0); PG8_BAR; PG8_MMA(1, 0, At, B0); PG8_MMA(1, 1, At, B1); PG8_BAR; PG8_SCHED;
;             PG8_LDB(B0, 1, 0); PG8_LDB(B1, 1, 1); PG8_SCHED; PG8_LDA(At, 1, 0); PG8_STAGE(PG8_SA(0, 1), a2, vA2[1]);
;             PG8_WAIT_V(8); PG8_WAIT_L(0); PG8_BAR; PG8_MMA(0, 0, At, B0); PG8_MMA(0, 1, At, B1); PG8_BAR; PG8_SCHED;
;             PG8_LDA(At, 1, 1); PG8_STAGE(PG8_SB(1, 0), b3, voffB[0]); PG8_STAGE(PG8_SB(1, 1), b3, voffB[1]); PG8_STAGE(PG8_SA(1, 0), a3, vA2[0]);
;             PG8_WAIT_V(8); PG8_WAIT_L(0); PG8_BAR; PG8_MMA(1, 0, At, B0); PG8_MMA(1, 1, At, B1); PG8_BAR; PG8_SCHED;
.Lpk0_911:
	ds_read_b128 v[18:21], v191
	ds_read_b128 v[22:25], v191 offset:1024
	ds_read_b128 v[26:29], v191 offset:2048
	ds_read_b128 v[30:33], v191 offset:3072
	ds_read_b128 v[2:5], v192
	ds_read_b128 v[6:9], v192 offset:1024
	ds_read_b128 v[10:13], v192 offset:2048
	ds_read_b128 v[14:17], v192 offset:3072
	s_add_u32 s30, s28, 0x8000
	s_addc_u32 s31, s29, 0
	s_cmp_eq_u32 s65, 12
	s_cselect_b32 s42, s22, s30
	s_cselect_b32 s43, s23, s31
	s_cselect_b32 s40, s24, s19
	s_cselect_b32 s41, s25, s21
	s_add_u32 s30, s42, 0x8000
	s_addc_u32 s31, s43, 0
	s_add_i32 m0, s27, 0xc000
	ds_read_b128 v[196:199], v193
	ds_read_b128 v[200:203], v193 offset:1024
	ds_read_b128 v[204:207], v193 offset:2048
	ds_read_b128 v[208:211], v193 offset:3072
	ds_read_b128 v[212:215], v193 offset:4096
	ds_read_b128 v[216:219], v193 offset:5120
	ds_read_b128 v[220:223], v193 offset:6144
	ds_read_b128 v[224:227], v193 offset:7168
	global_load_lds_dwordx4 v182, s[28:29]
	s_add_i32 m0, s27, 0xe000
	s_nop 0
	global_load_lds_dwordx4 v180, s[28:29]
	s_waitcnt vmcnt(8)
	s_waitcnt lgkmcnt(0)
	s_setprio 1
	v_mfma_f32_16x16x128_f8f6f4 v[158:161], v[18:25], v[196:203], 0
	v_mfma_f32_16x16x128_f8f6f4 v[154:157], v[26:33], v[196:203], 0
	v_mfma_f32_16x16x128_f8f6f4 v[150:153], v[18:25], v[204:211], 0
	v_mfma_f32_16x16x128_f8f6f4 v[146:149], v[26:33], v[204:211], 0
	v_mfma_f32_16x16x128_f8f6f4 v[130:133], v[18:25], v[212:219], 0
	v_mfma_f32_16x16x128_f8f6f4 v[122:125], v[26:33], v[212:219], 0
	v_mfma_f32_16x16x128_f8f6f4 v[114:117], v[18:25], v[220:227], 0
	v_mfma_f32_16x16x128_f8f6f4 v[106:109], v[26:33], v[220:227], 0
	s_nop 3
	s_setprio 0
	s_setprio 1
	v_mfma_f32_16x16x128_f8f6f4 v[142:145], v[2:9], v[196:203], 0
	v_mfma_f32_16x16x128_f8f6f4 v[138:141], v[10:17], v[196:203], 0
	v_mfma_f32_16x16x128_f8f6f4 v[134:137], v[2:9], v[204:211], 0
	v_mfma_f32_16x16x128_f8f6f4 v[126:129], v[10:17], v[204:211], 0
	v_mfma_f32_16x16x128_f8f6f4 v[118:121], v[2:9], v[212:219], 0
	v_mfma_f32_16x16x128_f8f6f4 v[110:113], v[10:17], v[212:219], 0
	v_mfma_f32_16x16x128_f8f6f4 v[102:105], v[2:9], v[220:227], 0
	v_mfma_f32_16x16x128_f8f6f4 v[98:101], v[10:17], v[220:227], 0
	s_setprio 0
	s_barrier
	s_add_i32 s66, s60, s48
	s_mov_b32 m0, s66
	ds_read_b128 v[196:199], v193 offset:16384
	ds_read_b128 v[200:203], v193 offset:17408
	ds_read_b128 v[204:207], v193 offset:18432
	ds_read_b128 v[208:211], v193 offset:19456
	ds_read_b128 v[212:215], v193 offset:20480
	ds_read_b128 v[216:219], v193 offset:21504
	ds_read_b128 v[220:223], v193 offset:22528
	ds_read_b128 v[224:227], v193 offset:23552
	global_load_lds_dwordx4 v162, s[40:41]
	s_add_i32 m0, s66, 0x2000
	s_add_i32 s66, s61, s48
	global_load_lds_dwordx4 v164, s[40:41]
	s_add_u32 s98, s40, s6
	s_addc_u32 s99, s41, s7
	s_mov_b32 m0, s66
	s_nop 0
	global_load_lds_dwordx4 v162, s[98:99]
	s_add_u32 s100, s40, s6
	s_addc_u32 s101, s41, s7
	s_add_i32 m0, s66, 0x2000
	s_nop 0
	global_load_lds_dwordx4 v164, s[100:101]
	s_mov_b32 m0, s27
	s_nop 0
	global_load_lds_dwordx4 v166, s[42:43]
	s_mov_b32 m0, s49
	s_nop 0
	global_load_lds_dwordx4 v168, s[42:43]
	s_waitcnt vmcnt(8)
	s_waitcnt lgkmcnt(0)
	s_setprio 1
	v_mfma_f32_16x16x128_f8f6f4 v[94:97], v[18:25], v[196:203], 0
	v_mfma_f32_16x16x128_f8f6f4 v[90:93], v[26:33], v[196:203], 0
	v_mfma_f32_16x16x128_f8f6f4 v[82:85], v[18:25], v[204:211], 0
	v_mfma_f32_16x16x128_f8f6f4 v[74:77], v[26:33], v[204:211], 0
	v_mfma_f32_16x16x128_f8f6f4 v[66:69], v[18:25], v[212:219], 0
	v_mfma_f32_16x16x128_f8f6f4 v[58:61], v[26:33], v[212:219], 0
	v_mfma_f32_16x16x128_f8f6f4 v[50:53], v[18:25], v[220:227], 0
	v_mfma_f32_16x16x128_f8f6f4 v[42:45], v[26:33], v[220:227], 0
	s_nop 3
	s_setprio 0
	s_setprio 1
	v_mfma_f32_16x16x128_f8f6f4 v[86:89], v[2:9], v[196:203], 0
	v_mfma_f32_16x16x128_f8f6f4 v[78:81], v[10:17], v[196:203], 0
	v_mfma_f32_16x16x128_f8f6f4 v[70:73], v[2:9], v[204:211], 0
	v_mfma_f32_16x16x128_f8f6f4 v[62:65], v[10:17], v[204:211], 0
	v_mfma_f32_16x16x128_f8f6f4 v[54:57], v[2:9], v[212:219], 0
	v_mfma_f32_16x16x128_f8f6f4 v[46:49], v[10:17], v[212:219], 0
	v_mfma_f32_16x16x128_f8f6f4 v[38:41], v[2:9], v[220:227], 0
	v_mfma_f32_16x16x128_f8f6f4 v[34:37], v[10:17], v[220:227], 0
	s_setprio 0
	s_barrier
	s_add_i32 s66, 0, 0x18000
	s_add_i32 s67, 0, 0x1c000
	v_add_u32_e32 v14, s66, v189
	v_add_u32_e32 v30, s67, v189
	ds_read_b128 v[2:5], v14
	ds_read_b128 v[6:9], v14 offset:1024
	ds_read_b128 v[10:13], v14 offset:2048
	ds_read_b128 v[14:17], v14 offset:3072
	ds_read_b128 v[18:21], v30
	ds_read_b128 v[22:25], v30 offset:1024
	ds_read_b128 v[26:29], v30 offset:2048
	ds_read_b128 v[30:33], v30 offset:3072
	s_mov_b32 m0, s50
	ds_read_b128 v[196:199], v193 offset:32768
	ds_read_b128 v[200:203], v193 offset:33792
	ds_read_b128 v[204:207], v193 offset:34816
	ds_read_b128 v[208:211], v193 offset:35840
	ds_read_b128 v[212:215], v193 offset:36864
	ds_read_b128 v[216:219], v193 offset:37888
	ds_read_b128 v[220:223], v193 offset:38912
	ds_read_b128 v[224:227], v193 offset:39936
	global_load_lds_dwordx4 v172, s[42:43]
	s_mov_b32 m0, s51
	s_nop 0
	global_load_lds_dwordx4 v174, s[42:43]
	s_waitcnt vmcnt(8)
	s_waitcnt lgkmcnt(0)
	s_setprio 1
	v_mfma_f32_16x16x128_f8f6f4 v[158:161], v[2:9], v[196:203], v[158:161]
	v_mfma_f32_16x16x128_f8f6f4 v[154:157], v[10:17], v[196:203], v[154:157]
	v_mfma_f32_16x16x128_f8f6f4 v[150:153], v[2:9], v[204:211], v[150:153]
	v_mfma_f32_16x16x128_f8f6f4 v[146:149], v[10:17], v[204:211], v[146:149]
	v_mfma_f32_16x16x128_f8f6f4 v[130:133], v[2:9], v[212:219], v[130:133]
	v_mfma_f32_16x16x128_f8f6f4 v[122:125], v[10:17], v[212:219], v[122:125]
	v_mfma_f32_16x16x128_f8f6f4 v[114:117], v[2:9], v[220:227], v[114:117]
	v_mfma_f32_16x16x128_f8f6f4 v[106:109], v[10:17], v[220:227], v[106:109]
	s_nop 3
	s_setprio 0
	s_setprio 1
	v_mfma_f32_16x16x128_f8f6f4 v[142:145], v[18:25], v[196:203], v[142:145]
	v_mfma_f32_16x16x128_f8f6f4 v[138:141], v[26:33], v[196:203], v[138:141]
	v_mfma_f32_16x16x128_f8f6f4 v[134:137], v[18:25], v[204:211], v[134:137]
	v_mfma_f32_16x16x128_f8f6f4 v[126:129], v[26:33], v[204:211], v[126:129]
	v_mfma_f32_16x16x128_f8f6f4 v[118:121], v[18:25], v[212:219], v[118:121]
	v_mfma_f32_16x16x128_f8f6f4 v[110:113], v[26:33], v[212:219], v[110:113]
	v_mfma_f32_16x16x128_f8f6f4 v[102:105], v[18:25], v[220:227], v[102:105]
	v_mfma_f32_16x16x128_f8f6f4 v[98:101], v[26:33], v[220:227], v[98:101]
	s_setprio 0
	s_barrier
; #define PG8_STAGE(bufoff, gbase, voff) do { _Pragma("unroll") for (int _i = 0; _i < 2; ++_i) \
;         __builtin_amdgcn_global_load_lds((const unsigned*)((const char*)(gbase) + (voff)[_i]), (PG8_LAS unsigned*)(lds + (bufoff) + ldsw + _i * 8192), 16, 0, 0); } while (0)
; #define PG8_WAIT_V(n) asm volatile("s_waitcnt vmcnt(" #n ")" ::: "memory")
; #define PG8_WAIT_L(n) asm volatile("s_waitcnt lgkmcnt(" #n ")" ::: "memory")
; #define PG8_BAR __builtin_amdgcn_s_barrier()
; #define PG8_SCHED __builtin_amdgcn_sched_barrier(0)
; template <class Epi, class Sched, bool ALIGN_EPI = true, bool F8 = false>
; __device__ __forceinline__ void gemm_phase(PG8_LAS unsigned char* lds, const Sched& S, const Epi& E) {
;     ...
;             PG8_LDB(B0, 0, 0); PG8_LDB(B1, 0, 1); PG8_SCHED; PG8_LDA(At, 0, 0); PG8_STAGE(PG8_SA(1, 1), a1, voffA[1]);
;             PG8_WAIT_V(8); PG8_WAIT_L(0); PG8_BAR; PG8_MMA(0, 0, At, B0); PG8_MMA(0, 1, At, B1); PG8_BAR; PG8_SCHED;
;             PG8_LDA(At, 0, 1); PG8_STAGE(PG8_SB(0, 0), b2, voffB[0]); PG8_STAGE(PG8_SB(0, 1), b2, voffB[1]); PG8_STAGE(PG8_SA(0, 0), a2, vA2[0]);
;             PG8_WAIT_V(8); PG8_WAIT_L(0); PG8_BAR; PG8_MMA(1, 0, At, B0); PG8_MMA(1, 1, At, B1); PG8_BAR; PG8_SCHED;
;             PG8_LDB(B0, 1, 0); PG8_LDB(B1, 1, 1); PG8_SCHED; PG8_LDA(At, 1, 0); PG8_STAGE(PG8_SA(0, 1), a2, vA2[1]);
;             PG8_WAIT_V(8); PG8_WAIT_L(0); PG8_BAR; PG8_MMA(0, 0, At, B0); PG8_MMA(0, 1, At, B1); PG8_BAR; PG8_SCHED;
;             PG8_LDA(At, 1, 1); PG8_STAGE(PG8_SB(1, 0), b3, voffB[0]); PG8_STAGE(PG8_SB(1, 1), b3, voffB[1]); PG8_STAGE(PG8_SA(1, 0), a3, vA2[0]);
;             PG8_WAIT_V(8); PG8_WAIT_L(0); PG8_BAR; PG8_MMA(1, 0, At, B0); PG8_MMA(1, 1, At, B1); PG8_BAR; PG8_SCHED;
	s_add_u32 s40, s40, 0x8000
	s_addc_u32 s41, s41, 0
	s_add_i32 s42, s66, s48
	s_mov_b32 m0, s42
	ds_read_b128 v[196:199], v193 offset:49152
	ds_read_b128 v[200:203], v193 offset:50176
	ds_read_b128 v[204:207], v193 offset:51200
	ds_read_b128 v[208:211], v193 offset:52224
	ds_read_b128 v[212:215], v193 offset:53248
	ds_read_b128 v[216:219], v193 offset:54272
	ds_read_b128 v[220:223], v193 offset:55296
	ds_read_b128 v[224:227], v193 offset:56320
	global_load_lds_dwordx4 v162, s[40:41]
	s_add_i32 m0, s42, 0x2000
	s_add_i32 s42, s67, s48
	global_load_lds_dwordx4 v164, s[40:41]
	s_mov_b32 m0, s42
	s_nop 0
	global_load_lds_dwordx4 v176, s[40:41]
	s_add_i32 m0, s42, 0x2000
	s_nop 0
	global_load_lds_dwordx4 v178, s[40:41]
	s_mov_b32 m0, s53
	s_nop 0
	global_load_lds_dwordx4 v166, s[30:31]
	s_mov_b32 m0, s58
	s_nop 0
	global_load_lds_dwordx4 v168, s[30:31]
	s_waitcnt vmcnt(8)
	s_waitcnt lgkmcnt(0)
	s_setprio 1
	v_mfma_f32_16x16x128_f8f6f4 v[94:97], v[2:9], v[196:203], v[94:97]
	v_mfma_f32_16x16x128_f8f6f4 v[90:93], v[10:17], v[196:203], v[90:93]
	v_mfma_f32_16x16x128_f8f6f4 v[82:85], v[2:9], v[204:211], v[82:85]
	v_mfma_f32_16x16x128_f8f6f4 v[74:77], v[10:17], v[204:211], v[74:77]
	v_mfma_f32_16x16x128_f8f6f4 v[66:69], v[2:9], v[212:219], v[66:69]
	v_mfma_f32_16x16x128_f8f6f4 v[58:61], v[10:17], v[212:219], v[58:61]
	v_mfma_f32_16x16x128_f8f6f4 v[50:53], v[2:9], v[220:227], v[50:53]
	v_mfma_f32_16x16x128_f8f6f4 v[42:45], v[10:17], v[220:227], v[42:45]
	s_nop 3
	s_setprio 0
	s_setprio 1
	v_mfma_f32_16x16x128_f8f6f4 v[86:89], v[18:25], v[196:203], v[86:89]
	v_mfma_f32_16x16x128_f8f6f4 v[78:81], v[26:33], v[196:203], v[78:81]
	v_mfma_f32_16x16x128_f8f6f4 v[70:73], v[18:25], v[204:211], v[70:73]
	v_mfma_f32_16x16x128_f8f6f4 v[62:65], v[26:33], v[204:211], v[62:65]
	v_mfma_f32_16x16x128_f8f6f4 v[54:57], v[18:25], v[212:219], v[54:57]
	v_mfma_f32_16x16x128_f8f6f4 v[46:49], v[26:33], v[212:219], v[46:49]
	v_mfma_f32_16x16x128_f8f6f4 v[38:41], v[18:25], v[220:227], v[38:41]
	v_mfma_f32_16x16x128_f8f6f4 v[34:37], v[26:33], v[220:227], v[34:37]
	s_setprio 0
	s_barrier
	s_add_i32 s65, s65, 2
	s_add_u32 s19, s19, 0x10000
	s_addc_u32 s21, s21, 0
	s_add_u32 s28, s28, 0x10000
	s_addc_u32 s29, s29, 0
	s_cmp_gt_u32 s65, 13
	s_cbranch_scc0 .LBB0_911
	s_branch .Lfx_26630
.LBB0_911:
	ds_read_b128 v[18:21], v191
	ds_read_b128 v[22:25], v191 offset:1024
	ds_read_b128 v[26:29], v191 offset:2048
	ds_read_b128 v[30:33], v191 offset:3072
	ds_read_b128 v[2:5], v192
	ds_read_b128 v[6:9], v192 offset:1024
	ds_read_b128 v[10:13], v192 offset:2048
	ds_read_b128 v[14:17], v192 offset:3072
	s_add_u32 s30, s28, 0x8000
	s_addc_u32 s31, s29, 0
	s_cmp_eq_u32 s65, 12
	s_cselect_b32 s42, s22, s30
	s_cselect_b32 s43, s23, s31
	s_cselect_b32 s40, s24, s19
	s_cselect_b32 s41, s25, s21
	s_add_u32 s30, s42, 0x8000
	s_addc_u32 s31, s43, 0
	s_add_i32 m0, s27, 0xc000
	ds_read_b128 v[196:199], v193
	ds_read_b128 v[200:203], v193 offset:1024
	ds_read_b128 v[204:207], v193 offset:2048
	ds_read_b128 v[208:211], v193 offset:3072
	ds_read_b128 v[212:215], v193 offset:4096
	ds_read_b128 v[216:219], v193 offset:5120
	ds_read_b128 v[220:223], v193 offset:6144
	ds_read_b128 v[224:227], v193 offset:7168
	global_load_lds_dwordx4 v182, s[28:29]
	s_add_i32 m0, s27, 0xe000
	s_nop 0
	global_load_lds_dwordx4 v180, s[28:29]
	s_waitcnt vmcnt(8)
	s_waitcnt lgkmcnt(0)
	s_setprio 1
	v_mfma_f32_16x16x128_f8f6f4 v[158:161], v[18:25], v[196:203], v[158:161]
	v_mfma_f32_16x16x128_f8f6f4 v[154:157], v[26:33], v[196:203], v[154:157]
	v_mfma_f32_16x16x128_f8f6f4 v[150:153], v[18:25], v[204:211], v[150:153]
	v_mfma_f32_16x16x128_f8f6f4 v[146:149], v[26:33], v[204:211], v[146:149]
	v_mfma_f32_16x16x128_f8f6f4 v[130:133], v[18:25], v[212:219], v[130:133]
	v_mfma_f32_16x16x128_f8f6f4 v[122:125], v[26:33], v[212:219], v[122:125]
	v_mfma_f32_16x16x128_f8f6f4 v[114:117], v[18:25], v[220:227], v[114:117]
	v_mfma_f32_16x16x128_f8f6f4 v[106:109], v[26:33], v[220:227], v[106:109]
	s_nop 3
	s_setprio 0
	s_setprio 1
	v_mfma_f32_16x16x128_f8f6f4 v[142:145], v[2:9], v[196:203], v[142:145]
	v_mfma_f32_16x16x128_f8f6f4 v[138:141], v[10:17], v[196:203], v[138:141]
	v_mfma_f32_16x16x128_f8f6f4 v[134:137], v[2:9], v[204:211], v[134:137]
	v_mfma_f32_16x16x128_f8f6f4 v[126:129], v[10:17], v[204:211], v[126:129]
	v_mfma_f32_16x16x128_f8f6f4 v[118:121], v[2:9], v[212:219], v[118:121]
	v_mfma_f32_16x16x128_f8f6f4 v[110:113], v[10:17], v[212:219], v[110:113]
	v_mfma_f32_16x16x128_f8f6f4 v[102:105], v[2:9], v[220:227], v[102:105]
	v_mfma_f32_16x16x128_f8f6f4 v[98:101], v[10:17], v[220:227], v[98:101]
	s_setprio 0
	s_barrier
; #define PG8_STAGE(bufoff, gbase, voff) do { _Pragma("unroll") for (int _i = 0; _i < 2; ++_i) \
;         __builtin_amdgcn_global_load_lds((const unsigned*)((const char*)(gbase) + (voff)[_i]), (PG8_LAS unsigned*)(lds + (bufoff) + ldsw + _i * 8192), 16, 0, 0); } while (0)
; #define PG8_WAIT_V(n) asm volatile("s_waitcnt vmcnt(" #n ")" ::: "memory")
; #define PG8_WAIT_L(n) asm volatile("s_waitcnt lgkmcnt(" #n ")" ::: "memory")
; #define PG8_BAR __builtin_amdgcn_s_barrier()
; #define PG8_SCHED __builtin_amdgcn_sched_barrier(0)
; template <class Epi, class Sched, bool ALIGN_EPI = true, bool F8 = false>
; __device__ __forceinline__ void gemm_phase(PG8_LAS unsigned char* lds, const Sched& S, const Epi& E) {
;     ...
;             PG8_LDB(B0, 0, 0); PG8_LDB(B1, 0, 1); PG8_SCHED; PG8_LDA(At, 0, 0); PG8_STAGE(PG8_SA(1, 1), a1, voffA[1]);
;             PG8_WAIT_V(8); PG8_WAIT_L(0); PG8_BAR; PG8_MMA(0, 0, At, B0); PG8_MMA(0, 1, At, B1); PG8_BAR; PG8_SCHED;
;             PG8_LDA(At, 0, 1); PG8_STAGE(PG8_SB(0, 0), b2, voffB[0]); PG8_STAGE(PG8_SB(0, 1), b2, voffB[1]); PG8_STAGE(PG8_SA(0, 0), a2, vA2[0]);
;             PG8_WAIT_V(8); PG8_WAIT_L(0); PG8_BAR; PG8_MMA(1, 0, At, B0); PG8_MMA(1, 1, At, B1); PG8_BAR; PG8_SCHED;
;             PG8_LDB(B0, 1, 0); PG8_LDB(B1, 1, 1); PG8_SCHED; PG8_LDA(At, 1, 0); PG8_STAGE(PG8_SA(0, 1), a2, vA2[1]);
;             PG8_WAIT_V(8); PG8_WAIT_L(0); PG8_BAR; PG8_MMA(0, 0, At, B0); PG8_MMA(0, 1, At, B1); PG8_BAR; PG8_SCHED;
;             PG8_LDA(At, 1, 1); PG8_STAGE(PG8_SB(1, 0), b3, voffB[0]); PG8_STAGE(PG8_SB(1, 1), b3, voffB[1]); PG8_STAGE(PG8_SA(1, 0), a3, vA2[0]);
;             PG8_WAIT_V(8); PG8_WAIT_L(0); PG8_BAR; PG8_MMA(1, 0, At, B0); PG8_MMA(1, 1, At, B1); PG8_BAR; PG8_SCHED;
	s_add_i32 s66, s60, s48
	s_mov_b32 m0, s66
	ds_read_b128 v[196:199], v193 offset:16384
	ds_read_b128 v[200:203], v193 offset:17408
	ds_read_b128 v[204:207], v193 offset:18432
	ds_read_b128 v[208:211], v193 offset:19456
	ds_read_b128 v[212:215], v193 offset:20480
	ds_read_b128 v[216:219], v193 offset:21504
	ds_read_b128 v[220:223], v193 offset:22528
	ds_read_b128 v[224:227], v193 offset:23552
	global_load_lds_dwordx4 v162, s[40:41]
	s_add_i32 m0, s66, 0x2000
	s_add_i32 s66, s61, s48
	global_load_lds_dwordx4 v164, s[40:41]
	s_add_u32 s98, s40, s6
	s_addc_u32 s99, s41, s7
	s_mov_b32 m0, s66
	s_nop 0
	global_load_lds_dwordx4 v162, s[98:99]
	s_add_u32 s100, s40, s6
	s_addc_u32 s101, s41, s7
	s_add_i32 m0, s66, 0x2000
	s_nop 0
	global_load_lds_dwordx4 v164, s[100:101]
	s_mov_b32 m0, s27
	s_nop 0
	global_load_lds_dwordx4 v166, s[42:43]
	s_mov_b32 m0, s49
	s_nop 0
	global_load_lds_dwordx4 v168, s[42:43]
	s_waitcnt vmcnt(8)
	s_waitcnt lgkmcnt(0)
	s_setprio 1
	v_mfma_f32_16x16x128_f8f6f4 v[94:97], v[18:25], v[196:203], v[94:97]
	v_mfma_f32_16x16x128_f8f6f4 v[90:93], v[26:33], v[196:203], v[90:93]
	v_mfma_f32_16x16x128_f8f6f4 v[82:85], v[18:25], v[204:211], v[82:85]
	v_mfma_f32_16x16x128_f8f6f4 v[74:77], v[26:33], v[204:211], v[74:77]
	v_mfma_f32_16x16x128_f8f6f4 v[66:69], v[18:25], v[212:219], v[66:69]
	v_mfma_f32_16x16x128_f8f6f4 v[58:61], v[26:33], v[212:219], v[58:61]
	v_mfma_f32_16x16x128_f8f6f4 v[50:53], v[18:25], v[220:227], v[50:53]
	v_mfma_f32_16x16x128_f8f6f4 v[42:45], v[26:33], v[220:227], v[42:45]
	s_nop 3
	s_setprio 0
	s_setprio 1
	v_mfma_f32_16x16x128_f8f6f4 v[86:89], v[2:9], v[196:203], v[86:89]
	v_mfma_f32_16x16x128_f8f6f4 v[78:81], v[10:17], v[196:203], v[78:81]
	v_mfma_f32_16x16x128_f8f6f4 v[70:73], v[2:9], v[204:211], v[70:73]
	v_mfma_f32_16x16x128_f8f6f4 v[62:65], v[10:17], v[204:211], v[62:65]
	v_mfma_f32_16x16x128_f8f6f4 v[54:57], v[2:9], v[212:219], v[54:57]
	v_mfma_f32_16x16x128_f8f6f4 v[46:49], v[10:17], v[212:219], v[46:49]
	v_mfma_f32_16x16x128_f8f6f4 v[38:41], v[2:9], v[220:227], v[38:41]
	v_mfma_f32_16x16x128_f8f6f4 v[34:37], v[10:17], v[220:227], v[34:37]
	s_setprio 0
	s_barrier
	s_add_i32 s66, 0, 0x18000
	s_add_i32 s67, 0, 0x1c000
	v_add_u32_e32 v14, s66, v189
	v_add_u32_e32 v30, s67, v189
	ds_read_b128 v[2:5], v14
	ds_read_b128 v[6:9], v14 offset:1024
	ds_read_b128 v[10:13], v14 offset:2048
	ds_read_b128 v[14:17], v14 offset:3072
	ds_read_b128 v[18:21], v30
	ds_read_b128 v[22:25], v30 offset:1024
	ds_read_b128 v[26:29], v30 offset:2048
	ds_read_b128 v[30:33], v30 offset:3072
	s_mov_b32 m0, s50
	ds_read_b128 v[196:199], v193 offset:32768
	ds_read_b128 v[200:203], v193 offset:33792
	ds_read_b128 v[204:207], v193 offset:34816
	ds_read_b128 v[208:211], v193 offset:35840
	ds_read_b128 v[212:215], v193 offset:36864
	ds_read_b128 v[216:219], v193 offset:37888
	ds_read_b128 v[220:223], v193 offset:38912
	ds_read_b128 v[224:227], v193 offset:39936
	global_load_lds_dwordx4 v172, s[42:43]
	s_mov_b32 m0, s51
	s_nop 0
	global_load_lds_dwordx4 v174, s[42:43]
	s_waitcnt vmcnt(8)
	s_waitcnt lgkmcnt(0)
	s_setprio 1
	v_mfma_f32_16x16x128_f8f6f4 v[158:161], v[2:9], v[196:203], v[158:161]
	v_mfma_f32_16x16x128_f8f6f4 v[154:157], v[10:17], v[196:203], v[154:157]
	v_mfma_f32_16x16x128_f8f6f4 v[150:153], v[2:9], v[204:211], v[150:153]
	v_mfma_f32_16x16x128_f8f6f4 v[146:149], v[10:17], v[204:211], v[146:149]
	v_mfma_f32_16x16x128_f8f6f4 v[130:133], v[2:9], v[212:219], v[130:133]
	v_mfma_f32_16x16x128_f8f6f4 v[122:125], v[10:17], v[212:219], v[122:125]
	v_mfma_f32_16x16x128_f8f6f4 v[114:117], v[2:9], v[220:227], v[114:117]
	v_mfma_f32_16x16x128_f8f6f4 v[106:109], v[10:17], v[220:227], v[106:109]
	s_nop 3
	s_setprio 0
	s_setprio 1
	v_mfma_f32_16x16x128_f8f6f4 v[142:145], v[18:25], v[196:203], v[142:145]
	v_mfma_f32_16x16x128_f8f6f4 v[138:141], v[26:33], v[196:203], v[138:141]
	v_mfma_f32_16x16x128_f8f6f4 v[134:137], v[18:25], v[204:211], v[134:137]
	v_mfma_f32_16x16x128_f8f6f4 v[126:129], v[26:33], v[204:211], v[126:129]
	v_mfma_f32_16x16x128_f8f6f4 v[118:121], v[18:25], v[212:219], v[118:121]
	v_mfma_f32_16x16x128_f8f6f4 v[110:113], v[26:33], v[212:219], v[110:113]
	v_mfma_f32_16x16x128_f8f6f4 v[102:105], v[18:25], v[220:227], v[102:105]
	v_mfma_f32_16x16x128_f8f6f4 v[98:101], v[26:33], v[220:227], v[98:101]
	s_setprio 0
	s_barrier
	s_add_u32 s40, s40, 0x8000
	s_addc_u32 s41, s41, 0
	s_add_i32 s42, s66, s48
	s_mov_b32 m0, s42
	ds_read_b128 v[196:199], v193 offset:49152
	ds_read_b128 v[200:203], v193 offset:50176
	ds_read_b128 v[204:207], v193 offset:51200
	ds_read_b128 v[208:211], v193 offset:52224
	ds_read_b128 v[212:215], v193 offset:53248
	ds_read_b128 v[216:219], v193 offset:54272
	ds_read_b128 v[220:223], v193 offset:55296
	ds_read_b128 v[224:227], v193 offset:56320
	global_load_lds_dwordx4 v162, s[40:41]
	s_add_i32 m0, s42, 0x2000
	s_add_i32 s42, s67, s48
	global_load_lds_dwordx4 v164, s[40:41]
	s_mov_b32 m0, s42
	s_nop 0
	global_load_lds_dwordx4 v176, s[40:41]
	s_add_i32 m0, s42, 0x2000
	s_nop 0
	global_load_lds_dwordx4 v178, s[40:41]
	s_mov_b32 m0, s53
	s_nop 0
	global_load_lds_dwordx4 v166, s[30:31]
	s_mov_b32 m0, s58
	s_nop 0
	global_load_lds_dwordx4 v168, s[30:31]
	s_waitcnt vmcnt(8)
	s_waitcnt lgkmcnt(0)
	s_setprio 1
	v_mfma_f32_16x16x128_f8f6f4 v[94:97], v[2:9], v[196:203], v[94:97]
	v_mfma_f32_16x16x128_f8f6f4 v[90:93], v[10:17], v[196:203], v[90:93]
	v_mfma_f32_16x16x128_f8f6f4 v[82:85], v[2:9], v[204:211], v[82:85]
	v_mfma_f32_16x16x128_f8f6f4 v[74:77], v[10:17], v[204:211], v[74:77]
	v_mfma_f32_16x16x128_f8f6f4 v[66:69], v[2:9], v[212:219], v[66:69]
	v_mfma_f32_16x16x128_f8f6f4 v[58:61], v[10:17], v[212:219], v[58:61]
	v_mfma_f32_16x16x128_f8f6f4 v[50:53], v[2:9], v[220:227], v[50:53]
	v_mfma_f32_16x16x128_f8f6f4 v[42:45], v[10:17], v[220:227], v[42:45]
	s_nop 3
	s_setprio 0
	s_setprio 1
	v_mfma_f32_16x16x128_f8f6f4 v[86:89], v[18:25], v[196:203], v[86:89]
	v_mfma_f32_16x16x128_f8f6f4 v[78:81], v[26:33], v[196:203], v[78:81]
	v_mfma_f32_16x16x128_f8f6f4 v[70:73], v[18:25], v[204:211], v[70:73]
	v_mfma_f32_16x16x128_f8f6f4 v[62:65], v[26:33], v[204:211], v[62:65]
	v_mfma_f32_16x16x128_f8f6f4 v[54:57], v[18:25], v[212:219], v[54:57]
	v_mfma_f32_16x16x128_f8f6f4 v[46:49], v[26:33], v[212:219], v[46:49]
	v_mfma_f32_16x16x128_f8f6f4 v[38:41], v[18:25], v[220:227], v[38:41]
	v_mfma_f32_16x16x128_f8f6f4 v[34:37], v[26:33], v[220:227], v[34:37]
	s_setprio 0
	s_barrier
	s_add_i32 s65, s65, 2
	s_add_u32 s19, s19, 0x10000
	s_addc_u32 s21, s21, 0
	s_add_u32 s28, s28, 0x10000
	s_addc_u32 s29, s29, 0
	s_cmp_gt_u32 s65, 13
	s_cbranch_scc0 .LBB0_911
	s_branch .Lfx_26630
; #define PG8_STAGE(bufoff, gbase, voff) do { _Pragma("unroll") for (int _i = 0; _i < 2; ++_i) \
;         __builtin_amdgcn_global_load_lds((const unsigned*)((const char*)(gbase) + (voff)[_i]), (PG8_LAS unsigned*)(lds + (bufoff) + ldsw + _i * 8192), 16, 0, 0); } while (0)
; #define PG8_WAIT_V(n) asm volatile("s_waitcnt vmcnt(" #n ")" ::: "memory")
; #define PG8_WAIT_L(n) asm volatile("s_waitcnt lgkmcnt(" #n ")" ::: "memory")
; #define PG8_BAR __builtin_amdgcn_s_barrier()
; #define PG8_SCHED __builtin_amdgcn_sched_barrier(0)
; template <class Epi, class Sched, bool ALIGN_EPI = true, bool F8 = false>
; __device__ __forceinline__ void gemm_phase(PG8_LAS unsigned char* lds, const Sched& S, const Epi& E) {
;     ...
;             PG8_LDB(B0, 0, 0); PG8_LDB(B1, 0, 1); PG8_SCHED; PG8_LDA(At, 0, 0); PG8_STAGE(PG8_SA(1, 1), a1, voffA[1]);
;             PG8_WAIT_V(8); PG8_WAIT_L(0); PG8_BAR; PG8_MMA(0, 0, At, B0); PG8_MMA(0, 1, At, B1); PG8_BAR; PG8_SCHED;
;             PG8_LDA(At, 0, 1); PG8_STAGE(PG8_SB(0, 0), b2, voffB[0]); PG8_STAGE(PG8_SB(0, 1), b2, voffB[1]); PG8_STAGE(PG8_SA(0, 0), a2, vA2[0]);
;             PG8_WAIT_V(8); PG8_WAIT_L(0); PG8_BAR; PG8_MMA(1, 0, At, B0); PG8_MMA(1, 1, At, B1); PG8_BAR; PG8_SCHED;
;             PG8_LDB(B0, 1, 0); PG8_LDB(B1, 1, 1); PG8_SCHED; PG8_LDA(At, 1, 0); PG8_STAGE(PG8_SA(0, 1), a2, vA2[1]);
;             PG8_WAIT_V(8); PG8_WAIT_L(0); PG8_BAR; PG8_MMA(0, 0, At, B0); PG8_MMA(0, 1, At, B1); PG8_BAR; PG8_SCHED;
;             PG8_LDA(At, 1, 1); PG8_STAGE(PG8_SB(1, 0), b3, voffB[0]); PG8_STAGE(PG8_SB(1, 1), b3, voffB[1]); PG8_STAGE(PG8_SA(1, 0), a3, vA2[0]);
;             PG8_WAIT_V(8); PG8_WAIT_L(0); PG8_BAR; PG8_MMA(1, 0, At, B0); PG8_MMA(1, 1, At, B1); PG8_BAR; PG8_SCHED;
.Lh1e_26630:
.Lpk1_911:
	ds_read_b128 v[18:21], v191
	ds_read_b128 v[22:25], v191 offset:1024
	ds_read_b128 v[26:29], v191 offset:2048
	ds_read_b128 v[30:33], v191 offset:3072
	ds_read_b128 v[2:5], v192
	ds_read_b128 v[6:9], v192 offset:1024
	ds_read_b128 v[10:13], v192 offset:2048
	ds_read_b128 v[14:17], v192 offset:3072
	s_add_u32 s30, s28, 0x8000
	s_addc_u32 s31, s29, 0
	s_cmp_eq_u32 s65, 12
	s_cselect_b32 s42, s22, s30
	s_cselect_b32 s43, s23, s31
	s_cselect_b32 s40, s24, s19
	s_cselect_b32 s41, s25, s21
	s_add_u32 s30, s42, 0x8000
	s_addc_u32 s31, s43, 0
	s_add_i32 m0, s27, 0xc000
	ds_read_b128 v[196:199], v193
	ds_read_b128 v[200:203], v193 offset:1024
	ds_read_b128 v[204:207], v193 offset:2048
	ds_read_b128 v[208:211], v193 offset:3072
	ds_read_b128 v[212:215], v193 offset:4096
	ds_read_b128 v[216:219], v193 offset:5120
	ds_read_b128 v[220:223], v193 offset:6144
	ds_read_b128 v[224:227], v193 offset:7168
	global_load_lds_dwordx4 v182, s[28:29]
	s_add_i32 m0, s27, 0xe000
	s_nop 0
	global_load_lds_dwordx4 v180, s[28:29]
	s_waitcnt vmcnt(8)
	s_waitcnt lgkmcnt(0)
	s_barrier
	s_setprio 2
	v_mfma_f32_16x16x128_f8f6f4 v[158:161], v[18:25], v[196:203], 0
	v_mfma_f32_16x16x128_f8f6f4 v[154:157], v[26:33], v[196:203], 0
	v_mfma_f32_16x16x128_f8f6f4 v[150:153], v[18:25], v[204:211], 0
	v_mfma_f32_16x16x128_f8f6f4 v[146:149], v[26:33], v[204:211], 0
	v_mfma_f32_16x16x128_f8f6f4 v[130:133], v[18:25], v[212:219], 0
	v_mfma_f32_16x16x128_f8f6f4 v[122:125], v[26:33], v[212:219], 0
	v_mfma_f32_16x16x128_f8f6f4 v[114:117], v[18:25], v[220:227], 0
	v_mfma_f32_16x16x128_f8f6f4 v[106:109], v[26:33], v[220:227], 0
	s_nop 3
	s_setprio 0
	s_setprio 2
	v_mfma_f32_16x16x128_f8f6f4 v[142:145], v[2:9], v[196:203], 0
	v_mfma_f32_16x16x128_f8f6f4 v[138:141], v[10:17], v[196:203], 0
	v_mfma_f32_16x16x128_f8f6f4 v[134:137], v[2:9], v[204:211], 0
	v_mfma_f32_16x16x128_f8f6f4 v[126:129], v[10:17], v[204:211], 0
	v_mfma_f32_16x16x128_f8f6f4 v[118:121], v[2:9], v[212:219], 0
	v_mfma_f32_16x16x128_f8f6f4 v[110:113], v[10:17], v[212:219], 0
	v_mfma_f32_16x16x128_f8f6f4 v[102:105], v[2:9], v[220:227], 0
	v_mfma_f32_16x16x128_f8f6f4 v[98:101], v[10:17], v[220:227], 0
	s_setprio 0
	s_add_i32 s66, s60, s48
	s_mov_b32 m0, s66
	ds_read_b128 v[196:199], v193 offset:16384
	ds_read_b128 v[200:203], v193 offset:17408
	ds_read_b128 v[204:207], v193 offset:18432
	ds_read_b128 v[208:211], v193 offset:19456
	ds_read_b128 v[212:215], v193 offset:20480
	ds_read_b128 v[216:219], v193 offset:21504
	ds_read_b128 v[220:223], v193 offset:22528
	ds_read_b128 v[224:227], v193 offset:23552
	global_load_lds_dwordx4 v162, s[40:41]
	s_add_i32 m0, s66, 0x2000
	s_add_i32 s66, s61, s48
	global_load_lds_dwordx4 v164, s[40:41]
	s_add_u32 s98, s40, s6
	s_addc_u32 s99, s41, s7
	s_mov_b32 m0, s66
	s_nop 0
	global_load_lds_dwordx4 v162, s[98:99]
	s_add_u32 s100, s40, s6
	s_addc_u32 s101, s41, s7
	s_add_i32 m0, s66, 0x2000
	s_nop 0
	global_load_lds_dwordx4 v164, s[100:101]
	s_mov_b32 m0, s27
	s_nop 0
	global_load_lds_dwordx4 v166, s[42:43]
	s_mov_b32 m0, s49
	s_nop 0
	global_load_lds_dwordx4 v168, s[42:43]
	s_waitcnt vmcnt(8)
	s_waitcnt lgkmcnt(0)
	s_barrier
	s_setprio 2
	v_mfma_f32_16x16x128_f8f6f4 v[94:97], v[18:25], v[196:203], 0
	v_mfma_f32_16x16x128_f8f6f4 v[90:93], v[26:33], v[196:203], 0
	v_mfma_f32_16x16x128_f8f6f4 v[82:85], v[18:25], v[204:211], 0
	v_mfma_f32_16x16x128_f8f6f4 v[74:77], v[26:33], v[204:211], 0
	v_mfma_f32_16x16x128_f8f6f4 v[66:69], v[18:25], v[212:219], 0
	v_mfma_f32_16x16x128_f8f6f4 v[58:61], v[26:33], v[212:219], 0
	v_mfma_f32_16x16x128_f8f6f4 v[50:53], v[18:25], v[220:227], 0
	v_mfma_f32_16x16x128_f8f6f4 v[42:45], v[26:33], v[220:227], 0
	s_nop 3
	s_setprio 0
	s_setprio 2
	v_mfma_f32_16x16x128_f8f6f4 v[86:89], v[2:9], v[196:203], 0
	v_mfma_f32_16x16x128_f8f6f4 v[78:81], v[10:17], v[196:203], 0
	v_mfma_f32_16x16x128_f8f6f4 v[70:73], v[2:9], v[204:211], 0
	v_mfma_f32_16x16x128_f8f6f4 v[62:65], v[10:17], v[204:211], 0
	v_mfma_f32_16x16x128_f8f6f4 v[54:57], v[2:9], v[212:219], 0
	v_mfma_f32_16x16x128_f8f6f4 v[46:49], v[10:17], v[212:219], 0
	v_mfma_f32_16x16x128_f8f6f4 v[38:41], v[2:9], v[220:227], 0
	v_mfma_f32_16x16x128_f8f6f4 v[34:37], v[10:17], v[220:227], 0
	s_setprio 0
	s_add_i32 s66, 0, 0x18000
	s_add_i32 s67, 0, 0x1c000
	v_add_u32_e32 v14, s66, v189
	v_add_u32_e32 v30, s67, v189
	ds_read_b128 v[2:5], v14
	ds_read_b128 v[6:9], v14 offset:1024
	ds_read_b128 v[10:13], v14 offset:2048
	ds_read_b128 v[14:17], v14 offset:3072
	ds_read_b128 v[18:21], v30
	ds_read_b128 v[22:25], v30 offset:1024
	ds_read_b128 v[26:29], v30 offset:2048
	ds_read_b128 v[30:33], v30 offset:3072
	s_mov_b32 m0, s50
	ds_read_b128 v[196:199], v193 offset:32768
	ds_read_b128 v[200:203], v193 offset:33792
	ds_read_b128 v[204:207], v193 offset:34816
	ds_read_b128 v[208:211], v193 offset:35840
	ds_read_b128 v[212:215], v193 offset:36864
	ds_read_b128 v[216:219], v193 offset:37888
	ds_read_b128 v[220:223], v193 offset:38912
	ds_read_b128 v[224:227], v193 offset:39936
	global_load_lds_dwordx4 v172, s[42:43]
	s_mov_b32 m0, s51
	s_nop 0
	global_load_lds_dwordx4 v174, s[42:43]
	s_waitcnt vmcnt(8)
	s_waitcnt lgkmcnt(0)
	s_barrier
; #define PG8_STAGE(bufoff, gbase, voff) do { _Pragma("unroll") for (int _i = 0; _i < 2; ++_i) \
;         __builtin_amdgcn_global_load_lds((const unsigned*)((const char*)(gbase) + (voff)[_i]), (PG8_LAS unsigned*)(lds + (bufoff) + ldsw + _i * 8192), 16, 0, 0); } while (0)
; #define PG8_WAIT_V(n) asm volatile("s_waitcnt vmcnt(" #n ")" ::: "memory")
; #define PG8_WAIT_L(n) asm volatile("s_waitcnt lgkmcnt(" #n ")" ::: "memory")
; #define PG8_BAR __builtin_amdgcn_s_barrier()
; #define PG8_SCHED __builtin_amdgcn_sched_barrier(0)
; template <class Epi, class Sched, bool ALIGN_EPI = true, bool F8 = false>
; __device__ __forceinline__ void gemm_phase(PG8_LAS unsigned char* lds, const Sched& S, const Epi& E) {
;     ...
;             PG8_LDB(B0, 0, 0); PG8_LDB(B1, 0, 1); PG8_SCHED; PG8_LDA(At, 0, 0); PG8_STAGE(PG8_SA(1, 1), a1, voffA[1]);
;             PG8_WAIT_V(8); PG8_WAIT_L(0); PG8_BAR; PG8_MMA(0, 0, At, B0); PG8_MMA(0, 1, At, B1); PG8_BAR; PG8_SCHED;
;             PG8_LDA(At, 0, 1); PG8_STAGE(PG8_SB(0, 0), b2, voffB[0]); PG8_STAGE(PG8_SB(0, 1), b2, voffB[1]); PG8_STAGE(PG8_SA(0, 0), a2, vA2[0]);
;             PG8_WAIT_V(8); PG8_WAIT_L(0); PG8_BAR; PG8_MMA(1, 0, At, B0); PG8_MMA(1, 1, At, B1); PG8_BAR; PG8_SCHED;
;             PG8_LDB(B0, 1, 0); PG8_LDB(B1, 1, 1); PG8_SCHED; PG8_LDA(At, 1, 0); PG8_STAGE(PG8_SA(0, 1), a2, vA2[1]);
;             PG8_WAIT_V(8); PG8_WAIT_L(0); PG8_BAR; PG8_MMA(0, 0, At, B0); PG8_MMA(0, 1, At, B1); PG8_BAR; PG8_SCHED;
;             PG8_LDA(At, 1, 1); PG8_STAGE(PG8_SB(1, 0), b3, voffB[0]); PG8_STAGE(PG8_SB(1, 1), b3, voffB[1]); PG8_STAGE(PG8_SA(1, 0), a3, vA2[0]);
;             PG8_WAIT_V(8); PG8_WAIT_L(0); PG8_BAR; PG8_MMA(1, 0, At, B0); PG8_MMA(1, 1, At, B1); PG8_BAR; PG8_SCHED;
	s_setprio 2
	v_mfma_f32_16x16x128_f8f6f4 v[158:161], v[2:9], v[196:203], v[158:161]
	v_mfma_f32_16x16x128_f8f6f4 v[154:157], v[10:17], v[196:203], v[154:157]
	v_mfma_f32_16x16x128_f8f6f4 v[150:153], v[2:9], v[204:211], v[150:153]
	v_mfma_f32_16x16x128_f8f6f4 v[146:149], v[10:17], v[204:211], v[146:149]
	v_mfma_f32_16x16x128_f8f6f4 v[130:133], v[2:9], v[212:219], v[130:133]
	v_mfma_f32_16x16x128_f8f6f4 v[122:125], v[10:17], v[212:219], v[122:125]
	v_mfma_f32_16x16x128_f8f6f4 v[114:117], v[2:9], v[220:227], v[114:117]
	v_mfma_f32_16x16x128_f8f6f4 v[106:109], v[10:17], v[220:227], v[106:109]
	s_nop 3
	s_setprio 0
	s_setprio 2
	v_mfma_f32_16x16x128_f8f6f4 v[142:145], v[18:25], v[196:203], v[142:145]
	v_mfma_f32_16x16x128_f8f6f4 v[138:141], v[26:33], v[196:203], v[138:141]
	v_mfma_f32_16x16x128_f8f6f4 v[134:137], v[18:25], v[204:211], v[134:137]
	v_mfma_f32_16x16x128_f8f6f4 v[126:129], v[26:33], v[204:211], v[126:129]
	v_mfma_f32_16x16x128_f8f6f4 v[118:121], v[18:25], v[212:219], v[118:121]
	v_mfma_f32_16x16x128_f8f6f4 v[110:113], v[26:33], v[212:219], v[110:113]
	v_mfma_f32_16x16x128_f8f6f4 v[102:105], v[18:25], v[220:227], v[102:105]
	v_mfma_f32_16x16x128_f8f6f4 v[98:101], v[26:33], v[220:227], v[98:101]
	s_setprio 0
	s_add_u32 s40, s40, 0x8000
	s_addc_u32 s41, s41, 0
	s_add_i32 s42, s66, s48
	s_mov_b32 m0, s42
	ds_read_b128 v[196:199], v193 offset:49152
	ds_read_b128 v[200:203], v193 offset:50176
	ds_read_b128 v[204:207], v193 offset:51200
	ds_read_b128 v[208:211], v193 offset:52224
	ds_read_b128 v[212:215], v193 offset:53248
	ds_read_b128 v[216:219], v193 offset:54272
	ds_read_b128 v[220:223], v193 offset:55296
	ds_read_b128 v[224:227], v193 offset:56320
	global_load_lds_dwordx4 v162, s[40:41]
	s_add_i32 m0, s42, 0x2000
	s_add_i32 s42, s67, s48
	global_load_lds_dwordx4 v164, s[40:41]
	s_mov_b32 m0, s42
	s_nop 0
	global_load_lds_dwordx4 v176, s[40:41]
	s_add_i32 m0, s42, 0x2000
	s_nop 0
	global_load_lds_dwordx4 v178, s[40:41]
	s_mov_b32 m0, s53
	s_nop 0
	global_load_lds_dwordx4 v166, s[30:31]
	s_mov_b32 m0, s58
	s_nop 0
	global_load_lds_dwordx4 v168, s[30:31]
	s_waitcnt vmcnt(8)
	s_waitcnt lgkmcnt(0)
	s_barrier
	s_setprio 2
	v_mfma_f32_16x16x128_f8f6f4 v[94:97], v[2:9], v[196:203], v[94:97]
	v_mfma_f32_16x16x128_f8f6f4 v[90:93], v[10:17], v[196:203], v[90:93]
	v_mfma_f32_16x16x128_f8f6f4 v[82:85], v[2:9], v[204:211], v[82:85]
	v_mfma_f32_16x16x128_f8f6f4 v[74:77], v[10:17], v[204:211], v[74:77]
	v_mfma_f32_16x16x128_f8f6f4 v[66:69], v[2:9], v[212:219], v[66:69]
	v_mfma_f32_16x16x128_f8f6f4 v[58:61], v[10:17], v[212:219], v[58:61]
	v_mfma_f32_16x16x128_f8f6f4 v[50:53], v[2:9], v[220:227], v[50:53]
	v_mfma_f32_16x16x128_f8f6f4 v[42:45], v[10:17], v[220:227], v[42:45]
	s_nop 3
	s_setprio 0
	s_setprio 2
	v_mfma_f32_16x16x128_f8f6f4 v[86:89], v[18:25], v[196:203], v[86:89]
	v_mfma_f32_16x16x128_f8f6f4 v[78:81], v[26:33], v[196:203], v[78:81]
	v_mfma_f32_16x16x128_f8f6f4 v[70:73], v[18:25], v[204:211], v[70:73]
	v_mfma_f32_16x16x128_f8f6f4 v[62:65], v[26:33], v[204:211], v[62:65]
	v_mfma_f32_16x16x128_f8f6f4 v[54:57], v[18:25], v[212:219], v[54:57]
	v_mfma_f32_16x16x128_f8f6f4 v[46:49], v[26:33], v[212:219], v[46:49]
	v_mfma_f32_16x16x128_f8f6f4 v[38:41], v[18:25], v[220:227], v[38:41]
	v_mfma_f32_16x16x128_f8f6f4 v[34:37], v[26:33], v[220:227], v[34:37]
	s_setprio 0
	s_add_i32 s65, s65, 2
	s_add_u32 s19, s19, 0x10000
	s_addc_u32 s21, s21, 0
	s_add_u32 s28, s28, 0x10000
	s_addc_u32 s29, s29, 0
	s_cmp_gt_u32 s65, 13
	s_cbranch_scc0 .Lh1_911
	s_branch .Lfx_26630
.Lh1_911:
	ds_read_b128 v[18:21], v191
	ds_read_b128 v[22:25], v191 offset:1024
	ds_read_b128 v[26:29], v191 offset:2048
	ds_read_b128 v[30:33], v191 offset:3072
	ds_read_b128 v[2:5], v192
	ds_read_b128 v[6:9], v192 offset:1024
	ds_read_b128 v[10:13], v192 offset:2048
	ds_read_b128 v[14:17], v192 offset:3072
	s_add_u32 s30, s28, 0x8000
	s_addc_u32 s31, s29, 0
	s_cmp_eq_u32 s65, 12
	s_cselect_b32 s42, s22, s30
	s_cselect_b32 s43, s23, s31
	s_cselect_b32 s40, s24, s19
	s_cselect_b32 s41, s25, s21
	s_add_u32 s30, s42, 0x8000
	s_addc_u32 s31, s43, 0
	s_add_i32 m0, s27, 0xc000
	ds_read_b128 v[196:199], v193
	ds_read_b128 v[200:203], v193 offset:1024
	ds_read_b128 v[204:207], v193 offset:2048
	ds_read_b128 v[208:211], v193 offset:3072
	ds_read_b128 v[212:215], v193 offset:4096
	ds_read_b128 v[216:219], v193 offset:5120
	ds_read_b128 v[220:223], v193 offset:6144
	ds_read_b128 v[224:227], v193 offset:7168
	global_load_lds_dwordx4 v182, s[28:29]
	s_add_i32 m0, s27, 0xe000
	s_nop 0
	global_load_lds_dwordx4 v180, s[28:29]
	s_waitcnt vmcnt(8)
	s_waitcnt lgkmcnt(0)
	s_barrier
; #define PG8_STAGE(bufoff, gbase, voff) do { _Pragma("unroll") for (int _i = 0; _i < 2; ++_i) \
;         __builtin_amdgcn_global_load_lds((const unsigned*)((const char*)(gbase) + (voff)[_i]), (PG8_LAS unsigned*)(lds + (bufoff) + ldsw + _i * 8192), 16, 0, 0); } while (0)
; #define PG8_WAIT_V(n) asm volatile("s_waitcnt vmcnt(" #n ")" ::: "memory")
; #define PG8_WAIT_L(n) asm volatile("s_waitcnt lgkmcnt(" #n ")" ::: "memory")
; #define PG8_BAR __builtin_amdgcn_s_barrier()
; #define PG8_SCHED __builtin_amdgcn_sched_barrier(0)
; template <class Epi, class Sched, bool ALIGN_EPI = true, bool F8 = false>
; __device__ __forceinline__ void gemm_phase(PG8_LAS unsigned char* lds, const Sched& S, const Epi& E) {
;     ...
;             PG8_LDB(B0, 0, 0); PG8_LDB(B1, 0, 1); PG8_SCHED; PG8_LDA(At, 0, 0); PG8_STAGE(PG8_SA(1, 1), a1, voffA[1]);
;             PG8_WAIT_V(8); PG8_WAIT_L(0); PG8_BAR; PG8_MMA(0, 0, At, B0); PG8_MMA(0, 1, At, B1); PG8_BAR; PG8_SCHED;
;             PG8_LDA(At, 0, 1); PG8_STAGE(PG8_SB(0, 0), b2, voffB[0]); PG8_STAGE(PG8_SB(0, 1), b2, voffB[1]); PG8_STAGE(PG8_SA(0, 0), a2, vA2[0]);
;             PG8_WAIT_V(8); PG8_WAIT_L(0); PG8_BAR; PG8_MMA(1, 0, At, B0); PG8_MMA(1, 1, At, B1); PG8_BAR; PG8_SCHED;
;             PG8_LDB(B0, 1, 0); PG8_LDB(B1, 1, 1); PG8_SCHED; PG8_LDA(At, 1, 0); PG8_STAGE(PG8_SA(0, 1), a2, vA2[1]);
;             PG8_WAIT_V(8); PG8_WAIT_L(0); PG8_BAR; PG8_MMA(0, 0, At, B0); PG8_MMA(0, 1, At, B1); PG8_BAR; PG8_SCHED;
;             PG8_LDA(At, 1, 1); PG8_STAGE(PG8_SB(1, 0), b3, voffB[0]); PG8_STAGE(PG8_SB(1, 1), b3, voffB[1]); PG8_STAGE(PG8_SA(1, 0), a3, vA2[0]);
;             PG8_WAIT_V(8); PG8_WAIT_L(0); PG8_BAR; PG8_MMA(1, 0, At, B0); PG8_MMA(1, 1, At, B1); PG8_BAR; PG8_SCHED;
	s_setprio 2
	v_mfma_f32_16x16x128_f8f6f4 v[158:161], v[18:25], v[196:203], v[158:161]
	v_mfma_f32_16x16x128_f8f6f4 v[154:157], v[26:33], v[196:203], v[154:157]
	v_mfma_f32_16x16x128_f8f6f4 v[150:153], v[18:25], v[204:211], v[150:153]
	v_mfma_f32_16x16x128_f8f6f4 v[146:149], v[26:33], v[204:211], v[146:149]
	v_mfma_f32_16x16x128_f8f6f4 v[130:133], v[18:25], v[212:219], v[130:133]
	v_mfma_f32_16x16x128_f8f6f4 v[122:125], v[26:33], v[212:219], v[122:125]
	v_mfma_f32_16x16x128_f8f6f4 v[114:117], v[18:25], v[220:227], v[114:117]
	v_mfma_f32_16x16x128_f8f6f4 v[106:109], v[26:33], v[220:227], v[106:109]
	s_nop 3
	s_setprio 0
	s_setprio 2
	v_mfma_f32_16x16x128_f8f6f4 v[142:145], v[2:9], v[196:203], v[142:145]
	v_mfma_f32_16x16x128_f8f6f4 v[138:141], v[10:17], v[196:203], v[138:141]
	v_mfma_f32_16x16x128_f8f6f4 v[134:137], v[2:9], v[204:211], v[134:137]
	v_mfma_f32_16x16x128_f8f6f4 v[126:129], v[10:17], v[204:211], v[126:129]
	v_mfma_f32_16x16x128_f8f6f4 v[118:121], v[2:9], v[212:219], v[118:121]
	v_mfma_f32_16x16x128_f8f6f4 v[110:113], v[10:17], v[212:219], v[110:113]
	v_mfma_f32_16x16x128_f8f6f4 v[102:105], v[2:9], v[220:227], v[102:105]
	v_mfma_f32_16x16x128_f8f6f4 v[98:101], v[10:17], v[220:227], v[98:101]
	s_setprio 0
	s_add_i32 s66, s60, s48
	s_mov_b32 m0, s66
	ds_read_b128 v[196:199], v193 offset:16384
	ds_read_b128 v[200:203], v193 offset:17408
	ds_read_b128 v[204:207], v193 offset:18432
	ds_read_b128 v[208:211], v193 offset:19456
	ds_read_b128 v[212:215], v193 offset:20480
	ds_read_b128 v[216:219], v193 offset:21504
	ds_read_b128 v[220:223], v193 offset:22528
	ds_read_b128 v[224:227], v193 offset:23552
	global_load_lds_dwordx4 v162, s[40:41]
	s_add_i32 m0, s66, 0x2000
	s_add_i32 s66, s61, s48
	global_load_lds_dwordx4 v164, s[40:41]
	s_add_u32 s98, s40, s6
	s_addc_u32 s99, s41, s7
	s_mov_b32 m0, s66
	s_nop 0
	global_load_lds_dwordx4 v162, s[98:99]
	s_add_u32 s100, s40, s6
	s_addc_u32 s101, s41, s7
	s_add_i32 m0, s66, 0x2000
	s_nop 0
	global_load_lds_dwordx4 v164, s[100:101]
	s_mov_b32 m0, s27
	s_nop 0
	global_load_lds_dwordx4 v166, s[42:43]
	s_mov_b32 m0, s49
	s_nop 0
	global_load_lds_dwordx4 v168, s[42:43]
	s_waitcnt vmcnt(8)
	s_waitcnt lgkmcnt(0)
	s_barrier
	s_setprio 2
	v_mfma_f32_16x16x128_f8f6f4 v[94:97], v[18:25], v[196:203], v[94:97]
	v_mfma_f32_16x16x128_f8f6f4 v[90:93], v[26:33], v[196:203], v[90:93]
	v_mfma_f32_16x16x128_f8f6f4 v[82:85], v[18:25], v[204:211], v[82:85]
	v_mfma_f32_16x16x128_f8f6f4 v[74:77], v[26:33], v[204:211], v[74:77]
	v_mfma_f32_16x16x128_f8f6f4 v[66:69], v[18:25], v[212:219], v[66:69]
	v_mfma_f32_16x16x128_f8f6f4 v[58:61], v[26:33], v[212:219], v[58:61]
	v_mfma_f32_16x16x128_f8f6f4 v[50:53], v[18:25], v[220:227], v[50:53]
	v_mfma_f32_16x16x128_f8f6f4 v[42:45], v[26:33], v[220:227], v[42:45]
	s_nop 3
	s_setprio 0
	s_setprio 2
	v_mfma_f32_16x16x128_f8f6f4 v[86:89], v[2:9], v[196:203], v[86:89]
	v_mfma_f32_16x16x128_f8f6f4 v[78:81], v[10:17], v[196:203], v[78:81]
	v_mfma_f32_16x16x128_f8f6f4 v[70:73], v[2:9], v[204:211], v[70:73]
	v_mfma_f32_16x16x128_f8f6f4 v[62:65], v[10:17], v[204:211], v[62:65]
	v_mfma_f32_16x16x128_f8f6f4 v[54:57], v[2:9], v[212:219], v[54:57]
	v_mfma_f32_16x16x128_f8f6f4 v[46:49], v[10:17], v[212:219], v[46:49]
	v_mfma_f32_16x16x128_f8f6f4 v[38:41], v[2:9], v[220:227], v[38:41]
	v_mfma_f32_16x16x128_f8f6f4 v[34:37], v[10:17], v[220:227], v[34:37]
	s_setprio 0
	s_add_i32 s66, 0, 0x18000
	s_add_i32 s67, 0, 0x1c000
	v_add_u32_e32 v14, s66, v189
	v_add_u32_e32 v30, s67, v189
	ds_read_b128 v[2:5], v14
	ds_read_b128 v[6:9], v14 offset:1024
	ds_read_b128 v[10:13], v14 offset:2048
	ds_read_b128 v[14:17], v14 offset:3072
	ds_read_b128 v[18:21], v30
	ds_read_b128 v[22:25], v30 offset:1024
	ds_read_b128 v[26:29], v30 offset:2048
	ds_read_b128 v[30:33], v30 offset:3072
	s_mov_b32 m0, s50
	ds_read_b128 v[196:199], v193 offset:32768
	ds_read_b128 v[200:203], v193 offset:33792
	ds_read_b128 v[204:207], v193 offset:34816
	ds_read_b128 v[208:211], v193 offset:35840
	ds_read_b128 v[212:215], v193 offset:36864
	ds_read_b128 v[216:219], v193 offset:37888
	ds_read_b128 v[220:223], v193 offset:38912
	ds_read_b128 v[224:227], v193 offset:39936
	global_load_lds_dwordx4 v172, s[42:43]
	s_mov_b32 m0, s51
	s_nop 0
	global_load_lds_dwordx4 v174, s[42:43]
	s_waitcnt vmcnt(8)
	s_waitcnt lgkmcnt(0)
	s_barrier
; #define PG8_STAGE(bufoff, gbase, voff) do { _Pragma("unroll") for (int _i = 0; _i < 2; ++_i) \
;         __builtin_amdgcn_global_load_lds((const unsigned*)((const char*)(gbase) + (voff)[_i]), (PG8_LAS unsigned*)(lds + (bufoff) + ldsw + _i * 8192), 16, 0, 0); } while (0)
; #define PG8_WAIT_V(n) asm volatile("s_waitcnt vmcnt(" #n ")" ::: "memory")
; #define PG8_WAIT_L(n) asm volatile("s_waitcnt lgkmcnt(" #n ")" ::: "memory")
; #define PG8_BAR __builtin_amdgcn_s_barrier()
; #define PG8_SCHED __builtin_amdgcn_sched_barrier(0)
; template <class Epi, class Sched, bool ALIGN_EPI = true, bool F8 = false>
; __device__ __forceinline__ void gemm_phase(PG8_LAS unsigned char* lds, const Sched& S, const Epi& E) {
;     ...
;             PG8_LDB(B0, 0, 0); PG8_LDB(B1, 0, 1); PG8_SCHED; PG8_LDA(At, 0, 0); PG8_STAGE(PG8_SA(1, 1), a1, voffA[1]);
;             PG8_WAIT_V(8); PG8_WAIT_L(0); PG8_BAR; PG8_MMA(0, 0, At, B0); PG8_MMA(0, 1, At, B1); PG8_BAR; PG8_SCHED;
;             PG8_LDA(At, 0, 1); PG8_STAGE(PG8_SB(0, 0), b2, voffB[0]); PG8_STAGE(PG8_SB(0, 1), b2, voffB[1]); PG8_STAGE(PG8_SA(0, 0), a2, vA2[0]);
;             PG8_WAIT_V(8); PG8_WAIT_L(0); PG8_BAR; PG8_MMA(1, 0, At, B0); PG8_MMA(1, 1, At, B1); PG8_BAR; PG8_SCHED;
;             PG8_LDB(B0, 1, 0); PG8_LDB(B1, 1, 1); PG8_SCHED; PG8_LDA(At, 1, 0); PG8_STAGE(PG8_SA(0, 1), a2, vA2[1]);
;             PG8_WAIT_V(8); PG8_WAIT_L(0); PG8_BAR; PG8_MMA(0, 0, At, B0); PG8_MMA(0, 1, At, B1); PG8_BAR; PG8_SCHED;
;             PG8_LDA(At, 1, 1); PG8_STAGE(PG8_SB(1, 0), b3, voffB[0]); PG8_STAGE(PG8_SB(1, 1), b3, voffB[1]); PG8_STAGE(PG8_SA(1, 0), a3, vA2[0]);
;             PG8_WAIT_V(8); PG8_WAIT_L(0); PG8_BAR; PG8_MMA(1, 0, At, B0); PG8_MMA(1, 1, At, B1); PG8_BAR; PG8_SCHED;
	s_setprio 2
	v_mfma_f32_16x16x128_f8f6f4 v[158:161], v[2:9], v[196:203], v[158:161]
	v_mfma_f32_16x16x128_f8f6f4 v[154:157], v[10:17], v[196:203], v[154:157]
	v_mfma_f32_16x16x128_f8f6f4 v[150:153], v[2:9], v[204:211], v[150:153]
	v_mfma_f32_16x16x128_f8f6f4 v[146:149], v[10:17], v[204:211], v[146:149]
	v_mfma_f32_16x16x128_f8f6f4 v[130:133], v[2:9], v[212:219], v[130:133]
	v_mfma_f32_16x16x128_f8f6f4 v[122:125], v[10:17], v[212:219], v[122:125]
	v_mfma_f32_16x16x128_f8f6f4 v[114:117], v[2:9], v[220:227], v[114:117]
	v_mfma_f32_16x16x128_f8f6f4 v[106:109], v[10:17], v[220:227], v[106:109]
	s_nop 3
	s_setprio 0
	s_setprio 2
	v_mfma_f32_16x16x128_f8f6f4 v[142:145], v[18:25], v[196:203], v[142:145]
	v_mfma_f32_16x16x128_f8f6f4 v[138:141], v[26:33], v[196:203], v[138:141]
	v_mfma_f32_16x16x128_f8f6f4 v[134:137], v[18:25], v[204:211], v[134:137]
	v_mfma_f32_16x16x128_f8f6f4 v[126:129], v[26:33], v[204:211], v[126:129]
	v_mfma_f32_16x16x128_f8f6f4 v[118:121], v[18:25], v[212:219], v[118:121]
	v_mfma_f32_16x16x128_f8f6f4 v[110:113], v[26:33], v[212:219], v[110:113]
	v_mfma_f32_16x16x128_f8f6f4 v[102:105], v[18:25], v[220:227], v[102:105]
	v_mfma_f32_16x16x128_f8f6f4 v[98:101], v[26:33], v[220:227], v[98:101]
	s_setprio 0
	s_add_u32 s40, s40, 0x8000
	s_addc_u32 s41, s41, 0
	s_add_i32 s42, s66, s48
	s_mov_b32 m0, s42
	ds_read_b128 v[196:199], v193 offset:49152
	ds_read_b128 v[200:203], v193 offset:50176
	ds_read_b128 v[204:207], v193 offset:51200
	ds_read_b128 v[208:211], v193 offset:52224
	ds_read_b128 v[212:215], v193 offset:53248
	ds_read_b128 v[216:219], v193 offset:54272
	ds_read_b128 v[220:223], v193 offset:55296
	ds_read_b128 v[224:227], v193 offset:56320
	global_load_lds_dwordx4 v162, s[40:41]
	s_add_i32 m0, s42, 0x2000
	s_add_i32 s42, s67, s48
	global_load_lds_dwordx4 v164, s[40:41]
	s_mov_b32 m0, s42
	s_nop 0
	global_load_lds_dwordx4 v176, s[40:41]
	s_add_i32 m0, s42, 0x2000
	s_nop 0
	global_load_lds_dwordx4 v178, s[40:41]
	s_mov_b32 m0, s53
	s_nop 0
	global_load_lds_dwordx4 v166, s[30:31]
	s_mov_b32 m0, s58
	s_nop 0
	global_load_lds_dwordx4 v168, s[30:31]
	s_waitcnt vmcnt(8)
	s_waitcnt lgkmcnt(0)
	s_barrier
	s_setprio 2
	v_mfma_f32_16x16x128_f8f6f4 v[94:97], v[2:9], v[196:203], v[94:97]
	v_mfma_f32_16x16x128_f8f6f4 v[90:93], v[10:17], v[196:203], v[90:93]
	v_mfma_f32_16x16x128_f8f6f4 v[82:85], v[2:9], v[204:211], v[82:85]
	v_mfma_f32_16x16x128_f8f6f4 v[74:77], v[10:17], v[204:211], v[74:77]
	v_mfma_f32_16x16x128_f8f6f4 v[66:69], v[2:9], v[212:219], v[66:69]
	v_mfma_f32_16x16x128_f8f6f4 v[58:61], v[10:17], v[212:219], v[58:61]
	v_mfma_f32_16x16x128_f8f6f4 v[50:53], v[2:9], v[220:227], v[50:53]
	v_mfma_f32_16x16x128_f8f6f4 v[42:45], v[10:17], v[220:227], v[42:45]
	s_nop 3
	s_setprio 0
	s_setprio 2
	v_mfma_f32_16x16x128_f8f6f4 v[86:89], v[18:25], v[196:203], v[86:89]
	v_mfma_f32_16x16x128_f8f6f4 v[78:81], v[26:33], v[196:203], v[78:81]
	v_mfma_f32_16x16x128_f8f6f4 v[70:73], v[18:25], v[204:211], v[70:73]
	v_mfma_f32_16x16x128_f8f6f4 v[62:65], v[26:33], v[204:211], v[62:65]
	v_mfma_f32_16x16x128_f8f6f4 v[54:57], v[18:25], v[212:219], v[54:57]
	v_mfma_f32_16x16x128_f8f6f4 v[46:49], v[26:33], v[212:219], v[46:49]
	v_mfma_f32_16x16x128_f8f6f4 v[38:41], v[18:25], v[220:227], v[38:41]
	v_mfma_f32_16x16x128_f8f6f4 v[34:37], v[26:33], v[220:227], v[34:37]
	s_setprio 0
	s_add_i32 s65, s65, 2
	s_add_u32 s19, s19, 0x10000
	s_addc_u32 s21, s21, 0
	s_add_u32 s28, s28, 0x10000
	s_addc_u32 s29, s29, 0
	s_cmp_gt_u32 s65, 13
	s_cbranch_scc0 .Lh1_911

; #define PG8_STAGE(bufoff, gbase, voff) do { _Pragma("unroll") for (int _i = 0; _i < 2; ++_i) \
;         __builtin_amdgcn_global_load_lds((const unsigned*)((const char*)(gbase) + (voff)[_i]), (PG8_LAS unsigned*)(lds + (bufoff) + ldsw + _i * 8192), 16, 0, 0); } while (0)
; #define PG8_WAIT_V(n) asm volatile("s_waitcnt vmcnt(" #n ")" ::: "memory")
; #define PG8_WAIT_L(n) asm volatile("s_waitcnt lgkmcnt(" #n ")" ::: "memory")
; template <class Epi, class Sched, bool ALIGN_EPI = true, bool F8 = false>
; __device__ __forceinline__ void gemm_phase(PG8_LAS unsigned char* lds, const Sched& S, const Epi& E) {
;     ...
;         for (int t = 0; t < nt; t += 2) {
;             const bool last = (t == nt - 2);
;             if constexpr (Sched::GATHER) { if (last && has_next) S.a_off(nxt, Rs, Cs, voffAn); }
;             const char* a1 = cA + (size_t)(t + 1) * kstep;
;             const char* a2 = last ? nA : cA + (size_t)(t + 2) * kstep; const char* b2 = last ? nB : cB + (size_t)(t + 2) * kstepB;
;             const char* a3 = a2 + kstep; const char* b3 = b2 + kstepB;
;             unsigned vA2[2][2];
; #pragma unroll
;             for (int h = 0; h < 2; ++h)
; #pragma unroll
;                 for (int i = 0; i < 2; ++i) { if constexpr (Sched::GATHER) vA2[h][i] = (last && has_next) ? voffAn[h][i] : voffA[h][i]; else vA2[h][i] = voffA[h][i]; }
;             PG8_LDB(B0, 0, 0); PG8_LDB(B1, 0, 1); PG8_SCHED; PG8_LDA(At, 0, 0); PG8_STAGE(PG8_SA(1, 1), a1, voffA[1]);
;             PG8_WAIT_V(8); PG8_WAIT_L(0); PG8_BAR; PG8_MMA(0, 0, At, B0); PG8_MMA(0, 1, At, B1); PG8_BAR; PG8_SCHED;
;             PG8_LDA(At, 0, 1); PG8_STAGE(PG8_SB(0, 0), b2, voffB[0]); PG8_STAGE(PG8_SB(0, 1), b2, voffB[1]); PG8_STAGE(PG8_SA(0, 0), a2, vA2[0]);
;             PG8_WAIT_V(8); PG8_WAIT_L(0); PG8_BAR; PG8_MMA(1, 0, At, B0); PG8_MMA(1, 1, At, B1); PG8_BAR; PG8_SCHED;
;             PG8_LDB(B0, 1, 0); PG8_LDB(B1, 1, 1); PG8_SCHED; PG8_LDA(At, 1, 0); PG8_STAGE(PG8_SA(0, 1), a2, vA2[1]);
;             PG8_WAIT_V(8); PG8_WAIT_L(0); PG8_BAR; PG8_MMA(0, 0, At, B0); PG8_MMA(0, 1, At, B1); PG8_BAR; PG8_SCHED;
;             PG8_LDA(At, 1, 1); PG8_STAGE(PG8_SB(1, 0), b3, voffB[0]); PG8_STAGE(PG8_SB(1, 1), b3, voffB[1]); PG8_STAGE(PG8_SA(1, 0), a3, vA2[0]);
;             PG8_WAIT_V(8); PG8_WAIT_L(0); PG8_BAR; PG8_MMA(1, 0, At, B0); PG8_MMA(1, 1, At, B1); PG8_BAR; PG8_SCHED;
.Lpk0_1060:
	v_add_u32_e32 v2, s12, v210
	v_add_u32_e32 v14, s62, v210
	s_add_u32 s28, s30, 0x100
	ds_read_b128 v[18:21], v2
	ds_read_b128 v[22:25], v2 offset:1024
	ds_read_b128 v[26:29], v2 offset:2048
	ds_read_b128 v[30:33], v2 offset:3072
	ds_read_b128 v[2:5], v14
	ds_read_b128 v[6:9], v14 offset:1024
	ds_read_b128 v[10:13], v14 offset:2048
	ds_read_b128 v[14:17], v14 offset:3072
	s_addc_u32 s29, s31, 0
	s_and_b64 s[42:43], s[40:41], exec
	s_cselect_b32 s42, 0, s28
	s_cselect_b32 s43, 0, s29
	s_add_u32 s42, s6, s42
	s_addc_u32 s43, s7, s43
	s_and_b64 s[40:41], s[40:41], exec
	s_cselect_b32 s41, s25, s68
	s_cselect_b32 s40, s24, s21
	v_lshl_add_u64 v[204:205], v[196:197], 0, s[30:31]
	s_add_i32 m0, s52, 0xc000
	ds_read_b128 v[222:225], v213
	ds_read_b128 v[226:229], v213 offset:1024
	ds_read_b128 v[230:233], v213 offset:2048
	ds_read_b128 v[234:237], v213 offset:3072
	ds_read_b128 v[238:241], v213 offset:4096
	ds_read_b128 v[242:245], v213 offset:5120
	ds_read_b128 v[246:249], v213 offset:6144
	ds_read_b128 v[250:253], v213 offset:7168
	global_load_lds_dwordx4 v[204:205], off
	v_lshl_add_u64 v[204:205], v[194:195], 0, s[30:31]
	s_add_i32 m0, s52, 0xe000
	s_nop 0
	global_load_lds_dwordx4 v[204:205], off
	s_waitcnt vmcnt(8)
	s_waitcnt lgkmcnt(0)
	s_setprio 1
	v_mfma_f32_16x16x128_f8f6f4 v[142:145], v[18:25], v[222:229], 0
	v_mfma_f32_16x16x128_f8f6f4 v[138:141], v[26:33], v[222:229], 0
	v_mfma_f32_16x16x128_f8f6f4 v[134:137], v[18:25], v[230:237], 0
	v_mfma_f32_16x16x128_f8f6f4 v[130:133], v[26:33], v[230:237], 0
	v_mfma_f32_16x16x128_f8f6f4 v[126:129], v[18:25], v[238:245], 0
	v_mfma_f32_16x16x128_f8f6f4 v[122:125], v[26:33], v[238:245], 0
	v_mfma_f32_16x16x128_f8f6f4 v[118:121], v[18:25], v[246:253], 0
	v_mfma_f32_16x16x128_f8f6f4 v[114:117], v[26:33], v[246:253], 0
	s_nop 3
	s_setprio 0
	s_setprio 1
	v_mfma_f32_16x16x128_f8f6f4 v[110:113], v[2:9], v[222:229], 0
	v_mfma_f32_16x16x128_f8f6f4 v[106:109], v[10:17], v[222:229], 0
	v_mfma_f32_16x16x128_f8f6f4 v[102:105], v[2:9], v[230:237], 0
	v_mfma_f32_16x16x128_f8f6f4 v[98:101], v[10:17], v[230:237], 0
	v_mfma_f32_16x16x128_f8f6f4 v[94:97], v[2:9], v[238:245], 0
	v_mfma_f32_16x16x128_f8f6f4 v[90:93], v[10:17], v[238:245], 0
	v_mfma_f32_16x16x128_f8f6f4 v[86:89], v[2:9], v[246:253], 0
	v_mfma_f32_16x16x128_f8f6f4 v[82:85], v[10:17], v[246:253], 0
	s_setprio 0
	s_barrier
	s_add_i32 s30, s12, s48
	v_lshl_add_u64 v[204:205], s[40:41], 0, v[162:163]
	s_mov_b32 m0, s30
	ds_read_b128 v[222:225], v213 offset:16384
	ds_read_b128 v[226:229], v213 offset:17408
	ds_read_b128 v[230:233], v213 offset:18432
	ds_read_b128 v[234:237], v213 offset:19456
	ds_read_b128 v[238:241], v213 offset:20480
	ds_read_b128 v[242:245], v213 offset:21504
	ds_read_b128 v[246:249], v213 offset:22528
	ds_read_b128 v[250:253], v213 offset:23552
	global_load_lds_dwordx4 v[204:205], off
	v_lshl_add_u64 v[204:205], s[40:41], 0, v[164:165]
	s_add_i32 m0, s30, 0x2000
	s_add_i32 s30, s62, s48
	global_load_lds_dwordx4 v[204:205], off
	v_lshl_add_u64 v[204:205], s[40:41], 0, v[166:167]
	s_mov_b32 m0, s30
	v_mov_b32_e32 v203, v171
	global_load_lds_dwordx4 v[204:205], off
	v_lshl_add_u64 v[204:205], s[40:41], 0, v[168:169]
	s_add_i32 m0, s30, 0x2000
	s_nop 0
	global_load_lds_dwordx4 v[204:205], off
	s_mov_b32 m0, s52
	v_lshl_add_u64 v[204:205], s[42:43], 0, v[170:171]
	global_load_lds_dwordx4 v170, s[42:43]
	s_mov_b32 m0, s53
	s_nop 0
	global_load_lds_dwordx4 v202, s[42:43]
	s_waitcnt vmcnt(8)
	s_waitcnt lgkmcnt(0)
	v_lshl_add_u64 v[202:203], s[42:43], 0, v[202:203]
	s_setprio 1
	v_mfma_f32_16x16x128_f8f6f4 v[78:81], v[18:25], v[222:229], 0
	v_mfma_f32_16x16x128_f8f6f4 v[74:77], v[26:33], v[222:229], 0
	v_mfma_f32_16x16x128_f8f6f4 v[70:73], v[18:25], v[230:237], 0
	v_mfma_f32_16x16x128_f8f6f4 v[66:69], v[26:33], v[230:237], 0
	v_mfma_f32_16x16x128_f8f6f4 v[62:65], v[18:25], v[238:245], 0
	v_mfma_f32_16x16x128_f8f6f4 v[58:61], v[26:33], v[238:245], 0
	v_mfma_f32_16x16x128_f8f6f4 v[54:57], v[18:25], v[246:253], 0
	v_mfma_f32_16x16x128_f8f6f4 v[50:53], v[26:33], v[246:253], 0
	s_nop 3
	s_setprio 0
	s_setprio 1
	v_mfma_f32_16x16x128_f8f6f4 v[46:49], v[2:9], v[222:229], 0
	v_mfma_f32_16x16x128_f8f6f4 v[42:45], v[10:17], v[222:229], 0
	v_mfma_f32_16x16x128_f8f6f4 v[38:41], v[2:9], v[230:237], 0
	v_mfma_f32_16x16x128_f8f6f4 v[34:37], v[10:17], v[230:237], 0
	v_mfma_f32_16x16x128_f8f6f4 v[146:149], v[2:9], v[238:245], 0
	v_mfma_f32_16x16x128_f8f6f4 v[150:153], v[10:17], v[238:245], 0
	v_mfma_f32_16x16x128_f8f6f4 v[154:157], v[2:9], v[246:253], 0
	v_mfma_f32_16x16x128_f8f6f4 v[158:161], v[10:17], v[246:253], 0
	s_setprio 0
	s_barrier
; #define PG8_STAGE(bufoff, gbase, voff) do { _Pragma("unroll") for (int _i = 0; _i < 2; ++_i) \
;         __builtin_amdgcn_global_load_lds((const unsigned*)((const char*)(gbase) + (voff)[_i]), (PG8_LAS unsigned*)(lds + (bufoff) + ldsw + _i * 8192), 16, 0, 0); } while (0)
; #define PG8_WAIT_V(n) asm volatile("s_waitcnt vmcnt(" #n ")" ::: "memory")
; #define PG8_WAIT_L(n) asm volatile("s_waitcnt lgkmcnt(" #n ")" ::: "memory")
; #define PG8_BAR __builtin_amdgcn_s_barrier()
; #define PG8_SCHED __builtin_amdgcn_sched_barrier(0)
; template <class Epi, class Sched, bool ALIGN_EPI = true, bool F8 = false>
; __device__ __forceinline__ void gemm_phase(PG8_LAS unsigned char* lds, const Sched& S, const Epi& E) {
;     ...
;             PG8_LDB(B0, 0, 0); PG8_LDB(B1, 0, 1); PG8_SCHED; PG8_LDA(At, 0, 0); PG8_STAGE(PG8_SA(1, 1), a1, voffA[1]);
;             PG8_WAIT_V(8); PG8_WAIT_L(0); PG8_BAR; PG8_MMA(0, 0, At, B0); PG8_MMA(0, 1, At, B1); PG8_BAR; PG8_SCHED;
;             PG8_LDA(At, 0, 1); PG8_STAGE(PG8_SB(0, 0), b2, voffB[0]); PG8_STAGE(PG8_SB(0, 1), b2, voffB[1]); PG8_STAGE(PG8_SA(0, 0), a2, vA2[0]);
;             PG8_WAIT_V(8); PG8_WAIT_L(0); PG8_BAR; PG8_MMA(1, 0, At, B0); PG8_MMA(1, 1, At, B1); PG8_BAR; PG8_SCHED;
;             PG8_LDB(B0, 1, 0); PG8_LDB(B1, 1, 1); PG8_SCHED; PG8_LDA(At, 1, 0); PG8_STAGE(PG8_SA(0, 1), a2, vA2[1]);
;             PG8_WAIT_V(8); PG8_WAIT_L(0); PG8_BAR; PG8_MMA(0, 0, At, B0); PG8_MMA(0, 1, At, B1); PG8_BAR; PG8_SCHED;
;             PG8_LDA(At, 1, 1); PG8_STAGE(PG8_SB(1, 0), b3, voffB[0]); PG8_STAGE(PG8_SB(1, 1), b3, voffB[1]); PG8_STAGE(PG8_SA(1, 0), a3, vA2[0]);
;             PG8_WAIT_V(8); PG8_WAIT_L(0); PG8_BAR; PG8_MMA(1, 0, At, B0); PG8_MMA(1, 1, At, B1); PG8_BAR; PG8_SCHED;
	s_add_i32 s70, 0, 0x18000
	s_add_i32 s71, 0, 0x1c000
	v_add_u32_e32 v14, s70, v210
	v_add_u32_e32 v30, s71, v210
	ds_read_b128 v[2:5], v14
	ds_read_b128 v[6:9], v14 offset:1024
	ds_read_b128 v[10:13], v14 offset:2048
	ds_read_b128 v[14:17], v14 offset:3072
	ds_read_b128 v[18:21], v30
	ds_read_b128 v[22:25], v30 offset:1024
	ds_read_b128 v[26:29], v30 offset:2048
	ds_read_b128 v[30:33], v30 offset:3072
	s_mov_b32 m0, s58
	v_lshl_add_u64 v[200:201], s[42:43], 0, v[200:201]
	ds_read_b128 v[222:225], v213 offset:32768
	ds_read_b128 v[226:229], v213 offset:33792
	ds_read_b128 v[230:233], v213 offset:34816
	ds_read_b128 v[234:237], v213 offset:35840
	ds_read_b128 v[238:241], v213 offset:36864
	ds_read_b128 v[242:245], v213 offset:37888
	ds_read_b128 v[246:249], v213 offset:38912
	ds_read_b128 v[250:253], v213 offset:39936
	global_load_lds_dwordx4 v[200:201], off
	v_lshl_add_u64 v[198:199], s[42:43], 0, v[198:199]
	s_mov_b32 m0, s59
	s_nop 0
	global_load_lds_dwordx4 v[198:199], off
	s_waitcnt vmcnt(8)
	s_waitcnt lgkmcnt(0)
	s_setprio 1
	v_mfma_f32_16x16x128_f8f6f4 v[142:145], v[2:9], v[222:229], v[142:145]
	v_mfma_f32_16x16x128_f8f6f4 v[138:141], v[10:17], v[222:229], v[138:141]
	v_mfma_f32_16x16x128_f8f6f4 v[134:137], v[2:9], v[230:237], v[134:137]
	v_mfma_f32_16x16x128_f8f6f4 v[130:133], v[10:17], v[230:237], v[130:133]
	v_mfma_f32_16x16x128_f8f6f4 v[126:129], v[2:9], v[238:245], v[126:129]
	v_mfma_f32_16x16x128_f8f6f4 v[122:125], v[10:17], v[238:245], v[122:125]
	v_mfma_f32_16x16x128_f8f6f4 v[118:121], v[2:9], v[246:253], v[118:121]
	v_mfma_f32_16x16x128_f8f6f4 v[114:117], v[10:17], v[246:253], v[114:117]
	s_nop 3
	s_setprio 0
	s_setprio 1
	v_mfma_f32_16x16x128_f8f6f4 v[110:113], v[18:25], v[222:229], v[110:113]
	v_mfma_f32_16x16x128_f8f6f4 v[106:109], v[26:33], v[222:229], v[106:109]
	v_mfma_f32_16x16x128_f8f6f4 v[102:105], v[18:25], v[230:237], v[102:105]
	v_mfma_f32_16x16x128_f8f6f4 v[98:101], v[26:33], v[230:237], v[98:101]
	v_mfma_f32_16x16x128_f8f6f4 v[94:97], v[18:25], v[238:245], v[94:97]
	v_mfma_f32_16x16x128_f8f6f4 v[90:93], v[26:33], v[238:245], v[90:93]
	v_mfma_f32_16x16x128_f8f6f4 v[86:89], v[18:25], v[246:253], v[86:89]
	v_mfma_f32_16x16x128_f8f6f4 v[82:85], v[26:33], v[246:253], v[82:85]
	s_setprio 0
	s_barrier
	s_add_u32 s30, s40, 0x8000
	s_addc_u32 s31, s41, 0
	s_add_i32 s40, s70, s48
	v_lshl_add_u64 v[198:199], s[30:31], 0, v[162:163]
	s_mov_b32 m0, s40
	ds_read_b128 v[222:225], v213 offset:49152
	ds_read_b128 v[226:229], v213 offset:50176
	ds_read_b128 v[230:233], v213 offset:51200
	ds_read_b128 v[234:237], v213 offset:52224
	ds_read_b128 v[238:241], v213 offset:53248
	ds_read_b128 v[242:245], v213 offset:54272
	ds_read_b128 v[246:249], v213 offset:55296
	ds_read_b128 v[250:253], v213 offset:56320
	global_load_lds_dwordx4 v[198:199], off
	v_lshl_add_u64 v[198:199], s[30:31], 0, v[164:165]
	s_add_i32 m0, s40, 0x2000
	s_add_i32 s40, s71, s48
	global_load_lds_dwordx4 v[198:199], off
	v_lshl_add_u64 v[198:199], s[30:31], 0, v[166:167]
	s_mov_b32 m0, s40
	s_nop 0
	global_load_lds_dwordx4 v[198:199], off
	v_lshl_add_u64 v[198:199], s[30:31], 0, v[168:169]
	s_add_i32 m0, s40, 0x2000
	s_nop 0
	global_load_lds_dwordx4 v[198:199], off
	v_lshl_add_u64 v[198:199], v[204:205], 0, s[18:19]
	s_mov_b32 m0, s60
	s_nop 0
	global_load_lds_dwordx4 v[198:199], off
	v_lshl_add_u64 v[198:199], v[202:203], 0, s[18:19]
	s_mov_b32 m0, s61
	s_nop 0
	global_load_lds_dwordx4 v[198:199], off
	s_waitcnt vmcnt(8)
	s_waitcnt lgkmcnt(0)
	s_setprio 1
	v_mfma_f32_16x16x128_f8f6f4 v[78:81], v[2:9], v[222:229], v[78:81]
	v_mfma_f32_16x16x128_f8f6f4 v[74:77], v[10:17], v[222:229], v[74:77]
	v_mfma_f32_16x16x128_f8f6f4 v[70:73], v[2:9], v[230:237], v[70:73]
	v_mfma_f32_16x16x128_f8f6f4 v[66:69], v[10:17], v[230:237], v[66:69]
	v_mfma_f32_16x16x128_f8f6f4 v[62:65], v[2:9], v[238:245], v[62:65]
	v_mfma_f32_16x16x128_f8f6f4 v[58:61], v[10:17], v[238:245], v[58:61]
	v_mfma_f32_16x16x128_f8f6f4 v[54:57], v[2:9], v[246:253], v[54:57]
	v_mfma_f32_16x16x128_f8f6f4 v[50:53], v[10:17], v[246:253], v[50:53]
	s_nop 3
	s_setprio 0
	s_setprio 1
	v_mfma_f32_16x16x128_f8f6f4 v[46:49], v[18:25], v[222:229], v[46:49]
	v_mfma_f32_16x16x128_f8f6f4 v[42:45], v[26:33], v[222:229], v[42:45]
	v_mfma_f32_16x16x128_f8f6f4 v[38:41], v[18:25], v[230:237], v[38:41]
	v_mfma_f32_16x16x128_f8f6f4 v[34:37], v[26:33], v[230:237], v[34:37]
	v_mfma_f32_16x16x128_f8f6f4 v[146:149], v[18:25], v[238:245], v[146:149]
	v_mfma_f32_16x16x128_f8f6f4 v[150:153], v[26:33], v[238:245], v[150:153]
	v_mfma_f32_16x16x128_f8f6f4 v[154:157], v[18:25], v[246:253], v[154:157]
	v_mfma_f32_16x16x128_f8f6f4 v[158:161], v[26:33], v[246:253], v[158:161]
	s_setprio 0
	s_barrier
	s_add_i32 s69, s69, 2
	s_add_u32 s21, s21, 0x10000
	s_addc_u32 s68, s68, 0
	s_cmp_gt_u32 s69, 13
	s_cbranch_scc1 .LBB0_1062
	s_mov_b64 s[30:31], s[28:29]
	s_branch .LBB0_1058

; #define PG8_STAGE(bufoff, gbase, voff) do { _Pragma("unroll") for (int _i = 0; _i < 2; ++_i) \
;         __builtin_amdgcn_global_load_lds((const unsigned*)((const char*)(gbase) + (voff)[_i]), (PG8_LAS unsigned*)(lds + (bufoff) + ldsw + _i * 8192), 16, 0, 0); } while (0)
; #define PG8_WAIT_V(n) asm volatile("s_waitcnt vmcnt(" #n ")" ::: "memory")
; #define PG8_WAIT_L(n) asm volatile("s_waitcnt lgkmcnt(" #n ")" ::: "memory")
; template <class Epi, class Sched, bool ALIGN_EPI = true, bool F8 = false>
; __device__ __forceinline__ void gemm_phase(PG8_LAS unsigned char* lds, const Sched& S, const Epi& E) {
;     ...
;         for (int t = 0; t < nt; t += 2) {
;             const bool last = (t == nt - 2);
;             if constexpr (Sched::GATHER) { if (last && has_next) S.a_off(nxt, Rs, Cs, voffAn); }
;             const char* a1 = cA + (size_t)(t + 1) * kstep;
;             const char* a2 = last ? nA : cA + (size_t)(t + 2) * kstep; const char* b2 = last ? nB : cB + (size_t)(t + 2) * kstepB;
;             const char* a3 = a2 + kstep; const char* b3 = b2 + kstepB;
;             unsigned vA2[2][2];
; #pragma unroll
;             for (int h = 0; h < 2; ++h)
; #pragma unroll
;                 for (int i = 0; i < 2; ++i) { if constexpr (Sched::GATHER) vA2[h][i] = (last && has_next) ? voffAn[h][i] : voffA[h][i]; else vA2[h][i] = voffA[h][i]; }
;             PG8_LDB(B0, 0, 0); PG8_LDB(B1, 0, 1); PG8_SCHED; PG8_LDA(At, 0, 0); PG8_STAGE(PG8_SA(1, 1), a1, voffA[1]);
;             PG8_WAIT_V(8); PG8_WAIT_L(0); PG8_BAR; PG8_MMA(0, 0, At, B0); PG8_MMA(0, 1, At, B1); PG8_BAR; PG8_SCHED;
;             PG8_LDA(At, 0, 1); PG8_STAGE(PG8_SB(0, 0), b2, voffB[0]); PG8_STAGE(PG8_SB(0, 1), b2, voffB[1]); PG8_STAGE(PG8_SA(0, 0), a2, vA2[0]);
;             PG8_WAIT_V(8); PG8_WAIT_L(0); PG8_BAR; PG8_MMA(1, 0, At, B0); PG8_MMA(1, 1, At, B1); PG8_BAR; PG8_SCHED;
;             PG8_LDB(B0, 1, 0); PG8_LDB(B1, 1, 1); PG8_SCHED; PG8_LDA(At, 1, 0); PG8_STAGE(PG8_SA(0, 1), a2, vA2[1]);
;             PG8_WAIT_V(8); PG8_WAIT_L(0); PG8_BAR; PG8_MMA(0, 0, At, B0); PG8_MMA(0, 1, At, B1); PG8_BAR; PG8_SCHED;
;             PG8_LDA(At, 1, 1); PG8_STAGE(PG8_SB(1, 0), b3, voffB[0]); PG8_STAGE(PG8_SB(1, 1), b3, voffB[1]); PG8_STAGE(PG8_SA(1, 0), a3, vA2[0]);
;             PG8_WAIT_V(8); PG8_WAIT_L(0); PG8_BAR; PG8_MMA(1, 0, At, B0); PG8_MMA(1, 1, At, B1); PG8_BAR; PG8_SCHED;
.Lpk1_1060:
	v_add_u32_e32 v2, s12, v210
	v_add_u32_e32 v14, s62, v210
	s_add_u32 s28, s30, 0x100
	ds_read_b128 v[18:21], v2
	ds_read_b128 v[22:25], v2 offset:1024
	ds_read_b128 v[26:29], v2 offset:2048
	ds_read_b128 v[30:33], v2 offset:3072
	ds_read_b128 v[2:5], v14
	ds_read_b128 v[6:9], v14 offset:1024
	ds_read_b128 v[10:13], v14 offset:2048
	ds_read_b128 v[14:17], v14 offset:3072
	s_addc_u32 s29, s31, 0
	s_and_b64 s[42:43], s[40:41], exec
	s_cselect_b32 s42, 0, s28
	s_cselect_b32 s43, 0, s29
	s_add_u32 s42, s6, s42
	s_addc_u32 s43, s7, s43
	s_and_b64 s[40:41], s[40:41], exec
	s_cselect_b32 s41, s25, s68
	s_cselect_b32 s40, s24, s21
	v_lshl_add_u64 v[204:205], v[196:197], 0, s[30:31]
	s_add_i32 m0, s52, 0xc000
	ds_read_b128 v[222:225], v213
	ds_read_b128 v[226:229], v213 offset:1024
	ds_read_b128 v[230:233], v213 offset:2048
	ds_read_b128 v[234:237], v213 offset:3072
	ds_read_b128 v[238:241], v213 offset:4096
	ds_read_b128 v[242:245], v213 offset:5120
	ds_read_b128 v[246:249], v213 offset:6144
	ds_read_b128 v[250:253], v213 offset:7168
	global_load_lds_dwordx4 v[204:205], off
	v_lshl_add_u64 v[204:205], v[194:195], 0, s[30:31]
	s_add_i32 m0, s52, 0xe000
	s_nop 0
	global_load_lds_dwordx4 v[204:205], off
	s_waitcnt vmcnt(8)
	s_waitcnt lgkmcnt(0)
	s_barrier
	s_setprio 2
	v_mfma_f32_16x16x128_f8f6f4 v[142:145], v[18:25], v[222:229], 0
	v_mfma_f32_16x16x128_f8f6f4 v[138:141], v[26:33], v[222:229], 0
	v_mfma_f32_16x16x128_f8f6f4 v[134:137], v[18:25], v[230:237], 0
	v_mfma_f32_16x16x128_f8f6f4 v[130:133], v[26:33], v[230:237], 0
	v_mfma_f32_16x16x128_f8f6f4 v[126:129], v[18:25], v[238:245], 0
	v_mfma_f32_16x16x128_f8f6f4 v[122:125], v[26:33], v[238:245], 0
	v_mfma_f32_16x16x128_f8f6f4 v[118:121], v[18:25], v[246:253], 0
	v_mfma_f32_16x16x128_f8f6f4 v[114:117], v[26:33], v[246:253], 0
	s_nop 3
	s_setprio 0
	s_setprio 2
	v_mfma_f32_16x16x128_f8f6f4 v[110:113], v[2:9], v[222:229], 0
	v_mfma_f32_16x16x128_f8f6f4 v[106:109], v[10:17], v[222:229], 0
	v_mfma_f32_16x16x128_f8f6f4 v[102:105], v[2:9], v[230:237], 0
	v_mfma_f32_16x16x128_f8f6f4 v[98:101], v[10:17], v[230:237], 0
	v_mfma_f32_16x16x128_f8f6f4 v[94:97], v[2:9], v[238:245], 0
	v_mfma_f32_16x16x128_f8f6f4 v[90:93], v[10:17], v[238:245], 0
	v_mfma_f32_16x16x128_f8f6f4 v[86:89], v[2:9], v[246:253], 0
	v_mfma_f32_16x16x128_f8f6f4 v[82:85], v[10:17], v[246:253], 0
	s_setprio 0
	s_add_i32 s30, s12, s48
	v_lshl_add_u64 v[204:205], s[40:41], 0, v[162:163]
	s_mov_b32 m0, s30
	ds_read_b128 v[222:225], v213 offset:16384
	ds_read_b128 v[226:229], v213 offset:17408
	ds_read_b128 v[230:233], v213 offset:18432
	ds_read_b128 v[234:237], v213 offset:19456
	ds_read_b128 v[238:241], v213 offset:20480
	ds_read_b128 v[242:245], v213 offset:21504
	ds_read_b128 v[246:249], v213 offset:22528
	ds_read_b128 v[250:253], v213 offset:23552
	global_load_lds_dwordx4 v[204:205], off
	v_lshl_add_u64 v[204:205], s[40:41], 0, v[164:165]
	s_add_i32 m0, s30, 0x2000
	s_add_i32 s30, s62, s48
	global_load_lds_dwordx4 v[204:205], off
	v_lshl_add_u64 v[204:205], s[40:41], 0, v[166:167]
	s_mov_b32 m0, s30
	v_mov_b32_e32 v203, v171
	global_load_lds_dwordx4 v[204:205], off
	v_lshl_add_u64 v[204:205], s[40:41], 0, v[168:169]
	s_add_i32 m0, s30, 0x2000
	s_nop 0
	global_load_lds_dwordx4 v[204:205], off
	s_mov_b32 m0, s52
	v_lshl_add_u64 v[204:205], s[42:43], 0, v[170:171]
	global_load_lds_dwordx4 v170, s[42:43]
	s_mov_b32 m0, s53
	s_nop 0
	global_load_lds_dwordx4 v202, s[42:43]
	s_waitcnt vmcnt(8)
	s_waitcnt lgkmcnt(0)
	v_lshl_add_u64 v[202:203], s[42:43], 0, v[202:203]
	s_barrier
	s_setprio 2
	v_mfma_f32_16x16x128_f8f6f4 v[78:81], v[18:25], v[222:229], 0
	v_mfma_f32_16x16x128_f8f6f4 v[74:77], v[26:33], v[222:229], 0
	v_mfma_f32_16x16x128_f8f6f4 v[70:73], v[18:25], v[230:237], 0
	v_mfma_f32_16x16x128_f8f6f4 v[66:69], v[26:33], v[230:237], 0
	v_mfma_f32_16x16x128_f8f6f4 v[62:65], v[18:25], v[238:245], 0
	v_mfma_f32_16x16x128_f8f6f4 v[58:61], v[26:33], v[238:245], 0
	v_mfma_f32_16x16x128_f8f6f4 v[54:57], v[18:25], v[246:253], 0
	v_mfma_f32_16x16x128_f8f6f4 v[50:53], v[26:33], v[246:253], 0
	s_nop 3
	s_setprio 0
	s_setprio 2
	v_mfma_f32_16x16x128_f8f6f4 v[46:49], v[2:9], v[222:229], 0
	v_mfma_f32_16x16x128_f8f6f4 v[42:45], v[10:17], v[222:229], 0
	v_mfma_f32_16x16x128_f8f6f4 v[38:41], v[2:9], v[230:237], 0
	v_mfma_f32_16x16x128_f8f6f4 v[34:37], v[10:17], v[230:237], 0
	v_mfma_f32_16x16x128_f8f6f4 v[146:149], v[2:9], v[238:245], 0
	v_mfma_f32_16x16x128_f8f6f4 v[150:153], v[10:17], v[238:245], 0
	v_mfma_f32_16x16x128_f8f6f4 v[154:157], v[2:9], v[246:253], 0
	v_mfma_f32_16x16x128_f8f6f4 v[158:161], v[10:17], v[246:253], 0
	s_setprio 0
	s_add_i32 s70, 0, 0x18000
	s_add_i32 s71, 0, 0x1c000
	v_add_u32_e32 v14, s70, v210
	v_add_u32_e32 v30, s71, v210
	ds_read_b128 v[2:5], v14
	ds_read_b128 v[6:9], v14 offset:1024
	ds_read_b128 v[10:13], v14 offset:2048
	ds_read_b128 v[14:17], v14 offset:3072
	ds_read_b128 v[18:21], v30
	ds_read_b128 v[22:25], v30 offset:1024
	ds_read_b128 v[26:29], v30 offset:2048
	ds_read_b128 v[30:33], v30 offset:3072
	s_mov_b32 m0, s58
	v_lshl_add_u64 v[200:201], s[42:43], 0, v[200:201]
	ds_read_b128 v[222:225], v213 offset:32768
	ds_read_b128 v[226:229], v213 offset:33792
	ds_read_b128 v[230:233], v213 offset:34816
	ds_read_b128 v[234:237], v213 offset:35840
	ds_read_b128 v[238:241], v213 offset:36864
	ds_read_b128 v[242:245], v213 offset:37888
	ds_read_b128 v[246:249], v213 offset:38912
	ds_read_b128 v[250:253], v213 offset:39936
	global_load_lds_dwordx4 v[200:201], off
	v_lshl_add_u64 v[198:199], s[42:43], 0, v[198:199]
	s_mov_b32 m0, s59
	s_nop 0
	global_load_lds_dwordx4 v[198:199], off
	s_waitcnt vmcnt(8)
	s_waitcnt lgkmcnt(0)
	s_barrier
; #define PG8_STAGE(bufoff, gbase, voff) do { _Pragma("unroll") for (int _i = 0; _i < 2; ++_i) \
;         __builtin_amdgcn_global_load_lds((const unsigned*)((const char*)(gbase) + (voff)[_i]), (PG8_LAS unsigned*)(lds + (bufoff) + ldsw + _i * 8192), 16, 0, 0); } while (0)
; #define PG8_WAIT_V(n) asm volatile("s_waitcnt vmcnt(" #n ")" ::: "memory")
; #define PG8_WAIT_L(n) asm volatile("s_waitcnt lgkmcnt(" #n ")" ::: "memory")
; #define PG8_BAR __builtin_amdgcn_s_barrier()
; #define PG8_SCHED __builtin_amdgcn_sched_barrier(0)
; template <class Epi, class Sched, bool ALIGN_EPI = true, bool F8 = false>
; __device__ __forceinline__ void gemm_phase(PG8_LAS unsigned char* lds, const Sched& S, const Epi& E) {
;     ...
;             PG8_LDB(B0, 0, 0); PG8_LDB(B1, 0, 1); PG8_SCHED; PG8_LDA(At, 0, 0); PG8_STAGE(PG8_SA(1, 1), a1, voffA[1]);
;             PG8_WAIT_V(8); PG8_WAIT_L(0); PG8_BAR; PG8_MMA(0, 0, At, B0); PG8_MMA(0, 1, At, B1); PG8_BAR; PG8_SCHED;
;             PG8_LDA(At, 0, 1); PG8_STAGE(PG8_SB(0, 0), b2, voffB[0]); PG8_STAGE(PG8_SB(0, 1), b2, voffB[1]); PG8_STAGE(PG8_SA(0, 0), a2, vA2[0]);
;             PG8_WAIT_V(8); PG8_WAIT_L(0); PG8_BAR; PG8_MMA(1, 0, At, B0); PG8_MMA(1, 1, At, B1); PG8_BAR; PG8_SCHED;
;             PG8_LDB(B0, 1, 0); PG8_LDB(B1, 1, 1); PG8_SCHED; PG8_LDA(At, 1, 0); PG8_STAGE(PG8_SA(0, 1), a2, vA2[1]);
;             PG8_WAIT_V(8); PG8_WAIT_L(0); PG8_BAR; PG8_MMA(0, 0, At, B0); PG8_MMA(0, 1, At, B1); PG8_BAR; PG8_SCHED;
;             PG8_LDA(At, 1, 1); PG8_STAGE(PG8_SB(1, 0), b3, voffB[0]); PG8_STAGE(PG8_SB(1, 1), b3, voffB[1]); PG8_STAGE(PG8_SA(1, 0), a3, vA2[0]);
;             PG8_WAIT_V(8); PG8_WAIT_L(0); PG8_BAR; PG8_MMA(1, 0, At, B0); PG8_MMA(1, 1, At, B1); PG8_BAR; PG8_SCHED;
	s_setprio 2
	v_mfma_f32_16x16x128_f8f6f4 v[142:145], v[2:9], v[222:229], v[142:145]
	v_mfma_f32_16x16x128_f8f6f4 v[138:141], v[10:17], v[222:229], v[138:141]
	v_mfma_f32_16x16x128_f8f6f4 v[134:137], v[2:9], v[230:237], v[134:137]
	v_mfma_f32_16x16x128_f8f6f4 v[130:133], v[10:17], v[230:237], v[130:133]
	v_mfma_f32_16x16x128_f8f6f4 v[126:129], v[2:9], v[238:245], v[126:129]
	v_mfma_f32_16x16x128_f8f6f4 v[122:125], v[10:17], v[238:245], v[122:125]
	v_mfma_f32_16x16x128_f8f6f4 v[118:121], v[2:9], v[246:253], v[118:121]
	v_mfma_f32_16x16x128_f8f6f4 v[114:117], v[10:17], v[246:253], v[114:117]
	s_nop 3
	s_setprio 0
	s_setprio 2
	v_mfma_f32_16x16x128_f8f6f4 v[110:113], v[18:25], v[222:229], v[110:113]
	v_mfma_f32_16x16x128_f8f6f4 v[106:109], v[26:33], v[222:229], v[106:109]
	v_mfma_f32_16x16x128_f8f6f4 v[102:105], v[18:25], v[230:237], v[102:105]
	v_mfma_f32_16x16x128_f8f6f4 v[98:101], v[26:33], v[230:237], v[98:101]
	v_mfma_f32_16x16x128_f8f6f4 v[94:97], v[18:25], v[238:245], v[94:97]
	v_mfma_f32_16x16x128_f8f6f4 v[90:93], v[26:33], v[238:245], v[90:93]
	v_mfma_f32_16x16x128_f8f6f4 v[86:89], v[18:25], v[246:253], v[86:89]
	v_mfma_f32_16x16x128_f8f6f4 v[82:85], v[26:33], v[246:253], v[82:85]
	s_setprio 0
	s_add_u32 s30, s40, 0x8000
	s_addc_u32 s31, s41, 0
	s_add_i32 s40, s70, s48
	v_lshl_add_u64 v[198:199], s[30:31], 0, v[162:163]
	s_mov_b32 m0, s40
	ds_read_b128 v[222:225], v213 offset:49152
	ds_read_b128 v[226:229], v213 offset:50176
	ds_read_b128 v[230:233], v213 offset:51200
	ds_read_b128 v[234:237], v213 offset:52224
	ds_read_b128 v[238:241], v213 offset:53248
	ds_read_b128 v[242:245], v213 offset:54272
	ds_read_b128 v[246:249], v213 offset:55296
	ds_read_b128 v[250:253], v213 offset:56320
	global_load_lds_dwordx4 v[198:199], off
	v_lshl_add_u64 v[198:199], s[30:31], 0, v[164:165]
	s_add_i32 m0, s40, 0x2000
	s_add_i32 s40, s71, s48
	global_load_lds_dwordx4 v[198:199], off
	v_lshl_add_u64 v[198:199], s[30:31], 0, v[166:167]
	s_mov_b32 m0, s40
	s_nop 0
	global_load_lds_dwordx4 v[198:199], off
	v_lshl_add_u64 v[198:199], s[30:31], 0, v[168:169]
	s_add_i32 m0, s40, 0x2000
	s_nop 0
	global_load_lds_dwordx4 v[198:199], off
	v_lshl_add_u64 v[198:199], v[204:205], 0, s[18:19]
	s_mov_b32 m0, s60
	s_nop 0
	global_load_lds_dwordx4 v[198:199], off
	v_lshl_add_u64 v[198:199], v[202:203], 0, s[18:19]
	s_mov_b32 m0, s61
	s_nop 0
	global_load_lds_dwordx4 v[198:199], off
	s_waitcnt vmcnt(8)
	s_waitcnt lgkmcnt(0)
	s_barrier
	s_setprio 2
	v_mfma_f32_16x16x128_f8f6f4 v[78:81], v[2:9], v[222:229], v[78:81]
	v_mfma_f32_16x16x128_f8f6f4 v[74:77], v[10:17], v[222:229], v[74:77]
	v_mfma_f32_16x16x128_f8f6f4 v[70:73], v[2:9], v[230:237], v[70:73]
	v_mfma_f32_16x16x128_f8f6f4 v[66:69], v[10:17], v[230:237], v[66:69]
	v_mfma_f32_16x16x128_f8f6f4 v[62:65], v[2:9], v[238:245], v[62:65]
	v_mfma_f32_16x16x128_f8f6f4 v[58:61], v[10:17], v[238:245], v[58:61]
	v_mfma_f32_16x16x128_f8f6f4 v[54:57], v[2:9], v[246:253], v[54:57]
	v_mfma_f32_16x16x128_f8f6f4 v[50:53], v[10:17], v[246:253], v[50:53]
	s_nop 3
	s_setprio 0
	s_setprio 2
	v_mfma_f32_16x16x128_f8f6f4 v[46:49], v[18:25], v[222:229], v[46:49]
	v_mfma_f32_16x16x128_f8f6f4 v[42:45], v[26:33], v[222:229], v[42:45]
	v_mfma_f32_16x16x128_f8f6f4 v[38:41], v[18:25], v[230:237], v[38:41]
	v_mfma_f32_16x16x128_f8f6f4 v[34:37], v[26:33], v[230:237], v[34:37]
	v_mfma_f32_16x16x128_f8f6f4 v[146:149], v[18:25], v[238:245], v[146:149]
	v_mfma_f32_16x16x128_f8f6f4 v[150:153], v[26:33], v[238:245], v[150:153]
	v_mfma_f32_16x16x128_f8f6f4 v[154:157], v[18:25], v[246:253], v[154:157]
	v_mfma_f32_16x16x128_f8f6f4 v[158:161], v[26:33], v[246:253], v[158:161]
	s_setprio 0
	s_add_i32 s69, s69, 2
	s_add_u32 s21, s21, 0x10000
	s_addc_u32 s68, s68, 0
	s_cmp_gt_u32 s69, 13
	s_cbranch_scc1 .LBB0_1062
	s_mov_b64 s[30:31], s[28:29]
	s_branch .Lh1_1058

; #define PG8_STAGE(bufoff, gbase, voff) do { _Pragma("unroll") for (int _i = 0; _i < 2; ++_i) \
;         __builtin_amdgcn_global_load_lds((const unsigned*)((const char*)(gbase) + (voff)[_i]), (PG8_LAS unsigned*)(lds + (bufoff) + ldsw + _i * 8192), 16, 0, 0); } while (0)
; #define PG8_WAIT_V(n) asm volatile("s_waitcnt vmcnt(" #n ")" ::: "memory")
; #define PG8_WAIT_L(n) asm volatile("s_waitcnt lgkmcnt(" #n ")" ::: "memory")
; template <class Epi, class Sched, bool ALIGN_EPI = true, bool F8 = false>
; __device__ __forceinline__ void gemm_phase(PG8_LAS unsigned char* lds, const Sched& S, const Epi& E) {
;     ...
;         for (int t = 0; t < nt; t += 2) {
;             const bool last = (t == nt - 2);
;             if constexpr (Sched::GATHER) { if (last && has_next) S.a_off(nxt, Rs, Cs, voffAn); }
;             const char* a1 = cA + (size_t)(t + 1) * kstep;
;             const char* a2 = last ? nA : cA + (size_t)(t + 2) * kstep; const char* b2 = last ? nB : cB + (size_t)(t + 2) * kstepB;
;             const char* a3 = a2 + kstep; const char* b3 = b2 + kstepB;
;             unsigned vA2[2][2];
; #pragma unroll
;             for (int h = 0; h < 2; ++h)
; #pragma unroll
;                 for (int i = 0; i < 2; ++i) { if constexpr (Sched::GATHER) vA2[h][i] = (last && has_next) ? voffAn[h][i] : voffA[h][i]; else vA2[h][i] = voffA[h][i]; }
;             PG8_LDB(B0, 0, 0); PG8_LDB(B1, 0, 1); PG8_SCHED; PG8_LDA(At, 0, 0); PG8_STAGE(PG8_SA(1, 1), a1, voffA[1]);
;             PG8_WAIT_V(8); PG8_WAIT_L(0); PG8_BAR; PG8_MMA(0, 0, At, B0); PG8_MMA(0, 1, At, B1); PG8_BAR; PG8_SCHED;
;             PG8_LDA(At, 0, 1); PG8_STAGE(PG8_SB(0, 0), b2, voffB[0]); PG8_STAGE(PG8_SB(0, 1), b2, voffB[1]); PG8_STAGE(PG8_SA(0, 0), a2, vA2[0]);
;             PG8_WAIT_V(8); PG8_WAIT_L(0); PG8_BAR; PG8_MMA(1, 0, At, B0); PG8_MMA(1, 1, At, B1); PG8_BAR; PG8_SCHED;
;             PG8_LDB(B0, 1, 0); PG8_LDB(B1, 1, 1); PG8_SCHED; PG8_LDA(At, 1, 0); PG8_STAGE(PG8_SA(0, 1), a2, vA2[1]);
;             PG8_WAIT_V(8); PG8_WAIT_L(0); PG8_BAR; PG8_MMA(0, 0, At, B0); PG8_MMA(0, 1, At, B1); PG8_BAR; PG8_SCHED;
;             PG8_LDA(At, 1, 1); PG8_STAGE(PG8_SB(1, 0), b3, voffB[0]); PG8_STAGE(PG8_SB(1, 1), b3, voffB[1]); PG8_STAGE(PG8_SA(1, 0), a3, vA2[0]);
;             PG8_WAIT_V(8); PG8_WAIT_L(0); PG8_BAR; PG8_MMA(1, 0, At, B0); PG8_MMA(1, 1, At, B1); PG8_BAR; PG8_SCHED;
.Lpk0_1138:
	ds_read_b128 v[18:21], v189
	ds_read_b128 v[22:25], v189 offset:1024
	ds_read_b128 v[26:29], v189 offset:2048
	ds_read_b128 v[30:33], v189 offset:3072
	ds_read_b128 v[2:5], v190
	ds_read_b128 v[6:9], v190 offset:1024
	ds_read_b128 v[10:13], v190 offset:2048
	ds_read_b128 v[14:17], v190 offset:3072
	s_add_u32 s26, s24, 0x8000
	s_addc_u32 s27, s25, 0
	s_cmp_eq_u32 s68, 4
	s_cselect_b32 s30, s16, s26
	s_cselect_b32 s31, s17, s27
	s_cselect_b32 s28, s18, s23
	s_cselect_b32 s29, s19, s67
	s_add_u32 s26, s30, 0x8000
	s_addc_u32 s27, s31, 0
	s_add_i32 m0, s44, 0xc000
	ds_read_b128 v[194:197], v191
	ds_read_b128 v[198:201], v191 offset:1024
	ds_read_b128 v[202:205], v191 offset:2048
	ds_read_b128 v[206:209], v191 offset:3072
	ds_read_b128 v[210:213], v191 offset:4096
	ds_read_b128 v[214:217], v191 offset:5120
	ds_read_b128 v[218:221], v191 offset:6144
	ds_read_b128 v[222:225], v191 offset:7168
	global_load_lds_dwordx4 v184, s[24:25]
	s_add_i32 m0, s44, 0xe000
	s_nop 0
	global_load_lds_dwordx4 v182, s[24:25]
	s_waitcnt vmcnt(8)
	s_waitcnt lgkmcnt(0)
	s_setprio 1
	v_mfma_f32_16x16x128_f8f6f4 v[158:161], v[18:25], v[194:201], 0
	v_mfma_f32_16x16x128_f8f6f4 v[154:157], v[26:33], v[194:201], 0
	v_mfma_f32_16x16x128_f8f6f4 v[142:145], v[18:25], v[202:209], 0
	v_mfma_f32_16x16x128_f8f6f4 v[138:141], v[26:33], v[202:209], 0
	v_mfma_f32_16x16x128_f8f6f4 v[126:129], v[18:25], v[210:217], 0
	v_mfma_f32_16x16x128_f8f6f4 v[122:125], v[26:33], v[210:217], 0
	v_mfma_f32_16x16x128_f8f6f4 v[110:113], v[18:25], v[218:225], 0
	v_mfma_f32_16x16x128_f8f6f4 v[106:109], v[26:33], v[218:225], 0
	s_nop 3
	s_setprio 0
	s_setprio 1
	v_mfma_f32_16x16x128_f8f6f4 v[150:153], v[2:9], v[194:201], 0
	v_mfma_f32_16x16x128_f8f6f4 v[146:149], v[10:17], v[194:201], 0
	v_mfma_f32_16x16x128_f8f6f4 v[134:137], v[2:9], v[202:209], 0
	v_mfma_f32_16x16x128_f8f6f4 v[130:133], v[10:17], v[202:209], 0
	v_mfma_f32_16x16x128_f8f6f4 v[118:121], v[2:9], v[210:217], 0
	v_mfma_f32_16x16x128_f8f6f4 v[114:117], v[10:17], v[210:217], 0
	v_mfma_f32_16x16x128_f8f6f4 v[102:105], v[2:9], v[218:225], 0
	v_mfma_f32_16x16x128_f8f6f4 v[98:101], v[10:17], v[218:225], 0
	s_setprio 0
	s_barrier
	s_add_i32 s69, s53, s43
	s_mov_b32 m0, s69
	ds_read_b128 v[194:197], v191 offset:16384
	ds_read_b128 v[198:201], v191 offset:17408
	ds_read_b128 v[202:205], v191 offset:18432
	ds_read_b128 v[206:209], v191 offset:19456
	ds_read_b128 v[210:213], v191 offset:20480
	ds_read_b128 v[214:217], v191 offset:21504
	ds_read_b128 v[218:221], v191 offset:22528
	ds_read_b128 v[222:225], v191 offset:23552
	global_load_lds_dwordx4 v164, s[28:29]
	s_add_i32 m0, s69, 0x2000
	s_add_i32 s69, s58, s43
	global_load_lds_dwordx4 v166, s[28:29]
	s_add_u32 s98, s28, s4
	s_addc_u32 s99, s29, s5
	s_mov_b32 m0, s69
	s_nop 0
	global_load_lds_dwordx4 v164, s[98:99]
	s_add_u32 s100, s28, s4
	s_addc_u32 s101, s29, s5
	s_add_i32 m0, s69, 0x2000
	s_nop 0
	global_load_lds_dwordx4 v166, s[100:101]
	s_mov_b32 m0, s44
	s_nop 0
	global_load_lds_dwordx4 v168, s[30:31]
	s_mov_b32 m0, s45
	s_nop 0
	global_load_lds_dwordx4 v170, s[30:31]
	s_waitcnt vmcnt(8)
	s_waitcnt lgkmcnt(0)
	s_setprio 1
	v_mfma_f32_16x16x128_f8f6f4 v[94:97], v[18:25], v[194:201], 0
	v_mfma_f32_16x16x128_f8f6f4 v[90:93], v[26:33], v[194:201], 0
	v_mfma_f32_16x16x128_f8f6f4 v[78:81], v[18:25], v[202:209], 0
	v_mfma_f32_16x16x128_f8f6f4 v[74:77], v[26:33], v[202:209], 0
	v_mfma_f32_16x16x128_f8f6f4 v[62:65], v[18:25], v[210:217], 0
	v_mfma_f32_16x16x128_f8f6f4 v[58:61], v[26:33], v[210:217], 0
	v_mfma_f32_16x16x128_f8f6f4 v[46:49], v[18:25], v[218:225], 0
	v_mfma_f32_16x16x128_f8f6f4 v[42:45], v[26:33], v[218:225], 0
	s_nop 3
	s_setprio 0
	s_setprio 1
	v_mfma_f32_16x16x128_f8f6f4 v[86:89], v[2:9], v[194:201], 0
	v_mfma_f32_16x16x128_f8f6f4 v[82:85], v[10:17], v[194:201], 0
	v_mfma_f32_16x16x128_f8f6f4 v[70:73], v[2:9], v[202:209], 0
	v_mfma_f32_16x16x128_f8f6f4 v[66:69], v[10:17], v[202:209], 0
	v_mfma_f32_16x16x128_f8f6f4 v[54:57], v[2:9], v[210:217], 0
	v_mfma_f32_16x16x128_f8f6f4 v[50:53], v[10:17], v[210:217], 0
	v_mfma_f32_16x16x128_f8f6f4 v[38:41], v[2:9], v[218:225], 0
	v_mfma_f32_16x16x128_f8f6f4 v[34:37], v[10:17], v[218:225], 0
	s_setprio 0
	s_barrier
	s_add_i32 s69, 0, 0x18000
	s_add_i32 s70, 0, 0x1c000
	v_add_u32_e32 v14, s69, v187
	v_add_u32_e32 v30, s70, v187
	ds_read_b128 v[2:5], v14
	ds_read_b128 v[6:9], v14 offset:1024
	ds_read_b128 v[10:13], v14 offset:2048
	ds_read_b128 v[14:17], v14 offset:3072
	ds_read_b128 v[18:21], v30
	ds_read_b128 v[22:25], v30 offset:1024
	ds_read_b128 v[26:29], v30 offset:2048
	ds_read_b128 v[30:33], v30 offset:3072
	s_mov_b32 m0, s46
	ds_read_b128 v[194:197], v191 offset:32768
	ds_read_b128 v[198:201], v191 offset:33792
	ds_read_b128 v[202:205], v191 offset:34816
	ds_read_b128 v[206:209], v191 offset:35840
	ds_read_b128 v[210:213], v191 offset:36864
	ds_read_b128 v[214:217], v191 offset:37888
	ds_read_b128 v[218:221], v191 offset:38912
	ds_read_b128 v[222:225], v191 offset:39936
	global_load_lds_dwordx4 v172, s[30:31]
	s_mov_b32 m0, s47
	s_nop 0
	global_load_lds_dwordx4 v174, s[30:31]
	s_waitcnt vmcnt(8)
	s_waitcnt lgkmcnt(0)
	s_setprio 1
	v_mfma_f32_16x16x128_f8f6f4 v[158:161], v[2:9], v[194:201], v[158:161]
	v_mfma_f32_16x16x128_f8f6f4 v[154:157], v[10:17], v[194:201], v[154:157]
	v_mfma_f32_16x16x128_f8f6f4 v[142:145], v[2:9], v[202:209], v[142:145]
	v_mfma_f32_16x16x128_f8f6f4 v[138:141], v[10:17], v[202:209], v[138:141]
	v_mfma_f32_16x16x128_f8f6f4 v[126:129], v[2:9], v[210:217], v[126:129]
	v_mfma_f32_16x16x128_f8f6f4 v[122:125], v[10:17], v[210:217], v[122:125]
	v_mfma_f32_16x16x128_f8f6f4 v[110:113], v[2:9], v[218:225], v[110:113]
	v_mfma_f32_16x16x128_f8f6f4 v[106:109], v[10:17], v[218:225], v[106:109]
	s_nop 3
	s_setprio 0
	s_setprio 1
	v_mfma_f32_16x16x128_f8f6f4 v[150:153], v[18:25], v[194:201], v[150:153]
	v_mfma_f32_16x16x128_f8f6f4 v[146:149], v[26:33], v[194:201], v[146:149]
	v_mfma_f32_16x16x128_f8f6f4 v[134:137], v[18:25], v[202:209], v[134:137]
	v_mfma_f32_16x16x128_f8f6f4 v[130:133], v[26:33], v[202:209], v[130:133]
	v_mfma_f32_16x16x128_f8f6f4 v[118:121], v[18:25], v[210:217], v[118:121]
	v_mfma_f32_16x16x128_f8f6f4 v[114:117], v[26:33], v[210:217], v[114:117]
	v_mfma_f32_16x16x128_f8f6f4 v[102:105], v[18:25], v[218:225], v[102:105]
	v_mfma_f32_16x16x128_f8f6f4 v[98:101], v[26:33], v[218:225], v[98:101]
	s_setprio 0
	s_barrier
; #define PG8_STAGE(bufoff, gbase, voff) do { _Pragma("unroll") for (int _i = 0; _i < 2; ++_i) \
;         __builtin_amdgcn_global_load_lds((const unsigned*)((const char*)(gbase) + (voff)[_i]), (PG8_LAS unsigned*)(lds + (bufoff) + ldsw + _i * 8192), 16, 0, 0); } while (0)
; #define PG8_WAIT_V(n) asm volatile("s_waitcnt vmcnt(" #n ")" ::: "memory")
; #define PG8_WAIT_L(n) asm volatile("s_waitcnt lgkmcnt(" #n ")" ::: "memory")
; #define PG8_BAR __builtin_amdgcn_s_barrier()
; #define PG8_SCHED __builtin_amdgcn_sched_barrier(0)
; template <class Epi, class Sched, bool ALIGN_EPI = true, bool F8 = false>
; __device__ __forceinline__ void gemm_phase(PG8_LAS unsigned char* lds, const Sched& S, const Epi& E) {
;     ...
;             PG8_LDB(B0, 0, 0); PG8_LDB(B1, 0, 1); PG8_SCHED; PG8_LDA(At, 0, 0); PG8_STAGE(PG8_SA(1, 1), a1, voffA[1]);
;             PG8_WAIT_V(8); PG8_WAIT_L(0); PG8_BAR; PG8_MMA(0, 0, At, B0); PG8_MMA(0, 1, At, B1); PG8_BAR; PG8_SCHED;
;             PG8_LDA(At, 0, 1); PG8_STAGE(PG8_SB(0, 0), b2, voffB[0]); PG8_STAGE(PG8_SB(0, 1), b2, voffB[1]); PG8_STAGE(PG8_SA(0, 0), a2, vA2[0]);
;             PG8_WAIT_V(8); PG8_WAIT_L(0); PG8_BAR; PG8_MMA(1, 0, At, B0); PG8_MMA(1, 1, At, B1); PG8_BAR; PG8_SCHED;
;             PG8_LDB(B0, 1, 0); PG8_LDB(B1, 1, 1); PG8_SCHED; PG8_LDA(At, 1, 0); PG8_STAGE(PG8_SA(0, 1), a2, vA2[1]);
;             PG8_WAIT_V(8); PG8_WAIT_L(0); PG8_BAR; PG8_MMA(0, 0, At, B0); PG8_MMA(0, 1, At, B1); PG8_BAR; PG8_SCHED;
;             PG8_LDA(At, 1, 1); PG8_STAGE(PG8_SB(1, 0), b3, voffB[0]); PG8_STAGE(PG8_SB(1, 1), b3, voffB[1]); PG8_STAGE(PG8_SA(1, 0), a3, vA2[0]);
;             PG8_WAIT_V(8); PG8_WAIT_L(0); PG8_BAR; PG8_MMA(1, 0, At, B0); PG8_MMA(1, 1, At, B1); PG8_BAR; PG8_SCHED;
	s_add_u32 s28, s28, 0x8000
	s_addc_u32 s29, s29, 0
	s_add_i32 s30, s69, s43
	s_mov_b32 m0, s30
	ds_read_b128 v[194:197], v191 offset:49152
	ds_read_b128 v[198:201], v191 offset:50176
	ds_read_b128 v[202:205], v191 offset:51200
	ds_read_b128 v[206:209], v191 offset:52224
	ds_read_b128 v[210:213], v191 offset:53248
	ds_read_b128 v[214:217], v191 offset:54272
	ds_read_b128 v[218:221], v191 offset:55296
	ds_read_b128 v[222:225], v191 offset:56320
	global_load_lds_dwordx4 v164, s[28:29]
	s_add_i32 m0, s30, 0x2000
	s_add_i32 s30, s70, s43
	global_load_lds_dwordx4 v166, s[28:29]
	s_mov_b32 m0, s30
	s_nop 0
	global_load_lds_dwordx4 v178, s[28:29]
	s_add_i32 m0, s30, 0x2000
	s_nop 0
	global_load_lds_dwordx4 v180, s[28:29]
	s_mov_b32 m0, s51
	s_nop 0
	global_load_lds_dwordx4 v168, s[26:27]
	s_mov_b32 m0, s52
	s_nop 0
	global_load_lds_dwordx4 v170, s[26:27]
	s_waitcnt vmcnt(8)
	s_waitcnt lgkmcnt(0)
	s_setprio 1
	v_mfma_f32_16x16x128_f8f6f4 v[94:97], v[2:9], v[194:201], v[94:97]
	v_mfma_f32_16x16x128_f8f6f4 v[90:93], v[10:17], v[194:201], v[90:93]
	v_mfma_f32_16x16x128_f8f6f4 v[78:81], v[2:9], v[202:209], v[78:81]
	v_mfma_f32_16x16x128_f8f6f4 v[74:77], v[10:17], v[202:209], v[74:77]
	v_mfma_f32_16x16x128_f8f6f4 v[62:65], v[2:9], v[210:217], v[62:65]
	v_mfma_f32_16x16x128_f8f6f4 v[58:61], v[10:17], v[210:217], v[58:61]
	v_mfma_f32_16x16x128_f8f6f4 v[46:49], v[2:9], v[218:225], v[46:49]
	v_mfma_f32_16x16x128_f8f6f4 v[42:45], v[10:17], v[218:225], v[42:45]
	s_nop 3
	s_setprio 0
	s_setprio 1
	v_mfma_f32_16x16x128_f8f6f4 v[86:89], v[18:25], v[194:201], v[86:89]
	v_mfma_f32_16x16x128_f8f6f4 v[82:85], v[26:33], v[194:201], v[82:85]
	v_mfma_f32_16x16x128_f8f6f4 v[70:73], v[18:25], v[202:209], v[70:73]
	v_mfma_f32_16x16x128_f8f6f4 v[66:69], v[26:33], v[202:209], v[66:69]
	v_mfma_f32_16x16x128_f8f6f4 v[54:57], v[18:25], v[210:217], v[54:57]
	v_mfma_f32_16x16x128_f8f6f4 v[50:53], v[26:33], v[210:217], v[50:53]
	v_mfma_f32_16x16x128_f8f6f4 v[38:41], v[18:25], v[218:225], v[38:41]
	v_mfma_f32_16x16x128_f8f6f4 v[34:37], v[26:33], v[218:225], v[34:37]
	s_setprio 0
	s_barrier
	s_add_i32 s68, s68, 2
	s_add_u32 s23, s23, 0x10000
	s_addc_u32 s67, s67, 0
	s_add_u32 s24, s24, 0x10000
	s_addc_u32 s25, s25, 0
	s_cmp_gt_u32 s68, 5
	s_cbranch_scc0 .LBB0_1138
	s_branch .Lfx_33571
.LBB0_1138:
	ds_read_b128 v[18:21], v189
	ds_read_b128 v[22:25], v189 offset:1024
	ds_read_b128 v[26:29], v189 offset:2048
	ds_read_b128 v[30:33], v189 offset:3072
	ds_read_b128 v[2:5], v190
	ds_read_b128 v[6:9], v190 offset:1024
	ds_read_b128 v[10:13], v190 offset:2048
	ds_read_b128 v[14:17], v190 offset:3072
	s_add_u32 s26, s24, 0x8000
	s_addc_u32 s27, s25, 0
	s_cmp_eq_u32 s68, 4
	s_cselect_b32 s30, s16, s26
	s_cselect_b32 s31, s17, s27
	s_cselect_b32 s28, s18, s23
	s_cselect_b32 s29, s19, s67
	s_add_u32 s26, s30, 0x8000
	s_addc_u32 s27, s31, 0
	s_add_i32 m0, s44, 0xc000
	ds_read_b128 v[194:197], v191
	ds_read_b128 v[198:201], v191 offset:1024
	ds_read_b128 v[202:205], v191 offset:2048
	ds_read_b128 v[206:209], v191 offset:3072
	ds_read_b128 v[210:213], v191 offset:4096
	ds_read_b128 v[214:217], v191 offset:5120
	ds_read_b128 v[218:221], v191 offset:6144
	ds_read_b128 v[222:225], v191 offset:7168
	global_load_lds_dwordx4 v184, s[24:25]
	s_add_i32 m0, s44, 0xe000
	s_nop 0
	global_load_lds_dwordx4 v182, s[24:25]
	s_waitcnt vmcnt(8)
	s_waitcnt lgkmcnt(0)
	s_setprio 1
	v_mfma_f32_16x16x128_f8f6f4 v[158:161], v[18:25], v[194:201], v[158:161]
	v_mfma_f32_16x16x128_f8f6f4 v[154:157], v[26:33], v[194:201], v[154:157]
	v_mfma_f32_16x16x128_f8f6f4 v[142:145], v[18:25], v[202:209], v[142:145]
	v_mfma_f32_16x16x128_f8f6f4 v[138:141], v[26:33], v[202:209], v[138:141]
	v_mfma_f32_16x16x128_f8f6f4 v[126:129], v[18:25], v[210:217], v[126:129]
	v_mfma_f32_16x16x128_f8f6f4 v[122:125], v[26:33], v[210:217], v[122:125]
	v_mfma_f32_16x16x128_f8f6f4 v[110:113], v[18:25], v[218:225], v[110:113]
	v_mfma_f32_16x16x128_f8f6f4 v[106:109], v[26:33], v[218:225], v[106:109]
	s_nop 3
	s_setprio 0
	s_setprio 1
	v_mfma_f32_16x16x128_f8f6f4 v[150:153], v[2:9], v[194:201], v[150:153]
	v_mfma_f32_16x16x128_f8f6f4 v[146:149], v[10:17], v[194:201], v[146:149]
	v_mfma_f32_16x16x128_f8f6f4 v[134:137], v[2:9], v[202:209], v[134:137]
	v_mfma_f32_16x16x128_f8f6f4 v[130:133], v[10:17], v[202:209], v[130:133]
	v_mfma_f32_16x16x128_f8f6f4 v[118:121], v[2:9], v[210:217], v[118:121]
	v_mfma_f32_16x16x128_f8f6f4 v[114:117], v[10:17], v[210:217], v[114:117]
	v_mfma_f32_16x16x128_f8f6f4 v[102:105], v[2:9], v[218:225], v[102:105]
	v_mfma_f32_16x16x128_f8f6f4 v[98:101], v[10:17], v[218:225], v[98:101]
	s_setprio 0
	s_barrier
; #define PG8_STAGE(bufoff, gbase, voff) do { _Pragma("unroll") for (int _i = 0; _i < 2; ++_i) \
;         __builtin_amdgcn_global_load_lds((const unsigned*)((const char*)(gbase) + (voff)[_i]), (PG8_LAS unsigned*)(lds + (bufoff) + ldsw + _i * 8192), 16, 0, 0); } while (0)
; #define PG8_WAIT_V(n) asm volatile("s_waitcnt vmcnt(" #n ")" ::: "memory")
; #define PG8_WAIT_L(n) asm volatile("s_waitcnt lgkmcnt(" #n ")" ::: "memory")
; #define PG8_BAR __builtin_amdgcn_s_barrier()
; #define PG8_SCHED __builtin_amdgcn_sched_barrier(0)
; template <class Epi, class Sched, bool ALIGN_EPI = true, bool F8 = false>
; __device__ __forceinline__ void gemm_phase(PG8_LAS unsigned char* lds, const Sched& S, const Epi& E) {
;     ...
;             const char* a1 = cA + (size_t)(t + 1) * kstep;
;             const char* a2 = last ? nA : cA + (size_t)(t + 2) * kstep; const char* b2 = last ? nB : cB + (size_t)(t + 2) * kstepB;
;             const char* a3 = a2 + kstep; const char* b3 = b2 + kstepB;
;             unsigned vA2[2][2];
; #pragma unroll
;             for (int h = 0; h < 2; ++h)
; #pragma unroll
;                 for (int i = 0; i < 2; ++i) { if constexpr (Sched::GATHER) vA2[h][i] = (last && has_next) ? voffAn[h][i] : voffA[h][i]; else vA2[h][i] = voffA[h][i]; }
;             PG8_LDB(B0, 0, 0); PG8_LDB(B1, 0, 1); PG8_SCHED; PG8_LDA(At, 0, 0); PG8_STAGE(PG8_SA(1, 1), a1, voffA[1]);
;             PG8_WAIT_V(8); PG8_WAIT_L(0); PG8_BAR; PG8_MMA(0, 0, At, B0); PG8_MMA(0, 1, At, B1); PG8_BAR; PG8_SCHED;
;             PG8_LDA(At, 0, 1); PG8_STAGE(PG8_SB(0, 0), b2, voffB[0]); PG8_STAGE(PG8_SB(0, 1), b2, voffB[1]); PG8_STAGE(PG8_SA(0, 0), a2, vA2[0]);
;             PG8_WAIT_V(8); PG8_WAIT_L(0); PG8_BAR; PG8_MMA(1, 0, At, B0); PG8_MMA(1, 1, At, B1); PG8_BAR; PG8_SCHED;
;             PG8_LDB(B0, 1, 0); PG8_LDB(B1, 1, 1); PG8_SCHED; PG8_LDA(At, 1, 0); PG8_STAGE(PG8_SA(0, 1), a2, vA2[1]);
;             PG8_WAIT_V(8); PG8_WAIT_L(0); PG8_BAR; PG8_MMA(0, 0, At, B0); PG8_MMA(0, 1, At, B1); PG8_BAR; PG8_SCHED;
;             PG8_LDA(At, 1, 1); PG8_STAGE(PG8_SB(1, 0), b3, voffB[0]); PG8_STAGE(PG8_SB(1, 1), b3, voffB[1]); PG8_STAGE(PG8_SA(1, 0), a3, vA2[0]);
;             PG8_WAIT_V(8); PG8_WAIT_L(0); PG8_BAR; PG8_MMA(1, 0, At, B0); PG8_MMA(1, 1, At, B1); PG8_BAR; PG8_SCHED;
	s_add_i32 s69, s53, s43
	s_mov_b32 m0, s69
	ds_read_b128 v[194:197], v191 offset:16384
	ds_read_b128 v[198:201], v191 offset:17408
	ds_read_b128 v[202:205], v191 offset:18432
	ds_read_b128 v[206:209], v191 offset:19456
	ds_read_b128 v[210:213], v191 offset:20480
	ds_read_b128 v[214:217], v191 offset:21504
	ds_read_b128 v[218:221], v191 offset:22528
	ds_read_b128 v[222:225], v191 offset:23552
	global_load_lds_dwordx4 v164, s[28:29]
	s_add_i32 m0, s69, 0x2000
	s_add_i32 s69, s58, s43
	global_load_lds_dwordx4 v166, s[28:29]
	s_add_u32 s98, s28, s4
	s_addc_u32 s99, s29, s5
	s_mov_b32 m0, s69
	s_nop 0
	global_load_lds_dwordx4 v164, s[98:99]
	s_add_u32 s100, s28, s4
	s_addc_u32 s101, s29, s5
	s_add_i32 m0, s69, 0x2000
	s_nop 0
	global_load_lds_dwordx4 v166, s[100:101]
	s_mov_b32 m0, s44
	s_nop 0
	global_load_lds_dwordx4 v168, s[30:31]
	s_mov_b32 m0, s45
	s_nop 0
	global_load_lds_dwordx4 v170, s[30:31]
	s_waitcnt vmcnt(8)
	s_waitcnt lgkmcnt(0)
	s_setprio 1
	v_mfma_f32_16x16x128_f8f6f4 v[94:97], v[18:25], v[194:201], v[94:97]
	v_mfma_f32_16x16x128_f8f6f4 v[90:93], v[26:33], v[194:201], v[90:93]
	v_mfma_f32_16x16x128_f8f6f4 v[78:81], v[18:25], v[202:209], v[78:81]
	v_mfma_f32_16x16x128_f8f6f4 v[74:77], v[26:33], v[202:209], v[74:77]
	v_mfma_f32_16x16x128_f8f6f4 v[62:65], v[18:25], v[210:217], v[62:65]
	v_mfma_f32_16x16x128_f8f6f4 v[58:61], v[26:33], v[210:217], v[58:61]
	v_mfma_f32_16x16x128_f8f6f4 v[46:49], v[18:25], v[218:225], v[46:49]
	v_mfma_f32_16x16x128_f8f6f4 v[42:45], v[26:33], v[218:225], v[42:45]
	s_nop 3
	s_setprio 0
	s_setprio 1
	v_mfma_f32_16x16x128_f8f6f4 v[86:89], v[2:9], v[194:201], v[86:89]
	v_mfma_f32_16x16x128_f8f6f4 v[82:85], v[10:17], v[194:201], v[82:85]
	v_mfma_f32_16x16x128_f8f6f4 v[70:73], v[2:9], v[202:209], v[70:73]
	v_mfma_f32_16x16x128_f8f6f4 v[66:69], v[10:17], v[202:209], v[66:69]
	v_mfma_f32_16x16x128_f8f6f4 v[54:57], v[2:9], v[210:217], v[54:57]
	v_mfma_f32_16x16x128_f8f6f4 v[50:53], v[10:17], v[210:217], v[50:53]
	v_mfma_f32_16x16x128_f8f6f4 v[38:41], v[2:9], v[218:225], v[38:41]
	v_mfma_f32_16x16x128_f8f6f4 v[34:37], v[10:17], v[218:225], v[34:37]
	s_setprio 0
	s_barrier
	s_add_i32 s69, 0, 0x18000
	s_add_i32 s70, 0, 0x1c000
	v_add_u32_e32 v14, s69, v187
	v_add_u32_e32 v30, s70, v187
	ds_read_b128 v[2:5], v14
	ds_read_b128 v[6:9], v14 offset:1024
	ds_read_b128 v[10:13], v14 offset:2048
	ds_read_b128 v[14:17], v14 offset:3072
	ds_read_b128 v[18:21], v30
	ds_read_b128 v[22:25], v30 offset:1024
	ds_read_b128 v[26:29], v30 offset:2048
	ds_read_b128 v[30:33], v30 offset:3072
	s_mov_b32 m0, s46
	ds_read_b128 v[194:197], v191 offset:32768
	ds_read_b128 v[198:201], v191 offset:33792
	ds_read_b128 v[202:205], v191 offset:34816
	ds_read_b128 v[206:209], v191 offset:35840
	ds_read_b128 v[210:213], v191 offset:36864
	ds_read_b128 v[214:217], v191 offset:37888
	ds_read_b128 v[218:221], v191 offset:38912
	ds_read_b128 v[222:225], v191 offset:39936
	global_load_lds_dwordx4 v172, s[30:31]
	s_mov_b32 m0, s47
	s_nop 0
	global_load_lds_dwordx4 v174, s[30:31]
	s_waitcnt vmcnt(8)
	s_waitcnt lgkmcnt(0)
	s_setprio 1
	v_mfma_f32_16x16x128_f8f6f4 v[158:161], v[2:9], v[194:201], v[158:161]
	v_mfma_f32_16x16x128_f8f6f4 v[154:157], v[10:17], v[194:201], v[154:157]
	v_mfma_f32_16x16x128_f8f6f4 v[142:145], v[2:9], v[202:209], v[142:145]
	v_mfma_f32_16x16x128_f8f6f4 v[138:141], v[10:17], v[202:209], v[138:141]
	v_mfma_f32_16x16x128_f8f6f4 v[126:129], v[2:9], v[210:217], v[126:129]
	v_mfma_f32_16x16x128_f8f6f4 v[122:125], v[10:17], v[210:217], v[122:125]
	v_mfma_f32_16x16x128_f8f6f4 v[110:113], v[2:9], v[218:225], v[110:113]
	v_mfma_f32_16x16x128_f8f6f4 v[106:109], v[10:17], v[218:225], v[106:109]
	s_nop 3
	s_setprio 0
	s_setprio 1
	v_mfma_f32_16x16x128_f8f6f4 v[150:153], v[18:25], v[194:201], v[150:153]
	v_mfma_f32_16x16x128_f8f6f4 v[146:149], v[26:33], v[194:201], v[146:149]
	v_mfma_f32_16x16x128_f8f6f4 v[134:137], v[18:25], v[202:209], v[134:137]
	v_mfma_f32_16x16x128_f8f6f4 v[130:133], v[26:33], v[202:209], v[130:133]
	v_mfma_f32_16x16x128_f8f6f4 v[118:121], v[18:25], v[210:217], v[118:121]
	v_mfma_f32_16x16x128_f8f6f4 v[114:117], v[26:33], v[210:217], v[114:117]
	v_mfma_f32_16x16x128_f8f6f4 v[102:105], v[18:25], v[218:225], v[102:105]
	v_mfma_f32_16x16x128_f8f6f4 v[98:101], v[26:33], v[218:225], v[98:101]
	s_setprio 0
	s_barrier
	s_add_u32 s28, s28, 0x8000
	s_addc_u32 s29, s29, 0
	s_add_i32 s30, s69, s43
	s_mov_b32 m0, s30
	ds_read_b128 v[194:197], v191 offset:49152
	ds_read_b128 v[198:201], v191 offset:50176
	ds_read_b128 v[202:205], v191 offset:51200
	ds_read_b128 v[206:209], v191 offset:52224
	ds_read_b128 v[210:213], v191 offset:53248
	ds_read_b128 v[214:217], v191 offset:54272
	ds_read_b128 v[218:221], v191 offset:55296
	ds_read_b128 v[222:225], v191 offset:56320
	global_load_lds_dwordx4 v164, s[28:29]
	s_add_i32 m0, s30, 0x2000
	s_add_i32 s30, s70, s43
	global_load_lds_dwordx4 v166, s[28:29]
	s_mov_b32 m0, s30
	s_nop 0
	global_load_lds_dwordx4 v178, s[28:29]
	s_add_i32 m0, s30, 0x2000
	s_nop 0
	global_load_lds_dwordx4 v180, s[28:29]
	s_mov_b32 m0, s51
	s_nop 0
	global_load_lds_dwordx4 v168, s[26:27]
	s_mov_b32 m0, s52
	s_nop 0
	global_load_lds_dwordx4 v170, s[26:27]
	s_waitcnt vmcnt(8)
	s_waitcnt lgkmcnt(0)
	s_setprio 1
	v_mfma_f32_16x16x128_f8f6f4 v[94:97], v[2:9], v[194:201], v[94:97]
	v_mfma_f32_16x16x128_f8f6f4 v[90:93], v[10:17], v[194:201], v[90:93]
	v_mfma_f32_16x16x128_f8f6f4 v[78:81], v[2:9], v[202:209], v[78:81]
	v_mfma_f32_16x16x128_f8f6f4 v[74:77], v[10:17], v[202:209], v[74:77]
	v_mfma_f32_16x16x128_f8f6f4 v[62:65], v[2:9], v[210:217], v[62:65]
	v_mfma_f32_16x16x128_f8f6f4 v[58:61], v[10:17], v[210:217], v[58:61]
	v_mfma_f32_16x16x128_f8f6f4 v[46:49], v[2:9], v[218:225], v[46:49]
	v_mfma_f32_16x16x128_f8f6f4 v[42:45], v[10:17], v[218:225], v[42:45]
	s_nop 3
	s_setprio 0
	s_setprio 1
	v_mfma_f32_16x16x128_f8f6f4 v[86:89], v[18:25], v[194:201], v[86:89]
	v_mfma_f32_16x16x128_f8f6f4 v[82:85], v[26:33], v[194:201], v[82:85]
	v_mfma_f32_16x16x128_f8f6f4 v[70:73], v[18:25], v[202:209], v[70:73]
	v_mfma_f32_16x16x128_f8f6f4 v[66:69], v[26:33], v[202:209], v[66:69]
	v_mfma_f32_16x16x128_f8f6f4 v[54:57], v[18:25], v[210:217], v[54:57]
	v_mfma_f32_16x16x128_f8f6f4 v[50:53], v[26:33], v[210:217], v[50:53]
	v_mfma_f32_16x16x128_f8f6f4 v[38:41], v[18:25], v[218:225], v[38:41]
	v_mfma_f32_16x16x128_f8f6f4 v[34:37], v[26:33], v[218:225], v[34:37]
	s_setprio 0
	s_barrier
	s_add_i32 s68, s68, 2
	s_add_u32 s23, s23, 0x10000
	s_addc_u32 s67, s67, 0
	s_add_u32 s24, s24, 0x10000
	s_addc_u32 s25, s25, 0
	s_cmp_gt_u32 s68, 5
	s_cbranch_scc0 .LBB0_1138
	s_branch .Lfx_33571
; #define PG8_STAGE(bufoff, gbase, voff) do { _Pragma("unroll") for (int _i = 0; _i < 2; ++_i) \
;         __builtin_amdgcn_global_load_lds((const unsigned*)((const char*)(gbase) + (voff)[_i]), (PG8_LAS unsigned*)(lds + (bufoff) + ldsw + _i * 8192), 16, 0, 0); } while (0)
; template <class Epi, class Sched, bool ALIGN_EPI = true, bool F8 = false>
; __device__ __forceinline__ void gemm_phase(PG8_LAS unsigned char* lds, const Sched& S, const Epi& E) {
;     ...
;         const bool has_next = S.next(ui + 1, nxt);
;         const char* nA = has_next ? nxt.A : cA; const char* nB = has_next ? nxt.B : cB;
;         const int nt = cur.nt;
; #pragma unroll 1
;         for (int t = 0; t < nt; t += 2) {
;             const bool last = (t == nt - 2);
;             if constexpr (Sched::GATHER) { if (last && has_next) S.a_off(nxt, Rs, Cs, voffAn); }
;             const char* a1 = cA + (size_t)(t + 1) * kstep;
;             const char* a2 = last ? nA : cA + (size_t)(t + 2) * kstep; const char* b2 = last ? nB : cB + (size_t)(t + 2) * kstepB;
;             const char* a3 = a2 + kstep; const char* b3 = b2 + kstepB;
;             unsigned vA2[2][2];
; #pragma unroll
;             for (int h = 0; h < 2; ++h)
; #pragma unroll
;                 for (int i = 0; i < 2; ++i) { if constexpr (Sched::GATHER) vA2[h][i] = (last && has_next) ? voffAn[h][i] : voffA[h][i]; else vA2[h][i] = voffA[h][i]; }
;             PG8_LDB(B0, 0, 0); PG8_LDB(B1, 0, 1); PG8_SCHED; PG8_LDA(At, 0, 0); PG8_STAGE(PG8_SA(1, 1), a1, voffA[1]);
;             PG8_WAIT_V(8); PG8_WAIT_L(0); PG8_BAR; PG8_MMA(0, 0, At, B0); PG8_MMA(0, 1, At, B1); PG8_BAR; PG8_SCHED;
;             PG8_LDA(At, 0, 1); PG8_STAGE(PG8_SB(0, 0), b2, voffB[0]); PG8_STAGE(PG8_SB(0, 1), b2, voffB[1]); PG8_STAGE(PG8_SA(0, 0), a2, vA2[0]);
;             PG8_WAIT_V(8); PG8_WAIT_L(0); PG8_BAR; PG8_MMA(1, 0, At, B0); PG8_MMA(1, 1, At, B1); PG8_BAR; PG8_SCHED;
;             PG8_LDB(B0, 1, 0); PG8_LDB(B1, 1, 1); PG8_SCHED; PG8_LDA(At, 1, 0); PG8_STAGE(PG8_SA(0, 1), a2, vA2[1]);
;             PG8_WAIT_V(8); PG8_WAIT_L(0); PG8_BAR; PG8_MMA(0, 0, At, B0); PG8_MMA(0, 1, At, B1); PG8_BAR; PG8_SCHED;
;             PG8_LDA(At, 1, 1); PG8_STAGE(PG8_SB(1, 0), b3, voffB[0]); PG8_STAGE(PG8_SB(1, 1), b3, voffB[1]); PG8_STAGE(PG8_SA(1, 0), a3, vA2[0]);
;             PG8_WAIT_V(8); PG8_WAIT_L(0); PG8_BAR; PG8_MMA(1, 0, At, B0); PG8_MMA(1, 1, At, B1); PG8_BAR; PG8_SCHED;
.Lh1e_33571:
.Lpk1_1138:
	ds_read_b128 v[18:21], v189
	ds_read_b128 v[22:25], v189 offset:1024
	ds_read_b128 v[26:29], v189 offset:2048
	ds_read_b128 v[30:33], v189 offset:3072
	ds_read_b128 v[2:5], v190
	ds_read_b128 v[6:9], v190 offset:1024
	ds_read_b128 v[10:13], v190 offset:2048
	ds_read_b128 v[14:17], v190 offset:3072
	s_add_u32 s26, s24, 0x8000
	s_addc_u32 s27, s25, 0
	s_cmp_eq_u32 s68, 4
	s_cselect_b32 s30, s16, s26
	s_cselect_b32 s31, s17, s27
	s_cselect_b32 s28, s18, s23
	s_cselect_b32 s29, s19, s67
	s_add_u32 s26, s30, 0x8000
	s_addc_u32 s27, s31, 0
	s_add_i32 m0, s44, 0xc000
	ds_read_b128 v[194:197], v191
	ds_read_b128 v[198:201], v191 offset:1024
	ds_read_b128 v[202:205], v191 offset:2048
	ds_read_b128 v[206:209], v191 offset:3072
	ds_read_b128 v[210:213], v191 offset:4096
	ds_read_b128 v[214:217], v191 offset:5120
	ds_read_b128 v[218:221], v191 offset:6144
	ds_read_b128 v[222:225], v191 offset:7168
	global_load_lds_dwordx4 v184, s[24:25]
	s_add_i32 m0, s44, 0xe000
	s_nop 0
	global_load_lds_dwordx4 v182, s[24:25]
	s_waitcnt vmcnt(8)
	s_waitcnt lgkmcnt(0)
	s_barrier
	s_setprio 2
	v_mfma_f32_16x16x128_f8f6f4 v[158:161], v[18:25], v[194:201], 0
	v_mfma_f32_16x16x128_f8f6f4 v[154:157], v[26:33], v[194:201], 0
	v_mfma_f32_16x16x128_f8f6f4 v[142:145], v[18:25], v[202:209], 0
	v_mfma_f32_16x16x128_f8f6f4 v[138:141], v[26:33], v[202:209], 0
	v_mfma_f32_16x16x128_f8f6f4 v[126:129], v[18:25], v[210:217], 0
	v_mfma_f32_16x16x128_f8f6f4 v[122:125], v[26:33], v[210:217], 0
	v_mfma_f32_16x16x128_f8f6f4 v[110:113], v[18:25], v[218:225], 0
	v_mfma_f32_16x16x128_f8f6f4 v[106:109], v[26:33], v[218:225], 0
	s_nop 3
	s_setprio 0
	s_setprio 2
	v_mfma_f32_16x16x128_f8f6f4 v[150:153], v[2:9], v[194:201], 0
	v_mfma_f32_16x16x128_f8f6f4 v[146:149], v[10:17], v[194:201], 0
	v_mfma_f32_16x16x128_f8f6f4 v[134:137], v[2:9], v[202:209], 0
	v_mfma_f32_16x16x128_f8f6f4 v[130:133], v[10:17], v[202:209], 0
	v_mfma_f32_16x16x128_f8f6f4 v[118:121], v[2:9], v[210:217], 0
	v_mfma_f32_16x16x128_f8f6f4 v[114:117], v[10:17], v[210:217], 0
	v_mfma_f32_16x16x128_f8f6f4 v[102:105], v[2:9], v[218:225], 0
	v_mfma_f32_16x16x128_f8f6f4 v[98:101], v[10:17], v[218:225], 0
	s_setprio 0
	s_add_i32 s69, s53, s43
	s_mov_b32 m0, s69
	ds_read_b128 v[194:197], v191 offset:16384
	ds_read_b128 v[198:201], v191 offset:17408
	ds_read_b128 v[202:205], v191 offset:18432
	ds_read_b128 v[206:209], v191 offset:19456
	ds_read_b128 v[210:213], v191 offset:20480
	ds_read_b128 v[214:217], v191 offset:21504
	ds_read_b128 v[218:221], v191 offset:22528
	ds_read_b128 v[222:225], v191 offset:23552
	global_load_lds_dwordx4 v164, s[28:29]
	s_add_i32 m0, s69, 0x2000
	s_add_i32 s69, s58, s43
	global_load_lds_dwordx4 v166, s[28:29]
	s_add_u32 s98, s28, s4
	s_addc_u32 s99, s29, s5
	s_mov_b32 m0, s69
	s_nop 0
	global_load_lds_dwordx4 v164, s[98:99]
	s_add_u32 s100, s28, s4
	s_addc_u32 s101, s29, s5
	s_add_i32 m0, s69, 0x2000
	s_nop 0
	global_load_lds_dwordx4 v166, s[100:101]
	s_mov_b32 m0, s44
	s_nop 0
	global_load_lds_dwordx4 v168, s[30:31]
	s_mov_b32 m0, s45
	s_nop 0
	global_load_lds_dwordx4 v170, s[30:31]
	s_waitcnt vmcnt(8)
	s_waitcnt lgkmcnt(0)
	s_barrier
	s_setprio 2
	v_mfma_f32_16x16x128_f8f6f4 v[94:97], v[18:25], v[194:201], 0
	v_mfma_f32_16x16x128_f8f6f4 v[90:93], v[26:33], v[194:201], 0
	v_mfma_f32_16x16x128_f8f6f4 v[78:81], v[18:25], v[202:209], 0
	v_mfma_f32_16x16x128_f8f6f4 v[74:77], v[26:33], v[202:209], 0
	v_mfma_f32_16x16x128_f8f6f4 v[62:65], v[18:25], v[210:217], 0
	v_mfma_f32_16x16x128_f8f6f4 v[58:61], v[26:33], v[210:217], 0
	v_mfma_f32_16x16x128_f8f6f4 v[46:49], v[18:25], v[218:225], 0
	v_mfma_f32_16x16x128_f8f6f4 v[42:45], v[26:33], v[218:225], 0
	s_nop 3
	s_setprio 0
	s_setprio 2
	v_mfma_f32_16x16x128_f8f6f4 v[86:89], v[2:9], v[194:201], 0
	v_mfma_f32_16x16x128_f8f6f4 v[82:85], v[10:17], v[194:201], 0
	v_mfma_f32_16x16x128_f8f6f4 v[70:73], v[2:9], v[202:209], 0
	v_mfma_f32_16x16x128_f8f6f4 v[66:69], v[10:17], v[202:209], 0
	v_mfma_f32_16x16x128_f8f6f4 v[54:57], v[2:9], v[210:217], 0
	v_mfma_f32_16x16x128_f8f6f4 v[50:53], v[10:17], v[210:217], 0
	v_mfma_f32_16x16x128_f8f6f4 v[38:41], v[2:9], v[218:225], 0
	v_mfma_f32_16x16x128_f8f6f4 v[34:37], v[10:17], v[218:225], 0
	s_setprio 0
	s_add_i32 s69, 0, 0x18000
	s_add_i32 s70, 0, 0x1c000
	v_add_u32_e32 v14, s69, v187
	v_add_u32_e32 v30, s70, v187
	ds_read_b128 v[2:5], v14
	ds_read_b128 v[6:9], v14 offset:1024
	ds_read_b128 v[10:13], v14 offset:2048
	ds_read_b128 v[14:17], v14 offset:3072
	ds_read_b128 v[18:21], v30
	ds_read_b128 v[22:25], v30 offset:1024
	ds_read_b128 v[26:29], v30 offset:2048
	ds_read_b128 v[30:33], v30 offset:3072
	s_mov_b32 m0, s46
	ds_read_b128 v[194:197], v191 offset:32768
	ds_read_b128 v[198:201], v191 offset:33792
	ds_read_b128 v[202:205], v191 offset:34816
	ds_read_b128 v[206:209], v191 offset:35840
	ds_read_b128 v[210:213], v191 offset:36864
	ds_read_b128 v[214:217], v191 offset:37888
	ds_read_b128 v[218:221], v191 offset:38912
	ds_read_b128 v[222:225], v191 offset:39936
	global_load_lds_dwordx4 v172, s[30:31]
	s_mov_b32 m0, s47
	s_nop 0
	global_load_lds_dwordx4 v174, s[30:31]
	s_waitcnt vmcnt(8)
	s_waitcnt lgkmcnt(0)
	s_barrier
; #define PG8_STAGE(bufoff, gbase, voff) do { _Pragma("unroll") for (int _i = 0; _i < 2; ++_i) \
;         __builtin_amdgcn_global_load_lds((const unsigned*)((const char*)(gbase) + (voff)[_i]), (PG8_LAS unsigned*)(lds + (bufoff) + ldsw + _i * 8192), 16, 0, 0); } while (0)
; #define PG8_WAIT_V(n) asm volatile("s_waitcnt vmcnt(" #n ")" ::: "memory")
; #define PG8_WAIT_L(n) asm volatile("s_waitcnt lgkmcnt(" #n ")" ::: "memory")
; #define PG8_BAR __builtin_amdgcn_s_barrier()
; #define PG8_SCHED __builtin_amdgcn_sched_barrier(0)
; template <class Epi, class Sched, bool ALIGN_EPI = true, bool F8 = false>
; __device__ __forceinline__ void gemm_phase(PG8_LAS unsigned char* lds, const Sched& S, const Epi& E) {
;     ...
;             const char* a1 = cA + (size_t)(t + 1) * kstep;
;             const char* a2 = last ? nA : cA + (size_t)(t + 2) * kstep; const char* b2 = last ? nB : cB + (size_t)(t + 2) * kstepB;
;             const char* a3 = a2 + kstep; const char* b3 = b2 + kstepB;
;             unsigned vA2[2][2];
; #pragma unroll
;             for (int h = 0; h < 2; ++h)
; #pragma unroll
;                 for (int i = 0; i < 2; ++i) { if constexpr (Sched::GATHER) vA2[h][i] = (last && has_next) ? voffAn[h][i] : voffA[h][i]; else vA2[h][i] = voffA[h][i]; }
;             PG8_LDB(B0, 0, 0); PG8_LDB(B1, 0, 1); PG8_SCHED; PG8_LDA(At, 0, 0); PG8_STAGE(PG8_SA(1, 1), a1, voffA[1]);
;             PG8_WAIT_V(8); PG8_WAIT_L(0); PG8_BAR; PG8_MMA(0, 0, At, B0); PG8_MMA(0, 1, At, B1); PG8_BAR; PG8_SCHED;
;             PG8_LDA(At, 0, 1); PG8_STAGE(PG8_SB(0, 0), b2, voffB[0]); PG8_STAGE(PG8_SB(0, 1), b2, voffB[1]); PG8_STAGE(PG8_SA(0, 0), a2, vA2[0]);
;             PG8_WAIT_V(8); PG8_WAIT_L(0); PG8_BAR; PG8_MMA(1, 0, At, B0); PG8_MMA(1, 1, At, B1); PG8_BAR; PG8_SCHED;
;             PG8_LDB(B0, 1, 0); PG8_LDB(B1, 1, 1); PG8_SCHED; PG8_LDA(At, 1, 0); PG8_STAGE(PG8_SA(0, 1), a2, vA2[1]);
;             PG8_WAIT_V(8); PG8_WAIT_L(0); PG8_BAR; PG8_MMA(0, 0, At, B0); PG8_MMA(0, 1, At, B1); PG8_BAR; PG8_SCHED;
;             PG8_LDA(At, 1, 1); PG8_STAGE(PG8_SB(1, 0), b3, voffB[0]); PG8_STAGE(PG8_SB(1, 1), b3, voffB[1]); PG8_STAGE(PG8_SA(1, 0), a3, vA2[0]);
;             PG8_WAIT_V(8); PG8_WAIT_L(0); PG8_BAR; PG8_MMA(1, 0, At, B0); PG8_MMA(1, 1, At, B1); PG8_BAR; PG8_SCHED;
	s_setprio 2
	v_mfma_f32_16x16x128_f8f6f4 v[158:161], v[2:9], v[194:201], v[158:161]
	v_mfma_f32_16x16x128_f8f6f4 v[154:157], v[10:17], v[194:201], v[154:157]
	v_mfma_f32_16x16x128_f8f6f4 v[142:145], v[2:9], v[202:209], v[142:145]
	v_mfma_f32_16x16x128_f8f6f4 v[138:141], v[10:17], v[202:209], v[138:141]
	v_mfma_f32_16x16x128_f8f6f4 v[126:129], v[2:9], v[210:217], v[126:129]
	v_mfma_f32_16x16x128_f8f6f4 v[122:125], v[10:17], v[210:217], v[122:125]
	v_mfma_f32_16x16x128_f8f6f4 v[110:113], v[2:9], v[218:225], v[110:113]
	v_mfma_f32_16x16x128_f8f6f4 v[106:109], v[10:17], v[218:225], v[106:109]
	s_nop 3
	s_setprio 0
	s_setprio 2
	v_mfma_f32_16x16x128_f8f6f4 v[150:153], v[18:25], v[194:201], v[150:153]
	v_mfma_f32_16x16x128_f8f6f4 v[146:149], v[26:33], v[194:201], v[146:149]
	v_mfma_f32_16x16x128_f8f6f4 v[134:137], v[18:25], v[202:209], v[134:137]
	v_mfma_f32_16x16x128_f8f6f4 v[130:133], v[26:33], v[202:209], v[130:133]
	v_mfma_f32_16x16x128_f8f6f4 v[118:121], v[18:25], v[210:217], v[118:121]
	v_mfma_f32_16x16x128_f8f6f4 v[114:117], v[26:33], v[210:217], v[114:117]
	v_mfma_f32_16x16x128_f8f6f4 v[102:105], v[18:25], v[218:225], v[102:105]
	v_mfma_f32_16x16x128_f8f6f4 v[98:101], v[26:33], v[218:225], v[98:101]
	s_setprio 0
	s_add_u32 s28, s28, 0x8000
	s_addc_u32 s29, s29, 0
	s_add_i32 s30, s69, s43
	s_mov_b32 m0, s30
	ds_read_b128 v[194:197], v191 offset:49152
	ds_read_b128 v[198:201], v191 offset:50176
	ds_read_b128 v[202:205], v191 offset:51200
	ds_read_b128 v[206:209], v191 offset:52224
	ds_read_b128 v[210:213], v191 offset:53248
	ds_read_b128 v[214:217], v191 offset:54272
	ds_read_b128 v[218:221], v191 offset:55296
	ds_read_b128 v[222:225], v191 offset:56320
	global_load_lds_dwordx4 v164, s[28:29]
	s_add_i32 m0, s30, 0x2000
	s_add_i32 s30, s70, s43
	global_load_lds_dwordx4 v166, s[28:29]
	s_mov_b32 m0, s30
	s_nop 0
	global_load_lds_dwordx4 v178, s[28:29]
	s_add_i32 m0, s30, 0x2000
	s_nop 0
	global_load_lds_dwordx4 v180, s[28:29]
	s_mov_b32 m0, s51
	s_nop 0
	global_load_lds_dwordx4 v168, s[26:27]
	s_mov_b32 m0, s52
	s_nop 0
	global_load_lds_dwordx4 v170, s[26:27]
	s_waitcnt vmcnt(8)
	s_waitcnt lgkmcnt(0)
	s_barrier
	s_setprio 2
	v_mfma_f32_16x16x128_f8f6f4 v[94:97], v[2:9], v[194:201], v[94:97]
	v_mfma_f32_16x16x128_f8f6f4 v[90:93], v[10:17], v[194:201], v[90:93]
	v_mfma_f32_16x16x128_f8f6f4 v[78:81], v[2:9], v[202:209], v[78:81]
	v_mfma_f32_16x16x128_f8f6f4 v[74:77], v[10:17], v[202:209], v[74:77]
	v_mfma_f32_16x16x128_f8f6f4 v[62:65], v[2:9], v[210:217], v[62:65]
	v_mfma_f32_16x16x128_f8f6f4 v[58:61], v[10:17], v[210:217], v[58:61]
	v_mfma_f32_16x16x128_f8f6f4 v[46:49], v[2:9], v[218:225], v[46:49]
	v_mfma_f32_16x16x128_f8f6f4 v[42:45], v[10:17], v[218:225], v[42:45]
	s_nop 3
	s_setprio 0
	s_setprio 2
	v_mfma_f32_16x16x128_f8f6f4 v[86:89], v[18:25], v[194:201], v[86:89]
	v_mfma_f32_16x16x128_f8f6f4 v[82:85], v[26:33], v[194:201], v[82:85]
	v_mfma_f32_16x16x128_f8f6f4 v[70:73], v[18:25], v[202:209], v[70:73]
	v_mfma_f32_16x16x128_f8f6f4 v[66:69], v[26:33], v[202:209], v[66:69]
	v_mfma_f32_16x16x128_f8f6f4 v[54:57], v[18:25], v[210:217], v[54:57]
	v_mfma_f32_16x16x128_f8f6f4 v[50:53], v[26:33], v[210:217], v[50:53]
	v_mfma_f32_16x16x128_f8f6f4 v[38:41], v[18:25], v[218:225], v[38:41]
	v_mfma_f32_16x16x128_f8f6f4 v[34:37], v[26:33], v[218:225], v[34:37]
	s_setprio 0
	s_add_i32 s68, s68, 2
	s_add_u32 s23, s23, 0x10000
	s_addc_u32 s67, s67, 0
	s_add_u32 s24, s24, 0x10000
	s_addc_u32 s25, s25, 0
	s_cmp_gt_u32 s68, 5
	s_cbranch_scc0 .Lh1_1138
	s_branch .Lfx_33571
.Lh1_1138:
	ds_read_b128 v[18:21], v189
	ds_read_b128 v[22:25], v189 offset:1024
	ds_read_b128 v[26:29], v189 offset:2048
	ds_read_b128 v[30:33], v189 offset:3072
	ds_read_b128 v[2:5], v190
	ds_read_b128 v[6:9], v190 offset:1024
	ds_read_b128 v[10:13], v190 offset:2048
	ds_read_b128 v[14:17], v190 offset:3072
	s_add_u32 s26, s24, 0x8000
	s_addc_u32 s27, s25, 0
	s_cmp_eq_u32 s68, 4
	s_cselect_b32 s30, s16, s26
	s_cselect_b32 s31, s17, s27
	s_cselect_b32 s28, s18, s23
	s_cselect_b32 s29, s19, s67
	s_add_u32 s26, s30, 0x8000
	s_addc_u32 s27, s31, 0
	s_add_i32 m0, s44, 0xc000
	ds_read_b128 v[194:197], v191
	ds_read_b128 v[198:201], v191 offset:1024
	ds_read_b128 v[202:205], v191 offset:2048
	ds_read_b128 v[206:209], v191 offset:3072
	ds_read_b128 v[210:213], v191 offset:4096
	ds_read_b128 v[214:217], v191 offset:5120
	ds_read_b128 v[218:221], v191 offset:6144
	ds_read_b128 v[222:225], v191 offset:7168
	global_load_lds_dwordx4 v184, s[24:25]
	s_add_i32 m0, s44, 0xe000
	s_nop 0
	global_load_lds_dwordx4 v182, s[24:25]
	s_waitcnt vmcnt(8)
	s_waitcnt lgkmcnt(0)
	s_barrier
; #define PG8_STAGE(bufoff, gbase, voff) do { _Pragma("unroll") for (int _i = 0; _i < 2; ++_i) \
;         __builtin_amdgcn_global_load_lds((const unsigned*)((const char*)(gbase) + (voff)[_i]), (PG8_LAS unsigned*)(lds + (bufoff) + ldsw + _i * 8192), 16, 0, 0); } while (0)
; #define PG8_WAIT_V(n) asm volatile("s_waitcnt vmcnt(" #n ")" ::: "memory")
; #define PG8_WAIT_L(n) asm volatile("s_waitcnt lgkmcnt(" #n ")" ::: "memory")
; #define PG8_BAR __builtin_amdgcn_s_barrier()
; #define PG8_SCHED __builtin_amdgcn_sched_barrier(0)
; template <class Epi, class Sched, bool ALIGN_EPI = true, bool F8 = false>
; __device__ __forceinline__ void gemm_phase(PG8_LAS unsigned char* lds, const Sched& S, const Epi& E) {
;     ...
;             const char* a1 = cA + (size_t)(t + 1) * kstep;
;             const char* a2 = last ? nA : cA + (size_t)(t + 2) * kstep; const char* b2 = last ? nB : cB + (size_t)(t + 2) * kstepB;
;             const char* a3 = a2 + kstep; const char* b3 = b2 + kstepB;
;             unsigned vA2[2][2];
; #pragma unroll
;             for (int h = 0; h < 2; ++h)
; #pragma unroll
;                 for (int i = 0; i < 2; ++i) { if constexpr (Sched::GATHER) vA2[h][i] = (last && has_next) ? voffAn[h][i] : voffA[h][i]; else vA2[h][i] = voffA[h][i]; }
;             PG8_LDB(B0, 0, 0); PG8_LDB(B1, 0, 1); PG8_SCHED; PG8_LDA(At, 0, 0); PG8_STAGE(PG8_SA(1, 1), a1, voffA[1]);
;             PG8_WAIT_V(8); PG8_WAIT_L(0); PG8_BAR; PG8_MMA(0, 0, At, B0); PG8_MMA(0, 1, At, B1); PG8_BAR; PG8_SCHED;
;             PG8_LDA(At, 0, 1); PG8_STAGE(PG8_SB(0, 0), b2, voffB[0]); PG8_STAGE(PG8_SB(0, 1), b2, voffB[1]); PG8_STAGE(PG8_SA(0, 0), a2, vA2[0]);
;             PG8_WAIT_V(8); PG8_WAIT_L(0); PG8_BAR; PG8_MMA(1, 0, At, B0); PG8_MMA(1, 1, At, B1); PG8_BAR; PG8_SCHED;
;             PG8_LDB(B0, 1, 0); PG8_LDB(B1, 1, 1); PG8_SCHED; PG8_LDA(At, 1, 0); PG8_STAGE(PG8_SA(0, 1), a2, vA2[1]);
;             PG8_WAIT_V(8); PG8_WAIT_L(0); PG8_BAR; PG8_MMA(0, 0, At, B0); PG8_MMA(0, 1, At, B1); PG8_BAR; PG8_SCHED;
;             PG8_LDA(At, 1, 1); PG8_STAGE(PG8_SB(1, 0), b3, voffB[0]); PG8_STAGE(PG8_SB(1, 1), b3, voffB[1]); PG8_STAGE(PG8_SA(1, 0), a3, vA2[0]);
;             PG8_WAIT_V(8); PG8_WAIT_L(0); PG8_BAR; PG8_MMA(1, 0, At, B0); PG8_MMA(1, 1, At, B1); PG8_BAR; PG8_SCHED;
	s_setprio 2
	v_mfma_f32_16x16x128_f8f6f4 v[158:161], v[18:25], v[194:201], v[158:161]
	v_mfma_f32_16x16x128_f8f6f4 v[154:157], v[26:33], v[194:201], v[154:157]
	v_mfma_f32_16x16x128_f8f6f4 v[142:145], v[18:25], v[202:209], v[142:145]
	v_mfma_f32_16x16x128_f8f6f4 v[138:141], v[26:33], v[202:209], v[138:141]
	v_mfma_f32_16x16x128_f8f6f4 v[126:129], v[18:25], v[210:217], v[126:129]
	v_mfma_f32_16x16x128_f8f6f4 v[122:125], v[26:33], v[210:217], v[122:125]
	v_mfma_f32_16x16x128_f8f6f4 v[110:113], v[18:25], v[218:225], v[110:113]
	v_mfma_f32_16x16x128_f8f6f4 v[106:109], v[26:33], v[218:225], v[106:109]
	s_nop 3
	s_setprio 0
	s_setprio 2
	v_mfma_f32_16x16x128_f8f6f4 v[150:153], v[2:9], v[194:201], v[150:153]
	v_mfma_f32_16x16x128_f8f6f4 v[146:149], v[10:17], v[194:201], v[146:149]
	v_mfma_f32_16x16x128_f8f6f4 v[134:137], v[2:9], v[202:209], v[134:137]
	v_mfma_f32_16x16x128_f8f6f4 v[130:133], v[10:17], v[202:209], v[130:133]
	v_mfma_f32_16x16x128_f8f6f4 v[118:121], v[2:9], v[210:217], v[118:121]
	v_mfma_f32_16x16x128_f8f6f4 v[114:117], v[10:17], v[210:217], v[114:117]
	v_mfma_f32_16x16x128_f8f6f4 v[102:105], v[2:9], v[218:225], v[102:105]
	v_mfma_f32_16x16x128_f8f6f4 v[98:101], v[10:17], v[218:225], v[98:101]
	s_setprio 0
	s_add_i32 s69, s53, s43
	s_mov_b32 m0, s69
	ds_read_b128 v[194:197], v191 offset:16384
	ds_read_b128 v[198:201], v191 offset:17408
	ds_read_b128 v[202:205], v191 offset:18432
	ds_read_b128 v[206:209], v191 offset:19456
	ds_read_b128 v[210:213], v191 offset:20480
	ds_read_b128 v[214:217], v191 offset:21504
	ds_read_b128 v[218:221], v191 offset:22528
	ds_read_b128 v[222:225], v191 offset:23552
	global_load_lds_dwordx4 v164, s[28:29]
	s_add_i32 m0, s69, 0x2000
	s_add_i32 s69, s58, s43
	global_load_lds_dwordx4 v166, s[28:29]
	s_add_u32 s98, s28, s4
	s_addc_u32 s99, s29, s5
	s_mov_b32 m0, s69
	s_nop 0
	global_load_lds_dwordx4 v164, s[98:99]
	s_add_u32 s100, s28, s4
	s_addc_u32 s101, s29, s5
	s_add_i32 m0, s69, 0x2000
	s_nop 0
	global_load_lds_dwordx4 v166, s[100:101]
	s_mov_b32 m0, s44
	s_nop 0
	global_load_lds_dwordx4 v168, s[30:31]
	s_mov_b32 m0, s45
	s_nop 0
	global_load_lds_dwordx4 v170, s[30:31]
	s_waitcnt vmcnt(8)
	s_waitcnt lgkmcnt(0)
	s_barrier
	s_setprio 2
	v_mfma_f32_16x16x128_f8f6f4 v[94:97], v[18:25], v[194:201], v[94:97]
	v_mfma_f32_16x16x128_f8f6f4 v[90:93], v[26:33], v[194:201], v[90:93]
	v_mfma_f32_16x16x128_f8f6f4 v[78:81], v[18:25], v[202:209], v[78:81]
	v_mfma_f32_16x16x128_f8f6f4 v[74:77], v[26:33], v[202:209], v[74:77]
	v_mfma_f32_16x16x128_f8f6f4 v[62:65], v[18:25], v[210:217], v[62:65]
	v_mfma_f32_16x16x128_f8f6f4 v[58:61], v[26:33], v[210:217], v[58:61]
	v_mfma_f32_16x16x128_f8f6f4 v[46:49], v[18:25], v[218:225], v[46:49]
	v_mfma_f32_16x16x128_f8f6f4 v[42:45], v[26:33], v[218:225], v[42:45]
	s_nop 3
	s_setprio 0
	s_setprio 2
	v_mfma_f32_16x16x128_f8f6f4 v[86:89], v[2:9], v[194:201], v[86:89]
	v_mfma_f32_16x16x128_f8f6f4 v[82:85], v[10:17], v[194:201], v[82:85]
	v_mfma_f32_16x16x128_f8f6f4 v[70:73], v[2:9], v[202:209], v[70:73]
	v_mfma_f32_16x16x128_f8f6f4 v[66:69], v[10:17], v[202:209], v[66:69]
	v_mfma_f32_16x16x128_f8f6f4 v[54:57], v[2:9], v[210:217], v[54:57]
	v_mfma_f32_16x16x128_f8f6f4 v[50:53], v[10:17], v[210:217], v[50:53]
	v_mfma_f32_16x16x128_f8f6f4 v[38:41], v[2:9], v[218:225], v[38:41]
	v_mfma_f32_16x16x128_f8f6f4 v[34:37], v[10:17], v[218:225], v[34:37]
	s_setprio 0
	s_add_i32 s69, 0, 0x18000
	s_add_i32 s70, 0, 0x1c000
	v_add_u32_e32 v14, s69, v187
	v_add_u32_e32 v30, s70, v187
	ds_read_b128 v[2:5], v14
	ds_read_b128 v[6:9], v14 offset:1024
	ds_read_b128 v[10:13], v14 offset:2048
	ds_read_b128 v[14:17], v14 offset:3072
	ds_read_b128 v[18:21], v30
	ds_read_b128 v[22:25], v30 offset:1024
	ds_read_b128 v[26:29], v30 offset:2048
	ds_read_b128 v[30:33], v30 offset:3072
	s_mov_b32 m0, s46
	ds_read_b128 v[194:197], v191 offset:32768
	ds_read_b128 v[198:201], v191 offset:33792
	ds_read_b128 v[202:205], v191 offset:34816
	ds_read_b128 v[206:209], v191 offset:35840
	ds_read_b128 v[210:213], v191 offset:36864
	ds_read_b128 v[214:217], v191 offset:37888
	ds_read_b128 v[218:221], v191 offset:38912
	ds_read_b128 v[222:225], v191 offset:39936
	global_load_lds_dwordx4 v172, s[30:31]
	s_mov_b32 m0, s47
	s_nop 0
	global_load_lds_dwordx4 v174, s[30:31]
	s_waitcnt vmcnt(8)
	s_waitcnt lgkmcnt(0)
	s_barrier
; #define PG8_STAGE(bufoff, gbase, voff) do { _Pragma("unroll") for (int _i = 0; _i < 2; ++_i) \
;         __builtin_amdgcn_global_load_lds((const unsigned*)((const char*)(gbase) + (voff)[_i]), (PG8_LAS unsigned*)(lds + (bufoff) + ldsw + _i * 8192), 16, 0, 0); } while (0)
; #define PG8_WAIT_V(n) asm volatile("s_waitcnt vmcnt(" #n ")" ::: "memory")
; #define PG8_WAIT_L(n) asm volatile("s_waitcnt lgkmcnt(" #n ")" ::: "memory")
; #define PG8_BAR __builtin_amdgcn_s_barrier()
; #define PG8_SCHED __builtin_amdgcn_sched_barrier(0)
; template <class Epi, class Sched, bool ALIGN_EPI = true, bool F8 = false>
; __device__ __forceinline__ void gemm_phase(PG8_LAS unsigned char* lds, const Sched& S, const Epi& E) {
;     ...
;             const char* a1 = cA + (size_t)(t + 1) * kstep;
;             const char* a2 = last ? nA : cA + (size_t)(t + 2) * kstep; const char* b2 = last ? nB : cB + (size_t)(t + 2) * kstepB;
;             const char* a3 = a2 + kstep; const char* b3 = b2 + kstepB;
;             unsigned vA2[2][2];
; #pragma unroll
;             for (int h = 0; h < 2; ++h)
; #pragma unroll
;                 for (int i = 0; i < 2; ++i) { if constexpr (Sched::GATHER) vA2[h][i] = (last && has_next) ? voffAn[h][i] : voffA[h][i]; else vA2[h][i] = voffA[h][i]; }
;             PG8_LDB(B0, 0, 0); PG8_LDB(B1, 0, 1); PG8_SCHED; PG8_LDA(At, 0, 0); PG8_STAGE(PG8_SA(1, 1), a1, voffA[1]);
;             PG8_WAIT_V(8); PG8_WAIT_L(0); PG8_BAR; PG8_MMA(0, 0, At, B0); PG8_MMA(0, 1, At, B1); PG8_BAR; PG8_SCHED;
;             PG8_LDA(At, 0, 1); PG8_STAGE(PG8_SB(0, 0), b2, voffB[0]); PG8_STAGE(PG8_SB(0, 1), b2, voffB[1]); PG8_STAGE(PG8_SA(0, 0), a2, vA2[0]);
;             PG8_WAIT_V(8); PG8_WAIT_L(0); PG8_BAR; PG8_MMA(1, 0, At, B0); PG8_MMA(1, 1, At, B1); PG8_BAR; PG8_SCHED;
;             PG8_LDB(B0, 1, 0); PG8_LDB(B1, 1, 1); PG8_SCHED; PG8_LDA(At, 1, 0); PG8_STAGE(PG8_SA(0, 1), a2, vA2[1]);
;             PG8_WAIT_V(8); PG8_WAIT_L(0); PG8_BAR; PG8_MMA(0, 0, At, B0); PG8_MMA(0, 1, At, B1); PG8_BAR; PG8_SCHED;
;             PG8_LDA(At, 1, 1); PG8_STAGE(PG8_SB(1, 0), b3, voffB[0]); PG8_STAGE(PG8_SB(1, 1), b3, voffB[1]); PG8_STAGE(PG8_SA(1, 0), a3, vA2[0]);
;             PG8_WAIT_V(8); PG8_WAIT_L(0); PG8_BAR; PG8_MMA(1, 0, At, B0); PG8_MMA(1, 1, At, B1); PG8_BAR; PG8_SCHED;
	s_setprio 2
	v_mfma_f32_16x16x128_f8f6f4 v[158:161], v[2:9], v[194:201], v[158:161]
	v_mfma_f32_16x16x128_f8f6f4 v[154:157], v[10:17], v[194:201], v[154:157]
	v_mfma_f32_16x16x128_f8f6f4 v[142:145], v[2:9], v[202:209], v[142:145]
	v_mfma_f32_16x16x128_f8f6f4 v[138:141], v[10:17], v[202:209], v[138:141]
	v_mfma_f32_16x16x128_f8f6f4 v[126:129], v[2:9], v[210:217], v[126:129]
	v_mfma_f32_16x16x128_f8f6f4 v[122:125], v[10:17], v[210:217], v[122:125]
	v_mfma_f32_16x16x128_f8f6f4 v[110:113], v[2:9], v[218:225], v[110:113]
	v_mfma_f32_16x16x128_f8f6f4 v[106:109], v[10:17], v[218:225], v[106:109]
	s_nop 3
	s_setprio 0
	s_setprio 2
	v_mfma_f32_16x16x128_f8f6f4 v[150:153], v[18:25], v[194:201], v[150:153]
	v_mfma_f32_16x16x128_f8f6f4 v[146:149], v[26:33], v[194:201], v[146:149]
	v_mfma_f32_16x16x128_f8f6f4 v[134:137], v[18:25], v[202:209], v[134:137]
	v_mfma_f32_16x16x128_f8f6f4 v[130:133], v[26:33], v[202:209], v[130:133]
	v_mfma_f32_16x16x128_f8f6f4 v[118:121], v[18:25], v[210:217], v[118:121]
	v_mfma_f32_16x16x128_f8f6f4 v[114:117], v[26:33], v[210:217], v[114:117]
	v_mfma_f32_16x16x128_f8f6f4 v[102:105], v[18:25], v[218:225], v[102:105]
	v_mfma_f32_16x16x128_f8f6f4 v[98:101], v[26:33], v[218:225], v[98:101]
	s_setprio 0
	s_add_u32 s28, s28, 0x8000
	s_addc_u32 s29, s29, 0
	s_add_i32 s30, s69, s43
	s_mov_b32 m0, s30
	ds_read_b128 v[194:197], v191 offset:49152
	ds_read_b128 v[198:201], v191 offset:50176
	ds_read_b128 v[202:205], v191 offset:51200
	ds_read_b128 v[206:209], v191 offset:52224
	ds_read_b128 v[210:213], v191 offset:53248
	ds_read_b128 v[214:217], v191 offset:54272
	ds_read_b128 v[218:221], v191 offset:55296
	ds_read_b128 v[222:225], v191 offset:56320
	global_load_lds_dwordx4 v164, s[28:29]
	s_add_i32 m0, s30, 0x2000
	s_add_i32 s30, s70, s43
	global_load_lds_dwordx4 v166, s[28:29]
	s_mov_b32 m0, s30
	s_nop 0
	global_load_lds_dwordx4 v178, s[28:29]
	s_add_i32 m0, s30, 0x2000
	s_nop 0
	global_load_lds_dwordx4 v180, s[28:29]
	s_mov_b32 m0, s51
	s_nop 0
	global_load_lds_dwordx4 v168, s[26:27]
	s_mov_b32 m0, s52
	s_nop 0
	global_load_lds_dwordx4 v170, s[26:27]
	s_waitcnt vmcnt(8)
	s_waitcnt lgkmcnt(0)
	s_barrier
	s_setprio 2
	v_mfma_f32_16x16x128_f8f6f4 v[94:97], v[2:9], v[194:201], v[94:97]
	v_mfma_f32_16x16x128_f8f6f4 v[90:93], v[10:17], v[194:201], v[90:93]
	v_mfma_f32_16x16x128_f8f6f4 v[78:81], v[2:9], v[202:209], v[78:81]
	v_mfma_f32_16x16x128_f8f6f4 v[74:77], v[10:17], v[202:209], v[74:77]
	v_mfma_f32_16x16x128_f8f6f4 v[62:65], v[2:9], v[210:217], v[62:65]
	v_mfma_f32_16x16x128_f8f6f4 v[58:61], v[10:17], v[210:217], v[58:61]
	v_mfma_f32_16x16x128_f8f6f4 v[46:49], v[2:9], v[218:225], v[46:49]
	v_mfma_f32_16x16x128_f8f6f4 v[42:45], v[10:17], v[218:225], v[42:45]
	s_nop 3
	s_setprio 0
	s_setprio 2
	v_mfma_f32_16x16x128_f8f6f4 v[86:89], v[18:25], v[194:201], v[86:89]
	v_mfma_f32_16x16x128_f8f6f4 v[82:85], v[26:33], v[194:201], v[82:85]
	v_mfma_f32_16x16x128_f8f6f4 v[70:73], v[18:25], v[202:209], v[70:73]
	v_mfma_f32_16x16x128_f8f6f4 v[66:69], v[26:33], v[202:209], v[66:69]
	v_mfma_f32_16x16x128_f8f6f4 v[54:57], v[18:25], v[210:217], v[54:57]
	v_mfma_f32_16x16x128_f8f6f4 v[50:53], v[26:33], v[210:217], v[50:53]
	v_mfma_f32_16x16x128_f8f6f4 v[38:41], v[18:25], v[218:225], v[38:41]
	v_mfma_f32_16x16x128_f8f6f4 v[34:37], v[26:33], v[218:225], v[34:37]
	s_setprio 0
	s_add_i32 s68, s68, 2
	s_add_u32 s23, s23, 0x10000
	s_addc_u32 s67, s67, 0
	s_add_u32 s24, s24, 0x10000
	s_addc_u32 s25, s25, 0
	s_cmp_gt_u32 s68, 5
	s_cbranch_scc0 .Lh1_1138
